# instruction selection in the fp8 epilogues: E1 SwiGLU scale/bias steps as v_pk_mul_f32 / v_pk_fma_f32 (bit-identical), dead zero-inits in front of v_cvt_pk_fp8_f32 pairs removed
# baseline (speedup 1.0000x reference)
.LBB0_131:
	s_waitcnt vmcnt(4)
	v_cvt_pk_f32_fp8_e32 v[24:25], v54
	v_cvt_pk_f32_fp8_sdwa v[108:109], v54 src0_sel:WORD_1
	s_waitcnt vmcnt(3)
	v_cvt_pk_f32_fp8_e32 v[110:111], v58
	v_cvt_pk_f32_fp8_sdwa v[112:113], v58 src0_sel:WORD_1
	v_lshlrev_b32_e32 v16, 16, v14
	v_and_b32_e32 v17, 0xffff0000, v14
	v_lshlrev_b32_e32 v14, 16, v15
	v_and_b32_e32 v15, 0xffff0000, v15
	v_pk_add_f32 v[24:25], v[24:25], v[110:111]
	v_pk_add_f32 v[108:109], v[108:109], v[112:113]
	s_ashr_i32 s83, s82, 31
	v_pk_fma_f32 v[106:107], v[106:107], v[108:109], v[14:15]
	v_pk_fma_f32 v[14:15], v[104:105], v[24:25], v[16:17]
	v_cvt_pk_f32_fp8_e32 v[16:17], v55
	v_cvt_pk_f32_fp8_sdwa v[24:25], v55 src0_sel:WORD_1
	v_cvt_pk_f32_fp8_e32 v[54:55], v59
	v_cvt_pk_f32_fp8_sdwa v[58:59], v59 src0_sel:WORD_1
	v_lshlrev_b32_e32 v104, 16, v18
	v_and_b32_e32 v105, 0xffff0000, v18
	v_pk_add_f32 v[16:17], v[16:17], v[54:55]
	v_pk_add_f32 v[24:25], v[24:25], v[58:59]
	v_lshlrev_b32_e32 v18, 16, v19
	v_and_b32_e32 v19, 0xffff0000, v19
	v_pk_fma_f32 v[18:19], v[102:103], v[24:25], v[18:19]
	v_pk_fma_f32 v[16:17], v[100:101], v[16:17], v[104:105]
	v_cvt_pk_f32_fp8_e32 v[24:25], v56
	v_cvt_pk_f32_fp8_sdwa v[100:101], v56 src0_sel:WORD_1
	v_cvt_pk_f32_fp8_e32 v[102:103], v60
	v_cvt_pk_f32_fp8_sdwa v[104:105], v60 src0_sel:WORD_1
	v_cvt_pk_bf16_f32 v14, v14, v15
	v_cvt_pk_bf16_f32 v15, v106, v107
	v_cvt_pk_bf16_f32 v16, v16, v17
	v_cvt_pk_bf16_f32 v17, v18, v19
	v_pk_add_f32 v[18:19], v[24:25], v[102:103]
	v_and_b32_e32 v59, 0xffff0000, v15
	v_pk_add_f32 v[24:25], v[100:101], v[104:105]
	v_lshlrev_b32_e32 v106, 16, v22
	v_and_b32_e32 v107, 0xffff0000, v22
	v_lshlrev_b32_e32 v22, 16, v23
	v_and_b32_e32 v23, 0xffff0000, v23
	v_lshlrev_b32_e32 v58, 16, v15
	v_mul_f32_e32 v56, v59, v59
	v_pk_fma_f32 v[24:25], v[98:99], v[24:25], v[22:23]
	v_pk_fma_f32 v[100:101], v[58:59], v[58:59], v[56:57] op_sel_hi:[1,1,0]
	v_pk_fma_f32 v[18:19], v[96:97], v[18:19], v[106:107]
	v_cvt_pk_f32_fp8_e32 v[96:97], v61
	v_cvt_pk_bf16_f32 v22, v18, v19
	v_cvt_pk_bf16_f32 v23, v24, v25
	v_cvt_pk_f32_fp8_e32 v[24:25], v57
	v_cvt_pk_f32_fp8_sdwa v[56:57], v57 src0_sel:WORD_1
	v_cvt_pk_f32_fp8_sdwa v[60:61], v61 src0_sel:WORD_1
	v_lshlrev_b32_e32 v18, 16, v26
	v_and_b32_e32 v19, 0xffff0000, v26
	v_lshlrev_b32_e32 v26, 16, v27
	v_and_b32_e32 v27, 0xffff0000, v27
	v_pk_add_f32 v[56:57], v[56:57], v[60:61]
	v_and_b32_e32 v55, 0xffff0000, v14
	v_pk_add_f32 v[24:25], v[24:25], v[96:97]
	v_pk_fma_f32 v[26:27], v[94:95], v[56:57], v[26:27]
	v_lshlrev_b32_e32 v54, 16, v14
	v_and_b32_e32 v105, 0xffff0000, v17
	v_and_b32_e32 v104, 0xffff0000, v16
	v_pk_fma_f32 v[18:19], v[92:93], v[24:25], v[18:19]
	v_lshlrev_b32_e32 v102, 16, v16
	v_cvt_pk_bf16_f32 v24, v18, v19
	v_cvt_pk_bf16_f32 v25, v26, v27
	v_mul_f32_e32 v26, v55, v55
	v_lshlrev_b32_e32 v27, 16, v24
	v_lshlrev_b32_e32 v103, 16, v17
	v_pk_mul_f32 v[18:19], v[104:105], v[104:105]
	v_pk_fma_f32 v[96:97], v[54:55], v[54:55], v[26:27] op_sel_hi:[1,1,0]
	v_and_b32_e32 v57, 0xffff0000, v24
	v_pk_fma_f32 v[18:19], v[102:103], v[102:103], v[18:19]
	v_mov_b32_e32 v26, v96
	v_mov_b32_e32 v98, v100
	v_mov_b32_e32 v99, v27
	v_and_b32_e32 v93, 0xffff0000, v22
	v_mul_f32_e32 v1, v57, v57
	v_pk_add_f32 v[96:97], v[96:97], v[100:101]
	v_pk_mul_f32 v[98:99], v[26:27], v[98:99]
	v_pk_add_f32 v[18:19], v[18:19], v[18:19] op_sel:[0,1] op_sel_hi:[1,0]
	v_lshlrev_b32_e32 v92, 16, v22
	v_and_b32_e32 v95, 0xffff0000, v23
	v_mov_b32_e32 v97, v99
	v_mov_b32_e32 v19, v1
	v_mul_f32_e32 v26, v93, v93
	v_lshlrev_b32_e32 v60, 16, v25
	v_and_b32_e32 v61, 0xffff0000, v25
	v_lshlrev_b32_e32 v94, 16, v23
	v_pk_add_f32 v[18:19], v[96:97], v[18:19]
	v_pk_fma_f32 v[96:97], v[92:93], v[92:93], v[26:27] op_sel_hi:[1,1,0]
	v_mul_f32_e32 v26, v95, v95
	v_mul_f32_e32 v56, v60, v60
	v_mul_f32_e32 v67, v61, v61
	v_pk_fma_f32 v[98:99], v[94:95], v[94:95], v[26:27] op_sel_hi:[1,1,0]
	v_mov_b32_e32 v97, v56
	v_mov_b32_e32 v99, v67
	v_pk_add_f32 v[96:97], v[96:97], v[98:99]
	v_mov_b32_e32 v56, v27
	v_pk_add_f32 v[18:19], v[18:19], v[96:97]
	s_lshl_b64 s[48:49], s[82:83], 10
	v_add_f32_e32 v1, v18, v19
	s_lshl_b64 s[50:51], s[82:83], 11
	s_waitcnt lgkmcnt(0)
	s_nop 1
	v_add_f32_dpp v1, v1, v1 quad_perm:[1,0,3,2] row_mask:0xf bank_mask:0xf
	s_waitcnt lgkmcnt(0)
	s_nop 1
	v_add_f32_dpp v1, v1, v1 quad_perm:[2,3,0,1] row_mask:0xf bank_mask:0xf
	s_waitcnt lgkmcnt(0)
	s_nop 1
	v_add_f32_dpp v1, v1, v1 row_half_mirror row_mask:0xf bank_mask:0xf
	s_waitcnt lgkmcnt(0)
	s_nop 1
	v_add_f32_dpp v1, v1, v1 row_mirror row_mask:0xf bank_mask:0xf
	s_waitcnt lgkmcnt(0)
	s_nop 1
	v_add_f32_dpp v1, v1, v1 row_bcast:15 row_mask:0xa bank_mask:0xf
	s_waitcnt lgkmcnt(0)
	s_nop 1
	v_add_f32_dpp v1, v1, v1 row_bcast:31 row_mask:0xc bank_mask:0xf
	s_nop 0
	v_readlane_b32 s101, v1, 63
	s_nop 1
	v_mov_b32_e32 v1, s101
	v_fmamk_f32 v1, v1, 0x3a800000, v210
	v_rsq_f32_e32 v26, v1
	s_nop 0
	v_pk_mul_f32 v[18:19], v[26:27], v[54:55] op_sel_hi:[0,1]
	v_pk_fma_f32 v[28:29], v[18:19], v[28:29], v[62:63]
	v_cvt_pk_fp8_f32 v18, v28, v29
	v_pk_mul_f32 v[54:55], v[26:27], v[58:59] op_sel_hi:[0,1]
	v_pk_fma_f32 v[20:21], v[54:55], v[20:21], v[64:65]
	v_cvt_pk_fp8_f32 v18, v20, v21 op_sel:[0,0,1]
	v_mov_b32_e32 v20, v102
	v_mov_b32_e32 v21, v104
	v_pk_mul_f32 v[20:21], v[26:27], v[20:21] op_sel_hi:[0,1]
	v_pk_fma_f32 v[10:11], v[20:21], v[90:91], v[10:11]
	v_mov_b32_e32 v104, v103
	v_cvt_pk_fp8_f32 v19, v10, v11
	v_pk_mul_f32 v[10:11], v[26:27], v[104:105] op_sel_hi:[0,1]
	v_pk_fma_f32 v[10:11], v[10:11], v[88:89], v[12:13]
	v_cvt_pk_fp8_f32 v19, v10, v11 op_sel:[0,0,1]
	v_pk_mul_f32 v[10:11], v[26:27], v[92:93] op_sel_hi:[0,1]
	v_pk_fma_f32 v[6:7], v[10:11], v[86:87], v[6:7]
	v_cvt_pk_fp8_f32 v20, v6, v7
	v_pk_mul_f32 v[6:7], v[26:27], v[56:57] op_sel_hi:[0,1]
	v_pk_fma_f32 v[2:3], v[6:7], v[82:83], v[2:3]
	v_pk_mul_f32 v[12:13], v[26:27], v[94:95] op_sel_hi:[0,1]
	v_cvt_pk_fp8_f32 v21, v2, v3
	v_pk_mul_f32 v[2:3], v[26:27], v[60:61] op_sel_hi:[0,1]
	v_pk_fma_f32 v[8:9], v[12:13], v[84:85], v[8:9]
	v_pk_fma_f32 v[2:3], v[2:3], v[80:81], v[4:5]
	v_cvt_pk_fp8_f32 v20, v8, v9 op_sel:[0,0,1]
	v_cvt_pk_fp8_f32 v21, v2, v3 op_sel:[0,0,1]
	v_lshl_add_u64 v[28:29], v[76:77], 0, s[50:51]
	v_lshl_add_u64 v[2:3], v[70:71], 0, s[48:49]
	global_store_dwordx4 v[28:29], v[14:17], off
	global_store_dwordx4 v[28:29], v[22:25], off offset:16
	global_store_dwordx4 v[2:3], v[18:21], off
	v_mov_b64_e32 v[14:15], v[30:31]
	v_mov_b64_e32 v[22:23], v[38:39]
	v_mov_b64_e32 v[18:19], v[34:35]
	v_mov_b64_e32 v[26:27], v[42:43]
	s_waitcnt vmcnt(4)
	v_mov_b32_e32 v54, v50
	v_mov_b32_e32 v55, v51
	v_mov_b32_e32 v56, v52
	v_mov_b32_e32 v57, v53
	s_waitcnt vmcnt(3)
	v_mov_b32_e32 v58, v46
	v_mov_b32_e32 v59, v47
	v_mov_b32_e32 v60, v48
	v_mov_b32_e32 v61, v49
	v_mov_b64_e32 v[16:17], v[32:33]
	v_mov_b64_e32 v[20:21], v[36:37]
	v_mov_b64_e32 v[24:25], v[40:41]
	v_mov_b64_e32 v[28:29], v[44:45]
	s_cmp_lt_i32 s86, s26
	s_mov_b32 s82, s86
	s_cbranch_scc0 .LBB0_142

.LBB0_134:
	s_waitcnt vmcnt(6)
	v_lshlrev_b32_e32 v16, 16, v30
	v_and_b32_e32 v17, 0xffff0000, v30
	v_lshlrev_b32_e32 v24, 16, v31
	v_and_b32_e32 v25, 0xffff0000, v31
	s_waitcnt vmcnt(4)
	v_cvt_pk_f32_fp8_e32 v[30:31], v50
	v_cvt_pk_f32_fp8_sdwa v[34:35], v50 src0_sel:WORD_1
	s_waitcnt vmcnt(3)
	v_cvt_pk_f32_fp8_e32 v[42:43], v46
	v_cvt_pk_f32_fp8_sdwa v[124:125], v46 src0_sel:WORD_1
	s_add_i32 s84, s84, 4
	s_add_i32 s86, s82, 1
	v_pk_add_f32 v[30:31], v[30:31], v[42:43]
	v_pk_add_f32 v[34:35], v[34:35], v[124:125]
	v_pk_fma_f32 v[16:17], v[104:105], v[30:31], v[16:17]
	v_pk_fma_f32 v[24:25], v[106:107], v[34:35], v[24:25]
	v_cvt_pk_bf16_f32 v124, v16, v17
	v_cvt_pk_f32_fp8_e32 v[16:17], v51
	v_cvt_pk_bf16_f32 v125, v24, v25
	v_cvt_pk_f32_fp8_sdwa v[24:25], v51 src0_sel:WORD_1
	v_cvt_pk_f32_fp8_e32 v[30:31], v47
	v_cvt_pk_f32_fp8_sdwa v[34:35], v47 src0_sel:WORD_1
	v_lshlrev_b32_e32 v42, 16, v38
	v_and_b32_e32 v43, 0xffff0000, v38
	v_pk_add_f32 v[16:17], v[16:17], v[30:31]
	v_pk_add_f32 v[24:25], v[24:25], v[34:35]
	v_lshlrev_b32_e32 v34, 16, v32
	v_and_b32_e32 v35, 0xffff0000, v32
	v_lshlrev_b32_e32 v32, 16, v33
	v_and_b32_e32 v33, 0xffff0000, v33
	v_pk_fma_f32 v[24:25], v[102:103], v[24:25], v[32:33]
	v_pk_fma_f32 v[16:17], v[100:101], v[16:17], v[34:35]
	v_cvt_pk_f32_fp8_e32 v[32:33], v48
	v_cvt_pk_bf16_f32 v126, v16, v17
	v_cvt_pk_bf16_f32 v127, v24, v25
	v_cvt_pk_f32_fp8_e32 v[16:17], v52
	v_cvt_pk_f32_fp8_sdwa v[24:25], v52 src0_sel:WORD_1
	v_cvt_pk_f32_fp8_sdwa v[34:35], v48 src0_sel:WORD_1
	v_lshlrev_b32_e32 v38, 16, v39
	v_pk_add_f32 v[32:33], v[16:17], v[32:33]
	v_and_b32_e32 v39, 0xffff0000, v39
	v_pk_add_f32 v[24:25], v[24:25], v[34:35]
	v_pk_fma_f32 v[32:33], v[96:97], v[32:33], v[42:43]
	v_pk_fma_f32 v[24:25], v[98:99], v[24:25], v[38:39]
	v_cvt_pk_bf16_f32 v128, v32, v33
	v_cvt_pk_f32_fp8_sdwa v[32:33], v53 src0_sel:WORD_1
	v_cvt_pk_bf16_f32 v129, v24, v25
	v_cvt_pk_f32_fp8_e32 v[24:25], v53
	v_cvt_pk_f32_fp8_e32 v[38:39], v49
	v_cvt_pk_f32_fp8_sdwa v[42:43], v49 src0_sel:WORD_1
	v_and_b32_e32 v31, 0xffff0000, v124
	v_and_b32_e32 v133, 0xffff0000, v125
	v_pk_add_f32 v[24:25], v[24:25], v[38:39]
	v_pk_add_f32 v[32:33], v[32:33], v[42:43]
	v_lshlrev_b32_e32 v42, 16, v40
	v_and_b32_e32 v43, 0xffff0000, v40
	v_pk_fma_f32 v[24:25], v[92:93], v[24:25], v[42:43]
	v_lshlrev_b32_e32 v30, 16, v124
	v_lshlrev_b32_e32 v132, 16, v125
	v_mul_f32_e32 v16, v133, v133
	v_lshlrev_b32_e32 v40, 16, v41
	v_and_b32_e32 v41, 0xffff0000, v41
	v_cvt_pk_bf16_f32 v130, v24, v25
	v_mul_f32_e32 v24, v31, v31
	v_lshlrev_b32_e32 v25, 16, v130
	v_pk_fma_f32 v[134:135], v[132:133], v[132:133], v[16:17] op_sel_hi:[1,1,0]
	v_and_b32_e32 v17, 0xffff0000, v127
	v_and_b32_e32 v16, 0xffff0000, v126
	v_pk_fma_f32 v[32:33], v[94:95], v[32:33], v[40:41]
	v_pk_fma_f32 v[40:41], v[30:31], v[30:31], v[24:25] op_sel_hi:[1,1,0]
	v_lshlrev_b32_e32 v34, 16, v126
	v_lshlrev_b32_e32 v35, 16, v127
	v_pk_mul_f32 v[38:39], v[16:17], v[16:17]
	v_cvt_pk_bf16_f32 v131, v32, v33
	global_store_dwordx4 v[112:113], v[124:127], off
	global_store_dwordx4 v[114:115], v[128:131], off offset:16
	v_mov_b32_e32 v24, v40
	v_mov_b32_e32 v112, v134
	v_mov_b32_e32 v113, v25
	v_pk_fma_f32 v[136:137], v[34:35], v[34:35], v[38:39]
	v_and_b32_e32 v43, 0xffff0000, v130
	v_pk_add_f32 v[40:41], v[40:41], v[134:135]
	v_pk_mul_f32 v[112:113], v[24:25], v[112:113]
	v_and_b32_e32 v39, 0xffff0000, v128
	v_mul_f32_e32 v1, v43, v43
	v_mov_b32_e32 v41, v113
	v_pk_add_f32 v[112:113], v[136:137], v[136:137] op_sel:[0,1] op_sel_hi:[1,0]
	v_lshlrev_b32_e32 v38, 16, v128
	v_and_b32_e32 v139, 0xffff0000, v129
	v_mov_b32_e32 v113, v1
	v_mul_f32_e32 v24, v39, v39
	v_lshlrev_b32_e32 v138, 16, v129
	v_lshlrev_b32_e32 v32, 16, v131
	v_and_b32_e32 v33, 0xffff0000, v131
	v_pk_add_f32 v[40:41], v[40:41], v[112:113]
	v_pk_fma_f32 v[112:113], v[38:39], v[38:39], v[24:25] op_sel_hi:[1,1,0]
	v_mul_f32_e32 v24, v139, v139
	v_mul_f32_e32 v42, v32, v32
	v_mul_f32_e32 v67, v33, v33
	v_pk_fma_f32 v[114:115], v[138:139], v[138:139], v[24:25] op_sel_hi:[1,1,0]
	v_mov_b32_e32 v113, v42
	v_mov_b32_e32 v115, v67
	v_pk_add_f32 v[112:113], v[112:113], v[114:115]
	v_mov_b32_e32 v42, v25
	v_pk_add_f32 v[40:41], v[40:41], v[112:113]
	v_lshl_add_u64 v[44:45], v[44:45], 0, s[28:29]
	v_add_f32_e32 v1, v40, v41
	v_lshl_add_u64 v[108:109], v[108:109], 0, s[34:35]
	v_lshl_add_u64 v[110:111], v[110:111], 0, s[28:29]
	s_cmp_lt_i32 s86, s17
	s_waitcnt lgkmcnt(0)
	s_nop 1
	v_add_f32_dpp v1, v1, v1 quad_perm:[1,0,3,2] row_mask:0xf bank_mask:0xf
	s_waitcnt lgkmcnt(0)
	s_nop 1
	v_add_f32_dpp v1, v1, v1 quad_perm:[2,3,0,1] row_mask:0xf bank_mask:0xf
	s_waitcnt lgkmcnt(0)
	s_nop 1
	v_add_f32_dpp v1, v1, v1 row_half_mirror row_mask:0xf bank_mask:0xf
	s_waitcnt lgkmcnt(0)
	s_nop 1
	v_add_f32_dpp v1, v1, v1 row_mirror row_mask:0xf bank_mask:0xf
	s_waitcnt lgkmcnt(0)
	s_nop 1
	v_add_f32_dpp v1, v1, v1 row_bcast:15 row_mask:0xa bank_mask:0xf
	s_waitcnt lgkmcnt(0)
	s_nop 1
	v_add_f32_dpp v1, v1, v1 row_bcast:31 row_mask:0xc bank_mask:0xf
	s_nop 0
	v_readlane_b32 s101, v1, 63
	s_nop 1
	v_mov_b32_e32 v1, s101
	v_fmamk_f32 v1, v1, 0x3a800000, v210
	v_rsq_f32_e32 v24, v1
	s_nop 0
	v_pk_mul_f32 v[40:41], v[24:25], v[30:31] op_sel_hi:[0,1]
	v_pk_mul_f32 v[112:113], v[24:25], v[132:133] op_sel_hi:[0,1]
	v_pk_fma_f32 v[114:115], v[112:113], v[20:21], v[64:65]
	v_pk_fma_f32 v[40:41], v[40:41], v[28:29], v[62:63]
	v_cvt_pk_fp8_f32 v112, v40, v41
	v_mov_b32_e32 v40, v34
	v_mov_b32_e32 v41, v16
	v_pk_mul_f32 v[40:41], v[24:25], v[40:41] op_sel_hi:[0,1]
	v_pk_fma_f32 v[40:41], v[40:41], v[90:91], v[10:11]
	v_cvt_pk_fp8_f32 v113, v40, v41
	v_cvt_pk_fp8_f32 v112, v114, v115 op_sel:[0,0,1]
	v_mov_b32_e32 v114, v35
	v_mov_b32_e32 v115, v17
	v_pk_mul_f32 v[114:115], v[24:25], v[114:115] op_sel_hi:[0,1]
	v_pk_fma_f32 v[114:115], v[114:115], v[88:89], v[12:13]
	v_pk_mul_f32 v[40:41], v[24:25], v[38:39] op_sel_hi:[0,1]
	v_cvt_pk_fp8_f32 v113, v114, v115 op_sel:[0,0,1]
	v_pk_mul_f32 v[114:115], v[24:25], v[138:139] op_sel_hi:[0,1]
	v_pk_fma_f32 v[124:125], v[114:115], v[84:85], v[8:9]
	v_pk_fma_f32 v[40:41], v[40:41], v[86:87], v[6:7]
	v_cvt_pk_fp8_f32 v114, v40, v41
	v_pk_mul_f32 v[40:41], v[24:25], v[42:43] op_sel_hi:[0,1]
	v_pk_fma_f32 v[40:41], v[40:41], v[82:83], v[2:3]
	v_cvt_pk_fp8_f32 v115, v40, v41
	v_pk_mul_f32 v[32:33], v[24:25], v[32:33] op_sel_hi:[0,1]
	v_pk_fma_f32 v[32:33], v[32:33], v[80:81], v[4:5]
	v_cvt_pk_fp8_f32 v114, v124, v125 op_sel:[0,0,1]
	v_cvt_pk_fp8_f32 v115, v32, v33 op_sel:[0,0,1]
	v_lshl_add_u64 v[32:33], s[80:81], 0, v[36:37]
	v_lshl_add_u64 v[36:37], v[36:37], 0, s[34:35]
	global_store_dwordx4 v[32:33], v[112:115], off
	s_cbranch_scc0 .LBB0_137
.LBB0_135:
	s_waitcnt vmcnt(4)
	v_cvt_pk_f32_fp8_e32 v[24:25], v54
	v_cvt_pk_f32_fp8_sdwa v[34:35], v54 src0_sel:WORD_1
	s_waitcnt vmcnt(3)
	v_cvt_pk_f32_fp8_e32 v[42:43], v58
	v_cvt_pk_f32_fp8_sdwa v[124:125], v58 src0_sel:WORD_1
	v_lshl_add_u64 v[16:17], s[80:81], 0, v[44:45]
	s_mov_b64 s[48:49], 0x18200000
	s_ashr_i32 s85, s84, 31
	v_lshl_add_u64 v[112:113], v[16:17], 0, s[48:49]
	v_add_co_u32_e32 v114, vcc, s79, v16
	s_lshl_b64 s[48:49], s[84:85], 10
	s_nop 0
	v_addc_co_u32_e32 v115, vcc, 0, v17, vcc
	v_lshl_add_u64 v[16:17], v[78:79], 0, s[48:49]
	global_load_dwordx4 v[30:33], v[114:115], off
	global_load_dwordx4 v[38:41], v[112:113], off offset:16
	global_load_dwordx4 v[50:53], v[16:17], off
	global_load_dwordx4 v[46:49], v[16:17], off offset:1024
	v_lshlrev_b32_e32 v16, 16, v14
	v_and_b32_e32 v17, 0xffff0000, v14
	v_lshlrev_b32_e32 v14, 16, v15
	v_and_b32_e32 v15, 0xffff0000, v15
	v_pk_add_f32 v[24:25], v[24:25], v[42:43]
	v_pk_add_f32 v[34:35], v[34:35], v[124:125]
	v_pk_fma_f32 v[16:17], v[104:105], v[24:25], v[16:17]
	v_pk_fma_f32 v[14:15], v[106:107], v[34:35], v[14:15]
	v_cvt_pk_f32_fp8_e32 v[24:25], v55
	v_cvt_pk_f32_fp8_sdwa v[34:35], v55 src0_sel:WORD_1
	v_cvt_pk_f32_fp8_e32 v[42:43], v59
	v_cvt_pk_f32_fp8_sdwa v[126:127], v59 src0_sel:WORD_1
	v_cvt_pk_bf16_f32 v124, v16, v17
	v_cvt_pk_f32_fp8_e32 v[128:129], v60
	v_pk_add_f32 v[16:17], v[24:25], v[42:43]
	v_pk_add_f32 v[24:25], v[34:35], v[126:127]
	v_lshlrev_b32_e32 v42, 16, v18
	v_and_b32_e32 v43, 0xffff0000, v18
	v_lshlrev_b32_e32 v18, 16, v19
	v_and_b32_e32 v19, 0xffff0000, v19
	v_pk_fma_f32 v[18:19], v[102:103], v[24:25], v[18:19]
	v_pk_fma_f32 v[16:17], v[100:101], v[16:17], v[42:43]
	v_cvt_pk_f32_fp8_e32 v[24:25], v56
	v_cvt_pk_f32_fp8_sdwa v[42:43], v56 src0_sel:WORD_1
	v_cvt_pk_f32_fp8_sdwa v[130:131], v60 src0_sel:WORD_1
	v_cvt_pk_bf16_f32 v125, v14, v15
	v_cvt_pk_bf16_f32 v126, v16, v17
	v_cvt_pk_bf16_f32 v127, v18, v19
	v_pk_add_f32 v[16:17], v[24:25], v[128:129]
	v_pk_add_f32 v[18:19], v[42:43], v[130:131]
	v_lshlrev_b32_e32 v128, 16, v22
	v_and_b32_e32 v129, 0xffff0000, v22
	v_lshlrev_b32_e32 v22, 16, v23
	v_and_b32_e32 v23, 0xffff0000, v23
	v_cvt_pk_f32_fp8_sdwa v[130:131], v57 src0_sel:WORD_1
	v_cvt_pk_f32_fp8_sdwa v[136:137], v61 src0_sel:WORD_1
	v_pk_fma_f32 v[18:19], v[98:99], v[18:19], v[22:23]
	v_cvt_pk_f32_fp8_e32 v[22:23], v57
	v_cvt_pk_f32_fp8_e32 v[134:135], v61
	v_pk_fma_f32 v[16:17], v[96:97], v[16:17], v[128:129]
	v_and_b32_e32 v15, 0xffff0000, v124
	v_cvt_pk_bf16_f32 v128, v16, v17
	v_cvt_pk_bf16_f32 v129, v18, v19
	v_pk_add_f32 v[18:19], v[130:131], v[136:137]
	v_lshlrev_b32_e32 v130, 16, v26
	v_and_b32_e32 v131, 0xffff0000, v26
	v_lshlrev_b32_e32 v26, 16, v27
	v_and_b32_e32 v27, 0xffff0000, v27
	v_and_b32_e32 v35, 0xffff0000, v125
	v_pk_add_f32 v[16:17], v[22:23], v[134:135]
	v_pk_fma_f32 v[18:19], v[94:95], v[18:19], v[26:27]
	v_lshlrev_b32_e32 v14, 16, v124
	v_lshlrev_b32_e32 v34, 16, v125
	v_mul_f32_e32 v24, v35, v35
	v_pk_fma_f32 v[16:17], v[92:93], v[16:17], v[130:131]
	v_pk_fma_f32 v[24:25], v[34:35], v[34:35], v[24:25] op_sel_hi:[1,1,0]
	v_cvt_pk_bf16_f32 v130, v16, v17
	v_cvt_pk_bf16_f32 v131, v18, v19
	v_mul_f32_e32 v18, v15, v15
	v_and_b32_e32 v133, 0xffff0000, v127
	v_and_b32_e32 v132, 0xffff0000, v126
	v_lshlrev_b32_e32 v26, 16, v130
	v_pk_fma_f32 v[18:19], v[14:15], v[14:15], v[18:19] op_sel_hi:[1,1,0]
	v_lshlrev_b32_e32 v42, 16, v126
	v_lshlrev_b32_e32 v43, 16, v127
	v_pk_mul_f32 v[22:23], v[132:133], v[132:133]
	v_mov_b32_e32 v138, v18
	v_mov_b32_e32 v139, v26
	v_mov_b32_e32 v140, v24
	v_mov_b32_e32 v141, v26
	v_pk_fma_f32 v[134:135], v[42:43], v[42:43], v[22:23]
	v_and_b32_e32 v27, 0xffff0000, v130
	v_pk_add_f32 v[18:19], v[18:19], v[24:25]
	v_pk_mul_f32 v[24:25], v[138:139], v[140:141]
	v_mul_f32_e32 v1, v27, v27
	v_mov_b32_e32 v19, v25
	v_pk_add_f32 v[24:25], v[134:135], v[134:135] op_sel:[0,1] op_sel_hi:[1,0]
	v_and_b32_e32 v23, 0xffff0000, v128
	v_and_b32_e32 v137, 0xffff0000, v129
	v_mov_b32_e32 v25, v1
	v_lshlrev_b32_e32 v22, 16, v128
	v_lshlrev_b32_e32 v136, 16, v129
	v_lshlrev_b32_e32 v16, 16, v131
	v_and_b32_e32 v17, 0xffff0000, v131
	v_pk_add_f32 v[18:19], v[18:19], v[24:25]
	v_mul_f32_e32 v24, v23, v23
	v_mul_f32_e32 v134, v137, v137
	v_mul_f32_e32 v67, v16, v16
	v_mul_f32_e32 v75, v17, v17
	v_pk_fma_f32 v[24:25], v[22:23], v[22:23], v[24:25] op_sel_hi:[1,1,0]
	v_pk_fma_f32 v[134:135], v[136:137], v[136:137], v[134:135] op_sel_hi:[1,1,0]
	v_mov_b32_e32 v25, v67
	v_mov_b32_e32 v135, v75
	v_pk_add_f32 v[24:25], v[24:25], v[134:135]
	s_add_i32 s82, s82, 2
	v_pk_add_f32 v[18:19], v[18:19], v[24:25]
	v_lshl_add_u64 v[24:25], s[80:81], 0, v[110:111]
	v_add_f32_e32 v1, v18, v19
	v_add_co_u32_e32 v24, vcc, s79, v24
	v_mov_b32_e32 v19, v132
	s_nop 0
	v_addc_co_u32_e32 v25, vcc, 0, v25, vcc
	s_waitcnt lgkmcnt(0)
	s_nop 1
	v_add_f32_dpp v1, v1, v1 quad_perm:[1,0,3,2] row_mask:0xf bank_mask:0xf
	global_store_dwordx4 v[24:25], v[124:127], off
	global_store_dwordx4 v[24:25], v[128:131], off offset:16
	s_cmp_ge_i32 s82, s26
	s_waitcnt lgkmcnt(0)
	s_nop 1
	v_add_f32_dpp v1, v1, v1 quad_perm:[2,3,0,1] row_mask:0xf bank_mask:0xf
	s_waitcnt lgkmcnt(0)
	s_nop 1
	v_add_f32_dpp v1, v1, v1 row_half_mirror row_mask:0xf bank_mask:0xf
	s_waitcnt lgkmcnt(0)
	s_nop 1
	v_add_f32_dpp v1, v1, v1 row_mirror row_mask:0xf bank_mask:0xf
	s_waitcnt lgkmcnt(0)
	s_nop 1
	v_add_f32_dpp v1, v1, v1 row_bcast:15 row_mask:0xa bank_mask:0xf
	v_mov_b32_e32 v18, v42
	s_waitcnt lgkmcnt(0)
	s_nop 1
	v_add_f32_dpp v1, v1, v1 row_bcast:31 row_mask:0xc bank_mask:0xf
	s_nop 0
	v_readlane_b32 s101, v1, 63
	s_nop 1
	v_mov_b32_e32 v1, s101
	v_fmamk_f32 v1, v1, 0x3a800000, v210
	v_rsq_f32_e32 v134, v1
	s_nop 0
	v_pk_mul_f32 v[124:125], v[134:135], v[14:15] op_sel_hi:[0,1]
	v_pk_fma_f32 v[126:127], v[124:125], v[28:29], v[62:63]
	v_cvt_pk_fp8_f32 v124, v126, v127
	v_pk_mul_f32 v[24:25], v[134:135], v[34:35] op_sel_hi:[0,1]
	v_pk_fma_f32 v[24:25], v[24:25], v[20:21], v[64:65]
	v_cvt_pk_fp8_f32 v124, v24, v25 op_sel:[0,0,1]
	v_mov_b32_e32 v24, v42
	v_mov_b32_e32 v25, v132
	v_pk_mul_f32 v[24:25], v[134:135], v[24:25] op_sel_hi:[0,1]
	v_pk_fma_f32 v[24:25], v[24:25], v[90:91], v[10:11]
	v_mov_b32_e32 v132, v43
	v_cvt_pk_fp8_f32 v125, v24, v25
	v_pk_mul_f32 v[24:25], v[134:135], v[132:133] op_sel_hi:[0,1]
	v_pk_fma_f32 v[24:25], v[24:25], v[88:89], v[12:13]
	v_cvt_pk_fp8_f32 v125, v24, v25 op_sel:[0,0,1]
	v_pk_mul_f32 v[24:25], v[134:135], v[22:23] op_sel_hi:[0,1]
	v_pk_fma_f32 v[24:25], v[24:25], v[86:87], v[6:7]
	v_cvt_pk_fp8_f32 v126, v24, v25
	v_pk_mul_f32 v[24:25], v[134:135], v[26:27] op_sel_hi:[0,1]
	v_pk_fma_f32 v[24:25], v[24:25], v[82:83], v[2:3]
	v_pk_mul_f32 v[34:35], v[134:135], v[136:137] op_sel_hi:[0,1]
	v_cvt_pk_fp8_f32 v127, v24, v25
	v_pk_mul_f32 v[16:17], v[134:135], v[16:17] op_sel_hi:[0,1]
	v_pk_fma_f32 v[34:35], v[34:35], v[84:85], v[8:9]
	v_pk_fma_f32 v[16:17], v[16:17], v[80:81], v[4:5]
	v_cvt_pk_fp8_f32 v126, v34, v35 op_sel:[0,0,1]
	v_cvt_pk_fp8_f32 v127, v16, v17 op_sel:[0,0,1]
	v_lshl_add_u64 v[16:17], s[80:81], 0, v[108:109]
	global_store_dwordx4 v[16:17], v[124:127], off
	s_cbranch_scc1 .LBB0_134
	s_ashr_i32 s83, s82, 31
	s_lshl_b64 s[48:49], s[82:83], 11
	v_lshl_add_u64 v[14:15], v[76:77], 0, s[48:49]
	s_add_i32 s48, s84, 2
	s_ashr_i32 s49, s48, 31
	s_lshl_b64 s[48:49], s[48:49], 10
	global_load_dwordx4 v[22:25], v[14:15], off offset:16
	s_nop 0
	global_load_dwordx4 v[14:17], v[14:15], off
	v_lshl_add_u64 v[18:19], v[78:79], 0, s[48:49]
	global_load_dwordx4 v[54:57], v[18:19], off
	global_load_dwordx4 v[58:61], v[18:19], off offset:1024
	s_waitcnt vmcnt(3)
	v_mov_b32_e32 v26, v24
	s_waitcnt vmcnt(2)
	v_mov_b32_e32 v18, v16
	v_mov_b32_e32 v19, v17
	v_mov_b32_e32 v27, v25
	s_branch .LBB0_134

.LBB0_151:
	s_waitcnt vmcnt(1)
	v_pk_mul_f32 v[72:73], v[34:35], v[34:35]
	v_pk_mul_f32 v[74:75], v[32:33], v[32:33]
	v_mul_f32_e32 v1, v4, v4
	v_pk_mov_b32 v[76:77], v[74:75], v[72:73] op_sel:[1,0]
	v_mov_b32_e32 v75, v73
	v_pk_add_f32 v[72:73], v[76:77], v[74:75]
	v_pk_mul_f32 v[74:75], v[30:31], v[30:31]
	v_pk_mul_f32 v[76:77], v[28:29], v[28:29]
	v_mul_f32_e32 v53, v5, v5
	v_pk_mov_b32 v[84:85], v[76:77], v[74:75] op_sel:[1,0]
	v_mov_b32_e32 v77, v75
	v_pk_add_f32 v[74:75], v[84:85], v[76:77]
	v_pk_add_f32 v[72:73], v[72:73], v[72:73] op_sel:[0,1] op_sel_hi:[1,0]
	v_pk_add_f32 v[74:75], v[74:75], v[74:75] op_sel:[0,1] op_sel_hi:[1,0]
	v_mov_b32_e32 v73, v1
	v_mov_b32_e32 v75, v53
	v_pk_add_f32 v[72:73], v[72:73], v[74:75]
	v_mul_f32_e32 v74, v9, v9
	v_mul_f32_e32 v76, v6, v6
	v_pk_fma_f32 v[74:75], v[8:9], v[8:9], v[74:75] op_sel_hi:[1,1,0]
	v_mul_f32_e32 v84, v7, v7
	v_mov_b32_e32 v75, v76
	v_mul_f32_e32 v76, v11, v11
	v_pk_fma_f32 v[76:77], v[10:11], v[10:11], v[76:77] op_sel_hi:[1,1,0]
	s_ashr_i32 s1, s0, 31
	v_mov_b32_e32 v77, v84
	v_pk_add_f32 v[74:75], v[74:75], v[76:77]
	s_lshl_b64 s[0:1], s[0:1], 10
	v_pk_add_f32 v[72:73], v[72:73], v[74:75]
	s_mov_b32 s16, s22
	v_add_f32_e32 v1, v72, v73
	s_waitcnt lgkmcnt(0)
	s_nop 1
	v_add_f32_dpp v1, v1, v1 quad_perm:[1,0,3,2] row_mask:0xf bank_mask:0xf
	s_waitcnt lgkmcnt(0)
	s_nop 1
	v_add_f32_dpp v1, v1, v1 quad_perm:[2,3,0,1] row_mask:0xf bank_mask:0xf
	s_waitcnt lgkmcnt(0)
	s_nop 1
	v_add_f32_dpp v1, v1, v1 row_half_mirror row_mask:0xf bank_mask:0xf
	s_waitcnt lgkmcnt(0)
	s_nop 1
	v_add_f32_dpp v1, v1, v1 row_mirror row_mask:0xf bank_mask:0xf
	s_waitcnt lgkmcnt(0)
	s_nop 1
	v_add_f32_dpp v1, v1, v1 row_bcast:15 row_mask:0xa bank_mask:0xf
	s_waitcnt lgkmcnt(0)
	s_nop 1
	v_add_f32_dpp v1, v1, v1 row_bcast:31 row_mask:0xc bank_mask:0xf
	s_nop 0
	v_readlane_b32 s101, v1, 63
	s_nop 1
	v_mov_b32_e32 v1, s101
	v_fmamk_f32 v1, v1, 0x3a800000, v210
	v_rsq_f32_e32 v72, v1
	s_nop 0
	v_pk_mul_f32 v[32:33], v[72:73], v[32:33] op_sel_hi:[0,1]
	s_waitcnt vmcnt(0)
	v_pk_fma_f32 v[48:49], v[32:33], v[66:67], v[48:49]
	v_cvt_pk_fp8_f32 v32, v48, v49
	v_pk_mul_f32 v[34:35], v[72:73], v[34:35] op_sel_hi:[0,1]
	v_pk_fma_f32 v[34:35], v[34:35], v[64:65], v[50:51]
	v_pk_mul_f32 v[28:29], v[72:73], v[28:29] op_sel_hi:[0,1]
	v_pk_mul_f32 v[8:9], v[72:73], v[8:9] op_sel_hi:[0,1]
	v_pk_mul_f32 v[4:5], v[72:73], v[4:5] op_sel_hi:[0,1]
	v_cvt_pk_fp8_f32 v32, v34, v35 op_sel:[0,0,1]
	v_pk_fma_f32 v[28:29], v[28:29], v[70:71], v[44:45]
	v_pk_fma_f32 v[8:9], v[8:9], v[62:63], v[40:41]
	v_pk_fma_f32 v[2:3], v[4:5], v[2:3], v[36:37]
	v_cvt_pk_fp8_f32 v33, v28, v29
	v_cvt_pk_fp8_f32 v34, v8, v9
	v_cvt_pk_fp8_f32 v35, v2, v3
	v_pk_mul_f32 v[30:31], v[72:73], v[30:31] op_sel_hi:[0,1]
	v_pk_mul_f32 v[10:11], v[72:73], v[10:11] op_sel_hi:[0,1]
	v_pk_mul_f32 v[6:7], v[72:73], v[6:7] op_sel_hi:[0,1]
	v_pk_fma_f32 v[30:31], v[30:31], v[68:69], v[46:47]
	v_pk_fma_f32 v[10:11], v[10:11], v[60:61], v[42:43]
	v_pk_fma_f32 v[6:7], v[6:7], v[58:59], v[38:39]
	v_cvt_pk_fp8_f32 v33, v30, v31 op_sel:[0,0,1]
	v_cvt_pk_fp8_f32 v34, v10, v11 op_sel:[0,0,1]
	v_cvt_pk_fp8_f32 v35, v6, v7 op_sel:[0,0,1]
	v_lshl_add_u64 v[2:3], v[54:55], 0, s[0:1]
	v_mov_b64_e32 v[4:5], v[12:13]
	v_mov_b64_e32 v[8:9], v[16:17]
	global_store_dwordx4 v[2:3], v[32:35], off
	v_mov_b64_e32 v[30:31], v[22:23]
	v_mov_b64_e32 v[6:7], v[14:15]
	v_mov_b64_e32 v[34:35], v[26:27]
	v_mov_b64_e32 v[10:11], v[18:19]
	v_mov_b64_e32 v[28:29], v[20:21]
	v_mov_b64_e32 v[32:33], v[24:25]
	s_cmp_ge_i32 s16, s26
	s_cbranch_scc1 .LBB0_127

.LBB0_158:
	s_ashr_i32 s23, s22, 31
	s_lshl_b64 s[10:11], s[22:23], 12
	s_add_u32 s0, s0, s10
	s_addc_u32 s1, s1, s11
	global_load_dwordx4 v[12:15], v72, s[0:1] offset:48
	global_load_dwordx4 v[16:19], v72, s[0:1] offset:32
	global_load_dwordx4 v[20:23], v72, s[0:1] offset:16
	global_load_dwordx4 v[24:27], v72, s[0:1]
	s_waitcnt vmcnt(5)
	v_pk_mul_f32 v[84:85], v[34:35], v[34:35]
	v_pk_mul_f32 v[86:87], v[32:33], v[32:33]
	v_mul_f32_e32 v1, v4, v4
	v_pk_mov_b32 v[88:89], v[86:87], v[84:85] op_sel:[1,0]
	v_mov_b32_e32 v87, v85
	v_pk_add_f32 v[84:85], v[88:89], v[86:87]
	v_pk_mul_f32 v[86:87], v[30:31], v[30:31]
	v_pk_mul_f32 v[88:89], v[28:29], v[28:29]
	v_mul_f32_e32 v53, v5, v5
	v_pk_mov_b32 v[90:91], v[88:89], v[86:87] op_sel:[1,0]
	v_mov_b32_e32 v89, v87
	v_pk_add_f32 v[86:87], v[90:91], v[88:89]
	v_pk_add_f32 v[84:85], v[84:85], v[84:85] op_sel:[0,1] op_sel_hi:[1,0]
	v_pk_add_f32 v[86:87], v[86:87], v[86:87] op_sel:[0,1] op_sel_hi:[1,0]
	v_mov_b32_e32 v85, v1
	v_mov_b32_e32 v87, v53
	v_pk_add_f32 v[84:85], v[84:85], v[86:87]
	v_mul_f32_e32 v86, v9, v9
	v_mul_f32_e32 v88, v11, v11
	v_mul_f32_e32 v73, v6, v6
	v_mul_f32_e32 v90, v7, v7
	v_pk_fma_f32 v[86:87], v[8:9], v[8:9], v[86:87] op_sel_hi:[1,1,0]
	v_pk_fma_f32 v[88:89], v[10:11], v[10:11], v[88:89] op_sel_hi:[1,1,0]
	v_mov_b32_e32 v87, v73
	v_mov_b32_e32 v89, v90
	v_pk_add_f32 v[86:87], v[86:87], v[88:89]
	s_add_i32 s1, s16, 2
	v_pk_add_f32 v[84:85], v[84:85], v[86:87]
	s_add_i32 s0, s33, 0x101
	v_add_f32_e32 v1, v84, v85
	s_cmp_ge_i32 s0, s26
	s_waitcnt lgkmcnt(0)
	s_nop 1
	v_add_f32_dpp v1, v1, v1 quad_perm:[1,0,3,2] row_mask:0xf bank_mask:0xf
	s_waitcnt lgkmcnt(0)
	s_nop 1
	v_add_f32_dpp v1, v1, v1 quad_perm:[2,3,0,1] row_mask:0xf bank_mask:0xf
	s_waitcnt lgkmcnt(0)
	s_nop 1
	v_add_f32_dpp v1, v1, v1 row_half_mirror row_mask:0xf bank_mask:0xf
	s_waitcnt lgkmcnt(0)
	s_nop 1
	v_add_f32_dpp v1, v1, v1 row_mirror row_mask:0xf bank_mask:0xf
	s_waitcnt lgkmcnt(0)
	s_nop 1
	v_add_f32_dpp v1, v1, v1 row_bcast:15 row_mask:0xa bank_mask:0xf
	s_waitcnt lgkmcnt(0)
	s_nop 1
	v_add_f32_dpp v1, v1, v1 row_bcast:31 row_mask:0xc bank_mask:0xf
	s_nop 0
	v_readlane_b32 s101, v1, 63
	s_nop 1
	v_mov_b32_e32 v1, s101
	v_fmamk_f32 v1, v1, 0x3a800000, v210
	v_rsq_f32_e32 v88, v1
	s_nop 0
	v_pk_mul_f32 v[84:85], v[88:89], v[32:33] op_sel_hi:[0,1]
	s_waitcnt vmcnt(4)
	v_pk_fma_f32 v[90:91], v[84:85], v[66:67], v[48:49]
	v_cvt_pk_fp8_f32 v84, v90, v91
	v_pk_mul_f32 v[90:91], v[88:89], v[28:29] op_sel_hi:[0,1]
	v_pk_fma_f32 v[90:91], v[90:91], v[70:71], v[44:45]
	v_pk_mul_f32 v[86:87], v[88:89], v[34:35] op_sel_hi:[0,1]
	v_cvt_pk_fp8_f32 v85, v90, v91
	v_pk_fma_f32 v[86:87], v[86:87], v[64:65], v[50:51]
	v_pk_mul_f32 v[90:91], v[88:89], v[10:11] op_sel_hi:[0,1]
	v_cvt_pk_fp8_f32 v84, v86, v87 op_sel:[0,0,1]
	v_pk_mul_f32 v[86:87], v[88:89], v[30:31] op_sel_hi:[0,1]
	v_pk_fma_f32 v[86:87], v[86:87], v[68:69], v[46:47]
	v_pk_fma_f32 v[90:91], v[90:91], v[60:61], v[42:43]
	v_cvt_pk_fp8_f32 v85, v86, v87 op_sel:[0,0,1]
	v_pk_mul_f32 v[86:87], v[88:89], v[8:9] op_sel_hi:[0,1]
	v_pk_fma_f32 v[92:93], v[86:87], v[62:63], v[40:41]
	v_cvt_pk_fp8_f32 v86, v92, v93
	v_pk_mul_f32 v[92:93], v[88:89], v[4:5] op_sel_hi:[0,1]
	v_pk_fma_f32 v[92:93], v[92:93], v[2:3], v[36:37]
	v_cvt_pk_fp8_f32 v87, v92, v93
	v_pk_mul_f32 v[88:89], v[88:89], v[6:7] op_sel_hi:[0,1]
	v_pk_fma_f32 v[88:89], v[88:89], v[58:59], v[38:39]
	v_cvt_pk_fp8_f32 v86, v90, v91 op_sel:[0,0,1]
	v_cvt_pk_fp8_f32 v87, v88, v89 op_sel:[0,0,1]
	global_store_dwordx4 v[76:77], v[84:87], off
	s_cbranch_scc1 .LBB0_164
	s_mul_hi_i32 s10, s0, 0x78787879
	s_lshr_b32 s11, s10, 31
	s_ashr_i32 s17, s10, 11
	s_add_i32 s17, s17, s11
	s_mul_i32 s23, s17, 0xffffef00
	s_add_i32 s10, s33, s23
	s_addk_i32 s10, 0x101
	s_cmpk_gt_i32 s10, 0xff
	s_cbranch_scc0 .LBB0_161
	s_lshl_b32 s10, s17, 8
	s_sub_i32 s10, s33, s10
	s_add_i32 s22, s10, 1
	s_mov_b64 s[20:21], s[12:13]
	s_cbranch_execz .LBB0_162
	s_branch .LBB0_163

.LBB0_164:
	s_waitcnt vmcnt(1)
	v_pk_mul_f32 v[84:85], v[26:27], v[26:27]
	v_pk_mul_f32 v[86:87], v[24:25], v[24:25]
	v_mul_f32_e32 v1, v12, v12
	v_pk_mov_b32 v[88:89], v[86:87], v[84:85] op_sel:[1,0]
	v_mov_b32_e32 v87, v85
	v_pk_add_f32 v[84:85], v[88:89], v[86:87]
	v_pk_mul_f32 v[86:87], v[22:23], v[22:23]
	v_pk_mul_f32 v[88:89], v[20:21], v[20:21]
	v_mul_f32_e32 v53, v13, v13
	v_pk_mov_b32 v[90:91], v[88:89], v[86:87] op_sel:[1,0]
	v_mov_b32_e32 v89, v87
	v_pk_add_f32 v[86:87], v[90:91], v[88:89]
	v_pk_add_f32 v[84:85], v[84:85], v[84:85] op_sel:[0,1] op_sel_hi:[1,0]
	v_pk_add_f32 v[86:87], v[86:87], v[86:87] op_sel:[0,1] op_sel_hi:[1,0]
	v_mov_b32_e32 v85, v1
	v_mov_b32_e32 v87, v53
	v_pk_add_f32 v[84:85], v[84:85], v[86:87]
	v_mul_f32_e32 v86, v17, v17
	v_mul_f32_e32 v88, v19, v19
	v_mul_f32_e32 v73, v14, v14
	v_mul_f32_e32 v90, v15, v15
	v_pk_fma_f32 v[86:87], v[16:17], v[16:17], v[86:87] op_sel_hi:[1,1,0]
	v_pk_fma_f32 v[88:89], v[18:19], v[18:19], v[88:89] op_sel_hi:[1,1,0]
	v_mov_b32_e32 v87, v73
	v_mov_b32_e32 v89, v90
	v_pk_add_f32 v[86:87], v[86:87], v[88:89]
	s_add_i32 s20, s16, 3
	v_pk_add_f32 v[84:85], v[84:85], v[86:87]
	s_add_i32 s10, s33, 2
	v_add_f32_e32 v1, v84, v85
	s_add_i32 s22, s33, 0x102
	v_lshl_add_u64 v[76:77], v[76:77], 0, s[34:35]
	s_cmp_lt_i32 s22, s27
	s_waitcnt lgkmcnt(0)
	s_nop 1
	v_add_f32_dpp v1, v1, v1 quad_perm:[1,0,3,2] row_mask:0xf bank_mask:0xf
	s_waitcnt lgkmcnt(0)
	s_nop 1
	v_add_f32_dpp v1, v1, v1 quad_perm:[2,3,0,1] row_mask:0xf bank_mask:0xf
	s_waitcnt lgkmcnt(0)
	s_nop 1
	v_add_f32_dpp v1, v1, v1 row_half_mirror row_mask:0xf bank_mask:0xf
	s_waitcnt lgkmcnt(0)
	s_nop 1
	v_add_f32_dpp v1, v1, v1 row_mirror row_mask:0xf bank_mask:0xf
	s_waitcnt lgkmcnt(0)
	s_nop 1
	v_add_f32_dpp v1, v1, v1 row_bcast:15 row_mask:0xa bank_mask:0xf
	s_waitcnt lgkmcnt(0)
	s_nop 1
	v_add_f32_dpp v1, v1, v1 row_bcast:31 row_mask:0xc bank_mask:0xf
	s_nop 0
	v_readlane_b32 s101, v1, 63
	s_nop 1
	v_mov_b32_e32 v1, s101
	v_fmamk_f32 v1, v1, 0x3a800000, v210
	v_rsq_f32_e32 v88, v1
	s_nop 0
	v_pk_mul_f32 v[84:85], v[88:89], v[24:25] op_sel_hi:[0,1]
	v_pk_fma_f32 v[90:91], v[84:85], v[66:67], v[48:49]
	v_cvt_pk_fp8_f32 v84, v90, v91
	v_pk_mul_f32 v[86:87], v[88:89], v[26:27] op_sel_hi:[0,1]
	v_pk_fma_f32 v[86:87], v[86:87], v[64:65], v[50:51]
	v_cvt_pk_fp8_f32 v84, v86, v87 op_sel:[0,0,1]
	v_pk_mul_f32 v[86:87], v[88:89], v[20:21] op_sel_hi:[0,1]
	v_pk_fma_f32 v[86:87], v[86:87], v[70:71], v[44:45]
	v_pk_mul_f32 v[90:91], v[88:89], v[22:23] op_sel_hi:[0,1]
	v_cvt_pk_fp8_f32 v85, v86, v87
	v_pk_mul_f32 v[86:87], v[88:89], v[16:17] op_sel_hi:[0,1]
	v_pk_fma_f32 v[92:93], v[86:87], v[62:63], v[40:41]
	v_cvt_pk_fp8_f32 v86, v92, v93
	v_pk_fma_f32 v[90:91], v[90:91], v[68:69], v[46:47]
	v_cvt_pk_fp8_f32 v85, v90, v91 op_sel:[0,0,1]
	v_pk_mul_f32 v[90:91], v[88:89], v[18:19] op_sel_hi:[0,1]
	v_pk_fma_f32 v[90:91], v[90:91], v[60:61], v[42:43]
	s_nop 0
	v_cvt_pk_fp8_f32 v86, v90, v91 op_sel:[0,0,1]
	v_pk_mul_f32 v[90:91], v[88:89], v[12:13] op_sel_hi:[0,1]
	v_pk_fma_f32 v[90:91], v[90:91], v[2:3], v[36:37]
	v_pk_mul_f32 v[88:89], v[88:89], v[14:15] op_sel_hi:[0,1]
	v_cvt_pk_fp8_f32 v87, v90, v91
	v_pk_fma_f32 v[88:89], v[88:89], v[58:59], v[38:39]
	s_nop 0
	v_cvt_pk_fp8_f32 v87, v88, v89 op_sel:[0,0,1]
	global_store_dwordx4 v[74:75], v[84:87], off
	v_lshl_add_u64 v[74:75], v[74:75], 0, s[34:35]
	s_cbranch_scc0 .LBB0_167
	s_mov_b32 s33, s10
	s_mov_b32 s16, s1
	s_branch .LBB0_154

.LBB0_258:
	s_andn2_b64 vcc, exec, s[8:9]
	s_cbranch_vccnz .LBB0_260
	v_pk_mul_f32 v[2:3], v[180:181], v[158:159] op_sel_hi:[0,1]
	v_pk_mul_f32 v[8:9], v[180:181], v[154:155] op_sel_hi:[0,1]
	v_cvt_pk_fp8_f32 v6, v2, v3
	v_cvt_pk_fp8_f32 v7, v8, v9
	v_pk_mul_f32 v[2:3], v[180:181], v[160:161] op_sel_hi:[0,1]
	v_pk_mul_f32 v[8:9], v[180:181], v[156:157] op_sel_hi:[0,1]
	v_cvt_pk_fp8_f32 v6, v2, v3 op_sel:[0,0,1]
	v_cvt_pk_fp8_f32 v7, v8, v9 op_sel:[0,0,1]
	v_pk_mul_f32 v[2:3], v[180:181], v[150:151] op_sel_hi:[0,1]
	v_pk_mul_f32 v[10:11], v[180:181], v[146:147] op_sel_hi:[0,1]
	v_cvt_pk_fp8_f32 v8, v2, v3
	v_cvt_pk_fp8_f32 v9, v10, v11
	v_pk_mul_f32 v[2:3], v[180:181], v[152:153] op_sel_hi:[0,1]
	v_pk_mul_f32 v[10:11], v[180:181], v[148:149] op_sel_hi:[0,1]
	v_cvt_pk_fp8_f32 v8, v2, v3 op_sel:[0,0,1]
	v_cvt_pk_fp8_f32 v9, v10, v11 op_sel:[0,0,1]
	v_mul_lo_u32 v2, s85, v181
	v_mov_b32_e32 v3, v0
	v_lshl_add_u64 v[10:11], v[178:179], 0, v[2:3]
	v_lshl_add_u64 v[12:13], v[10:11], 0, s[20:21]
	v_lshl_add_u64 v[12:13], v[12:13], 0, -8
	v_permlane16_swap_b32_e32 v6, v8
	v_permlane16_swap_b32_e32 v7, v9
	v_cndmask_b32_e64 v11, v13, v11, s[0:1]
	v_cndmask_b32_e64 v10, v12, v10, s[0:1]
	global_store_dwordx4 v[10:11], v[6:9], off
	v_pk_mul_f32 v[10:11], v[180:181], v[138:139] op_sel_hi:[0,1]
	v_pk_mul_f32 v[12:13], v[180:181], v[130:131] op_sel_hi:[0,1]
	v_pk_mul_f32 v[8:9], v[180:181], v[142:143] op_sel_hi:[0,1]
	v_cvt_pk_fp8_f32 v6, v8, v9
	v_cvt_pk_fp8_f32 v7, v10, v11
	v_pk_mul_f32 v[8:9], v[180:181], v[144:145] op_sel_hi:[0,1]
	v_pk_mul_f32 v[10:11], v[180:181], v[140:141] op_sel_hi:[0,1]
	v_cvt_pk_fp8_f32 v6, v8, v9 op_sel:[0,0,1]
	v_cvt_pk_fp8_f32 v7, v10, v11 op_sel:[0,0,1]
	v_pk_mul_f32 v[10:11], v[180:181], v[134:135] op_sel_hi:[0,1]
	v_cvt_pk_fp8_f32 v8, v10, v11
	v_cvt_pk_fp8_f32 v9, v12, v13
	v_pk_mul_f32 v[10:11], v[180:181], v[136:137] op_sel_hi:[0,1]
	v_pk_mul_f32 v[12:13], v[180:181], v[132:133] op_sel_hi:[0,1]
	s_lshl_b32 s8, s85, 4
	v_cvt_pk_fp8_f32 v8, v10, v11 op_sel:[0,0,1]
	v_cvt_pk_fp8_f32 v9, v12, v13 op_sel:[0,0,1]
	v_add_u32_e32 v2, s8, v2
	v_lshl_add_u64 v[10:11], v[178:179], 0, v[2:3]
	v_lshl_add_u64 v[12:13], v[10:11], 0, s[20:21]
	v_lshl_add_u64 v[12:13], v[12:13], 0, -8
	v_permlane16_swap_b32_e32 v6, v8
	v_permlane16_swap_b32_e32 v7, v9
	v_cndmask_b32_e64 v11, v13, v11, s[0:1]
	v_cndmask_b32_e64 v10, v12, v10, s[0:1]
	global_store_dwordx4 v[10:11], v[6:9], off
	v_pk_mul_f32 v[10:11], v[180:181], v[122:123] op_sel_hi:[0,1]
	v_pk_mul_f32 v[12:13], v[180:181], v[114:115] op_sel_hi:[0,1]
	v_pk_mul_f32 v[8:9], v[180:181], v[126:127] op_sel_hi:[0,1]
	v_cvt_pk_fp8_f32 v6, v8, v9
	v_cvt_pk_fp8_f32 v7, v10, v11
	v_pk_mul_f32 v[8:9], v[180:181], v[128:129] op_sel_hi:[0,1]
	v_pk_mul_f32 v[10:11], v[180:181], v[124:125] op_sel_hi:[0,1]
	v_cvt_pk_fp8_f32 v6, v8, v9 op_sel:[0,0,1]
	v_cvt_pk_fp8_f32 v7, v10, v11 op_sel:[0,0,1]
	v_pk_mul_f32 v[10:11], v[180:181], v[118:119] op_sel_hi:[0,1]
	v_cvt_pk_fp8_f32 v8, v10, v11
	v_cvt_pk_fp8_f32 v9, v12, v13
	v_pk_mul_f32 v[10:11], v[180:181], v[120:121] op_sel_hi:[0,1]
	v_pk_mul_f32 v[12:13], v[180:181], v[116:117] op_sel_hi:[0,1]
	v_cvt_pk_fp8_f32 v8, v10, v11 op_sel:[0,0,1]
	v_cvt_pk_fp8_f32 v9, v12, v13 op_sel:[0,0,1]
	v_add_u32_e32 v2, s8, v2
	v_lshl_add_u64 v[10:11], v[178:179], 0, v[2:3]
	v_lshl_add_u64 v[12:13], v[10:11], 0, s[20:21]
	v_lshl_add_u64 v[12:13], v[12:13], 0, -8
	v_permlane16_swap_b32_e32 v6, v8
	v_permlane16_swap_b32_e32 v7, v9
	v_cndmask_b32_e64 v11, v13, v11, s[0:1]
	v_cndmask_b32_e64 v10, v12, v10, s[0:1]
	global_store_dwordx4 v[10:11], v[6:9], off
	v_pk_mul_f32 v[10:11], v[180:181], v[106:107] op_sel_hi:[0,1]
	v_pk_mul_f32 v[12:13], v[180:181], v[98:99] op_sel_hi:[0,1]
	v_pk_mul_f32 v[8:9], v[180:181], v[110:111] op_sel_hi:[0,1]
	v_cvt_pk_fp8_f32 v6, v8, v9
	v_cvt_pk_fp8_f32 v7, v10, v11
	v_pk_mul_f32 v[8:9], v[180:181], v[112:113] op_sel_hi:[0,1]
	v_pk_mul_f32 v[10:11], v[180:181], v[108:109] op_sel_hi:[0,1]
	v_cvt_pk_fp8_f32 v6, v8, v9 op_sel:[0,0,1]
	v_cvt_pk_fp8_f32 v7, v10, v11 op_sel:[0,0,1]
	v_pk_mul_f32 v[10:11], v[180:181], v[102:103] op_sel_hi:[0,1]
	v_cvt_pk_fp8_f32 v8, v10, v11
	v_cvt_pk_fp8_f32 v9, v12, v13
	v_pk_mul_f32 v[10:11], v[180:181], v[104:105] op_sel_hi:[0,1]
	v_pk_mul_f32 v[12:13], v[180:181], v[100:101] op_sel_hi:[0,1]
	v_cvt_pk_fp8_f32 v8, v10, v11 op_sel:[0,0,1]
	v_cvt_pk_fp8_f32 v9, v12, v13 op_sel:[0,0,1]
	v_add_u32_e32 v2, s8, v2
	v_lshl_add_u64 v[10:11], v[178:179], 0, v[2:3]
	v_lshl_add_u64 v[12:13], v[10:11], 0, s[20:21]
	v_lshl_add_u64 v[12:13], v[12:13], 0, -8
	v_permlane16_swap_b32_e32 v6, v8
	v_permlane16_swap_b32_e32 v7, v9
	v_cndmask_b32_e64 v11, v13, v11, s[0:1]
	v_cndmask_b32_e64 v10, v12, v10, s[0:1]
	global_store_dwordx4 v[10:11], v[6:9], off
	v_pk_mul_f32 v[10:11], v[180:181], v[90:91] op_sel_hi:[0,1]
	v_pk_mul_f32 v[12:13], v[180:181], v[82:83] op_sel_hi:[0,1]
	v_pk_mul_f32 v[8:9], v[180:181], v[94:95] op_sel_hi:[0,1]
	v_cvt_pk_fp8_f32 v6, v8, v9
	v_cvt_pk_fp8_f32 v7, v10, v11
	v_pk_mul_f32 v[8:9], v[180:181], v[96:97] op_sel_hi:[0,1]
	v_pk_mul_f32 v[10:11], v[180:181], v[92:93] op_sel_hi:[0,1]
	v_cvt_pk_fp8_f32 v6, v8, v9 op_sel:[0,0,1]
	v_cvt_pk_fp8_f32 v7, v10, v11 op_sel:[0,0,1]
	v_pk_mul_f32 v[10:11], v[180:181], v[86:87] op_sel_hi:[0,1]
	v_cvt_pk_fp8_f32 v8, v10, v11
	v_cvt_pk_fp8_f32 v9, v12, v13
	v_pk_mul_f32 v[10:11], v[180:181], v[88:89] op_sel_hi:[0,1]
	v_pk_mul_f32 v[12:13], v[180:181], v[84:85] op_sel_hi:[0,1]
	s_mul_i32 s9, s85, 0x50
	v_cvt_pk_fp8_f32 v8, v10, v11 op_sel:[0,0,1]
	v_cvt_pk_fp8_f32 v9, v12, v13 op_sel:[0,0,1]
	v_add_u32_e32 v2, s9, v2
	v_lshl_add_u64 v[10:11], v[178:179], 0, v[2:3]
	v_lshl_add_u64 v[12:13], v[10:11], 0, s[20:21]
	v_lshl_add_u64 v[12:13], v[12:13], 0, -8
	v_permlane16_swap_b32_e32 v6, v8
	v_permlane16_swap_b32_e32 v7, v9
	v_cndmask_b32_e64 v11, v13, v11, s[0:1]
	v_cndmask_b32_e64 v10, v12, v10, s[0:1]
	global_store_dwordx4 v[10:11], v[6:9], off
	v_pk_mul_f32 v[10:11], v[180:181], v[74:75] op_sel_hi:[0,1]
	v_pk_mul_f32 v[12:13], v[180:181], v[66:67] op_sel_hi:[0,1]
	v_pk_mul_f32 v[8:9], v[180:181], v[78:79] op_sel_hi:[0,1]
	v_cvt_pk_fp8_f32 v6, v8, v9
	v_cvt_pk_fp8_f32 v7, v10, v11
	v_pk_mul_f32 v[8:9], v[180:181], v[80:81] op_sel_hi:[0,1]
	v_pk_mul_f32 v[10:11], v[180:181], v[76:77] op_sel_hi:[0,1]
	v_cvt_pk_fp8_f32 v6, v8, v9 op_sel:[0,0,1]
	v_cvt_pk_fp8_f32 v7, v10, v11 op_sel:[0,0,1]
	v_pk_mul_f32 v[10:11], v[180:181], v[70:71] op_sel_hi:[0,1]
	v_cvt_pk_fp8_f32 v8, v10, v11
	v_cvt_pk_fp8_f32 v9, v12, v13
	v_pk_mul_f32 v[10:11], v[180:181], v[72:73] op_sel_hi:[0,1]
	v_pk_mul_f32 v[12:13], v[180:181], v[68:69] op_sel_hi:[0,1]
	v_cvt_pk_fp8_f32 v8, v10, v11 op_sel:[0,0,1]
	v_cvt_pk_fp8_f32 v9, v12, v13 op_sel:[0,0,1]
	v_add_u32_e32 v2, s8, v2
	v_lshl_add_u64 v[10:11], v[178:179], 0, v[2:3]
	v_lshl_add_u64 v[12:13], v[10:11], 0, s[20:21]
	v_lshl_add_u64 v[12:13], v[12:13], 0, -8
	v_permlane16_swap_b32_e32 v6, v8
	v_permlane16_swap_b32_e32 v7, v9
	v_cndmask_b32_e64 v11, v13, v11, s[0:1]
	v_cndmask_b32_e64 v10, v12, v10, s[0:1]
	global_store_dwordx4 v[10:11], v[6:9], off
	v_pk_mul_f32 v[10:11], v[180:181], v[50:51] op_sel_hi:[0,1]
	v_pk_mul_f32 v[12:13], v[180:181], v[58:59] op_sel_hi:[0,1]
	v_pk_mul_f32 v[8:9], v[180:181], v[54:55] op_sel_hi:[0,1]
	v_cvt_pk_fp8_f32 v6, v8, v9
	v_cvt_pk_fp8_f32 v7, v10, v11
	v_pk_mul_f32 v[8:9], v[180:181], v[56:57] op_sel_hi:[0,1]
	v_pk_mul_f32 v[10:11], v[180:181], v[52:53] op_sel_hi:[0,1]
	v_cvt_pk_fp8_f32 v6, v8, v9 op_sel:[0,0,1]
	v_cvt_pk_fp8_f32 v7, v10, v11 op_sel:[0,0,1]
	v_pk_mul_f32 v[10:11], v[180:181], v[62:63] op_sel_hi:[0,1]
	v_cvt_pk_fp8_f32 v8, v10, v11
	v_cvt_pk_fp8_f32 v9, v12, v13
	v_pk_mul_f32 v[10:11], v[180:181], v[64:65] op_sel_hi:[0,1]
	v_pk_mul_f32 v[12:13], v[180:181], v[60:61] op_sel_hi:[0,1]
	v_cvt_pk_fp8_f32 v8, v10, v11 op_sel:[0,0,1]
	v_cvt_pk_fp8_f32 v9, v12, v13 op_sel:[0,0,1]
	v_add_u32_e32 v2, s8, v2
	v_lshl_add_u64 v[10:11], v[178:179], 0, v[2:3]
	v_lshl_add_u64 v[12:13], v[10:11], 0, s[20:21]
	v_lshl_add_u64 v[12:13], v[12:13], 0, -8
	v_permlane16_swap_b32_e32 v6, v8
	v_permlane16_swap_b32_e32 v7, v9
	v_cndmask_b32_e64 v11, v13, v11, s[0:1]
	v_cndmask_b32_e64 v10, v12, v10, s[0:1]
	global_store_dwordx4 v[10:11], v[6:9], off
	v_pk_mul_f32 v[10:11], v[180:181], v[34:35] op_sel_hi:[0,1]
	v_pk_mul_f32 v[12:13], v[180:181], v[42:43] op_sel_hi:[0,1]
	v_pk_mul_f32 v[8:9], v[180:181], v[38:39] op_sel_hi:[0,1]
	v_cvt_pk_fp8_f32 v6, v8, v9
	v_cvt_pk_fp8_f32 v7, v10, v11
	v_pk_mul_f32 v[8:9], v[180:181], v[40:41] op_sel_hi:[0,1]
	v_pk_mul_f32 v[10:11], v[180:181], v[36:37] op_sel_hi:[0,1]
	v_cvt_pk_fp8_f32 v6, v8, v9 op_sel:[0,0,1]
	v_cvt_pk_fp8_f32 v7, v10, v11 op_sel:[0,0,1]
	v_pk_mul_f32 v[10:11], v[180:181], v[46:47] op_sel_hi:[0,1]
	v_cvt_pk_fp8_f32 v8, v10, v11
	v_cvt_pk_fp8_f32 v9, v12, v13
	v_pk_mul_f32 v[10:11], v[180:181], v[48:49] op_sel_hi:[0,1]
	v_pk_mul_f32 v[12:13], v[180:181], v[44:45] op_sel_hi:[0,1]
	v_cvt_pk_fp8_f32 v8, v10, v11 op_sel:[0,0,1]
	v_cvt_pk_fp8_f32 v9, v12, v13 op_sel:[0,0,1]
	v_add_u32_e32 v2, s8, v2
	v_lshl_add_u64 v[2:3], v[178:179], 0, v[2:3]
	v_lshl_add_u64 v[10:11], v[2:3], 0, s[20:21]
	v_lshl_add_u64 v[10:11], v[10:11], 0, -8
	v_permlane16_swap_b32_e32 v6, v8
	v_permlane16_swap_b32_e32 v7, v9
	v_cndmask_b32_e64 v3, v11, v3, s[0:1]
	v_cndmask_b32_e64 v2, v10, v2, s[0:1]
	global_store_dwordx4 v[2:3], v[6:9], off

.LBB0_264:
	s_andn2_b64 vcc, exec, s[8:9]
	s_cbranch_vccnz .LBB0_266
	s_waitcnt vmcnt(0)
	v_pk_mul_f32 v[30:31], v[180:181], v[30:31] op_sel_hi:[0,1]
	v_pk_mul_f32 v[162:163], v[180:181], v[26:27] op_sel_hi:[0,1]
	v_mov_b32_e32 v164, v30
	v_mov_b32_e32 v165, v162
	v_pk_mul_f32 v[26:27], v[158:159], v[164:165]
	v_mov_b32_e32 v166, v162
	v_mov_b32_e32 v167, v30
	v_sub_f32_e32 v168, v26, v27
	v_pk_mul_f32 v[26:27], v[158:159], v[166:167]
	v_mov_b32_e32 v162, v31
	v_pk_mul_f32 v[32:33], v[180:181], v[32:33] op_sel_hi:[0,1]
	v_pk_mul_f32 v[28:29], v[180:181], v[28:29] op_sel_hi:[0,1]
	v_add_f32_e32 v169, v27, v26
	v_pk_mul_f32 v[26:27], v[160:161], v[162:163]
	v_mov_b32_e32 v30, v163
	v_sub_f32_e32 v182, v26, v27
	v_pk_mul_f32 v[26:27], v[160:161], v[30:31]
	v_mov_b32_e32 v158, v32
	v_mov_b32_e32 v159, v28
	v_add_f32_e32 v184, v27, v26
	v_pk_mul_f32 v[26:27], v[154:155], v[158:159]
	v_mov_b32_e32 v160, v28
	v_mov_b32_e32 v161, v32
	v_sub_f32_e32 v185, v26, v27
	v_pk_mul_f32 v[26:27], v[154:155], v[160:161]
	v_mov_b32_e32 v28, v33
	v_add_f32_e32 v154, v27, v26
	v_pk_mul_f32 v[26:27], v[156:157], v[28:29]
	v_mov_b32_e32 v32, v29
	v_sub_f32_e32 v155, v26, v27
	v_pk_mul_f32 v[26:27], v[156:157], v[32:33]
	v_pk_mul_f32 v[30:31], v[152:153], v[30:31]
	v_add_f32_e32 v156, v27, v26
	v_cvt_pk_fp8_f32 v27, v185, v154
	v_pk_mul_f32 v[28:29], v[148:149], v[28:29]
	v_cvt_pk_fp8_f32 v26, v168, v169
	v_cvt_pk_fp8_f32 v27, v155, v156 op_sel:[0,0,1]
	v_pk_mul_f32 v[154:155], v[150:151], v[164:165]
	v_pk_mul_f32 v[150:151], v[150:151], v[166:167]
	v_sub_f32_e32 v154, v154, v155
	v_add_f32_e32 v155, v151, v150
	v_pk_mul_f32 v[150:151], v[152:153], v[162:163]
	v_cvt_pk_fp8_f32 v26, v182, v184 op_sel:[0,0,1]
	v_sub_f32_e32 v150, v150, v151
	v_add_f32_e32 v151, v31, v30
	v_pk_mul_f32 v[30:31], v[146:147], v[158:159]
	v_pk_mul_f32 v[22:23], v[180:181], v[22:23] op_sel_hi:[0,1]
	v_sub_f32_e32 v152, v30, v31
	v_pk_mul_f32 v[30:31], v[146:147], v[160:161]
	v_pk_mul_f32 v[24:25], v[180:181], v[24:25] op_sel_hi:[0,1]
	v_add_f32_e32 v30, v31, v30
	v_sub_f32_e32 v31, v28, v29
	v_pk_mul_f32 v[28:29], v[148:149], v[32:33]
	v_pk_mul_f32 v[20:21], v[180:181], v[20:21] op_sel_hi:[0,1]
	v_add_f32_e32 v32, v29, v28
	v_cvt_pk_fp8_f32 v28, v154, v155
	v_cvt_pk_fp8_f32 v29, v152, v30
	v_mul_lo_u32 v30, s85, v181
	s_lshl_b32 s8, s85, 4
	v_cvt_pk_fp8_f32 v28, v150, v151 op_sel:[0,0,1]
	v_cvt_pk_fp8_f32 v29, v31, v32 op_sel:[0,0,1]
	v_mov_b32_e32 v31, v0
	v_lshl_add_u64 v[32:33], v[178:179], 0, v[30:31]
	v_lshl_add_u64 v[146:147], v[32:33], 0, s[20:21]
	v_lshl_add_u64 v[146:147], v[146:147], 0, -8
	v_permlane16_swap_b32_e32 v26, v28
	v_permlane16_swap_b32_e32 v27, v29
	v_cndmask_b32_e64 v33, v147, v33, s[0:1]
	v_cndmask_b32_e64 v32, v146, v32, s[0:1]
	global_store_dwordx4 v[32:33], v[26:29], off
	v_mov_b32_e32 v33, v22
	v_pk_mul_f32 v[14:15], v[180:181], v[14:15] op_sel_hi:[0,1]
	v_pk_mul_f32 v[26:27], v[180:181], v[18:19] op_sel_hi:[0,1]
	v_mov_b32_e32 v28, v22
	v_mov_b32_e32 v29, v26
	v_pk_mul_f32 v[18:19], v[142:143], v[28:29]
	v_mov_b32_e32 v32, v26
	v_sub_f32_e32 v31, v18, v19
	v_pk_mul_f32 v[18:19], v[142:143], v[32:33]
	v_mov_b32_e32 v26, v23
	v_add_f32_e32 v146, v19, v18
	v_pk_mul_f32 v[18:19], v[144:145], v[26:27]
	v_mov_b32_e32 v22, v27
	v_sub_f32_e32 v147, v18, v19
	v_pk_mul_f32 v[18:19], v[144:145], v[22:23]
	v_mov_b32_e32 v142, v24
	v_mov_b32_e32 v143, v20
	v_add_f32_e32 v148, v19, v18
	v_pk_mul_f32 v[18:19], v[138:139], v[142:143]
	v_mov_b32_e32 v144, v20
	v_mov_b32_e32 v145, v24
	v_sub_f32_e32 v149, v18, v19
	v_pk_mul_f32 v[18:19], v[138:139], v[144:145]
	v_mov_b32_e32 v20, v25
	v_add_f32_e32 v138, v19, v18
	v_pk_mul_f32 v[18:19], v[140:141], v[20:21]
	v_mov_b32_e32 v24, v21
	v_sub_f32_e32 v139, v18, v19
	v_pk_mul_f32 v[18:19], v[140:141], v[24:25]
	v_pk_mul_f32 v[28:29], v[134:135], v[28:29]
	v_add_f32_e32 v140, v19, v18
	v_pk_mul_f32 v[26:27], v[136:137], v[26:27]
	v_pk_mul_f32 v[22:23], v[136:137], v[22:23]
	v_cvt_pk_fp8_f32 v18, v31, v146
	v_sub_f32_e32 v31, v28, v29
	v_pk_mul_f32 v[28:29], v[134:135], v[32:33]
	v_sub_f32_e32 v26, v26, v27
	v_add_f32_e32 v27, v23, v22
	v_pk_mul_f32 v[22:23], v[130:131], v[142:143]
	v_add_f32_e32 v28, v29, v28
	v_sub_f32_e32 v29, v22, v23
	v_pk_mul_f32 v[22:23], v[130:131], v[144:145]
	v_pk_mul_f32 v[20:21], v[132:133], v[20:21]
	v_add_f32_e32 v22, v23, v22
	v_sub_f32_e32 v23, v20, v21
	v_pk_mul_f32 v[20:21], v[132:133], v[24:25]
	v_add_f32_e32 v24, v21, v20
	v_cvt_pk_fp8_f32 v19, v149, v138
	v_cvt_pk_fp8_f32 v20, v31, v28
	v_cvt_pk_fp8_f32 v21, v29, v22
	v_cvt_pk_fp8_f32 v18, v147, v148 op_sel:[0,0,1]
	v_cvt_pk_fp8_f32 v19, v139, v140 op_sel:[0,0,1]
	v_cvt_pk_fp8_f32 v20, v26, v27 op_sel:[0,0,1]
	v_cvt_pk_fp8_f32 v21, v23, v24 op_sel:[0,0,1]
	v_add_u32_e32 v22, s8, v30
	v_mov_b32_e32 v23, v0
	v_lshl_add_u64 v[24:25], v[178:179], 0, v[22:23]
	v_lshl_add_u64 v[26:27], v[24:25], 0, s[20:21]
	v_lshl_add_u64 v[26:27], v[26:27], 0, -8
	v_permlane16_swap_b32_e32 v18, v20
	v_permlane16_swap_b32_e32 v19, v21
	v_cndmask_b32_e64 v25, v27, v25, s[0:1]
	v_cndmask_b32_e64 v24, v26, v24, s[0:1]
	global_store_dwordx4 v[24:25], v[18:21], off
	v_mov_b32_e32 v25, v14
	v_pk_mul_f32 v[16:17], v[180:181], v[16:17] op_sel_hi:[0,1]
	v_pk_mul_f32 v[18:19], v[180:181], v[10:11] op_sel_hi:[0,1]
	v_mov_b32_e32 v20, v14
	v_mov_b32_e32 v21, v18
	v_pk_mul_f32 v[10:11], v[126:127], v[20:21]
	v_mov_b32_e32 v24, v18
	v_sub_f32_e32 v23, v10, v11
	v_pk_mul_f32 v[10:11], v[126:127], v[24:25]
	v_mov_b32_e32 v18, v15
	v_pk_mul_f32 v[12:13], v[180:181], v[12:13] op_sel_hi:[0,1]
	v_add_f32_e32 v30, v11, v10
	v_pk_mul_f32 v[10:11], v[128:129], v[18:19]
	v_mov_b32_e32 v14, v19
	v_sub_f32_e32 v31, v10, v11
	v_pk_mul_f32 v[10:11], v[128:129], v[14:15]
	v_mov_b32_e32 v26, v16
	v_mov_b32_e32 v27, v12
	v_add_f32_e32 v32, v11, v10
	v_pk_mul_f32 v[10:11], v[122:123], v[26:27]
	v_mov_b32_e32 v28, v12
	v_mov_b32_e32 v29, v16
	v_sub_f32_e32 v33, v10, v11
	v_pk_mul_f32 v[10:11], v[122:123], v[28:29]
	v_mov_b32_e32 v12, v17
	v_add_f32_e32 v122, v11, v10
	v_pk_mul_f32 v[10:11], v[124:125], v[12:13]
	v_mov_b32_e32 v16, v13
	v_sub_f32_e32 v123, v10, v11
	v_pk_mul_f32 v[10:11], v[124:125], v[16:17]
	v_pk_mul_f32 v[20:21], v[118:119], v[20:21]
	v_add_f32_e32 v124, v11, v10
	v_pk_mul_f32 v[18:19], v[120:121], v[18:19]
	v_pk_mul_f32 v[14:15], v[120:121], v[14:15]
	v_cvt_pk_fp8_f32 v10, v23, v30
	v_sub_f32_e32 v23, v20, v21
	v_pk_mul_f32 v[20:21], v[118:119], v[24:25]
	v_sub_f32_e32 v18, v18, v19
	v_add_f32_e32 v19, v15, v14
	v_pk_mul_f32 v[14:15], v[114:115], v[26:27]
	v_add_f32_e32 v20, v21, v20
	v_sub_f32_e32 v21, v14, v15
	v_pk_mul_f32 v[14:15], v[114:115], v[28:29]
	v_pk_mul_f32 v[12:13], v[116:117], v[12:13]
	v_add_f32_e32 v14, v15, v14
	v_sub_f32_e32 v15, v12, v13
	v_pk_mul_f32 v[12:13], v[116:117], v[16:17]
	v_add_f32_e32 v16, v13, v12
	v_cvt_pk_fp8_f32 v11, v33, v122
	v_cvt_pk_fp8_f32 v12, v23, v20
	v_cvt_pk_fp8_f32 v13, v21, v14
	v_cvt_pk_fp8_f32 v10, v31, v32 op_sel:[0,0,1]
	v_cvt_pk_fp8_f32 v11, v123, v124 op_sel:[0,0,1]
	v_cvt_pk_fp8_f32 v12, v18, v19 op_sel:[0,0,1]
	v_cvt_pk_fp8_f32 v13, v15, v16 op_sel:[0,0,1]
	v_add_u32_e32 v14, s8, v22
	v_mov_b32_e32 v15, v0
	v_lshl_add_u64 v[16:17], v[178:179], 0, v[14:15]
	v_lshl_add_u64 v[18:19], v[16:17], 0, s[20:21]
	v_lshl_add_u64 v[18:19], v[18:19], 0, -8
	v_permlane16_swap_b32_e32 v10, v12
	v_permlane16_swap_b32_e32 v11, v13
	v_cndmask_b32_e64 v17, v19, v17, s[0:1]
	v_cndmask_b32_e64 v16, v18, v16, s[0:1]
	global_store_dwordx4 v[16:17], v[10:13], off
	v_pk_mul_f32 v[6:7], v[180:181], v[6:7] op_sel_hi:[0,1]
	v_mov_b32_e32 v17, v6
	v_pk_mul_f32 v[10:11], v[180:181], v[2:3] op_sel_hi:[0,1]
	v_mov_b32_e32 v12, v6
	v_mov_b32_e32 v13, v10
	v_pk_mul_f32 v[2:3], v[110:111], v[12:13]
	v_mov_b32_e32 v16, v10
	v_sub_f32_e32 v15, v2, v3
	v_pk_mul_f32 v[2:3], v[110:111], v[16:17]
	v_mov_b32_e32 v10, v7
	v_pk_mul_f32 v[8:9], v[180:181], v[8:9] op_sel_hi:[0,1]
	v_pk_mul_f32 v[4:5], v[180:181], v[4:5] op_sel_hi:[0,1]
	v_add_f32_e32 v22, v3, v2
	v_pk_mul_f32 v[2:3], v[112:113], v[10:11]
	v_mov_b32_e32 v6, v11
	v_sub_f32_e32 v23, v2, v3
	v_pk_mul_f32 v[2:3], v[112:113], v[6:7]
	v_mov_b32_e32 v18, v8
	v_mov_b32_e32 v19, v4
	v_add_f32_e32 v24, v3, v2
	v_pk_mul_f32 v[2:3], v[106:107], v[18:19]
	v_mov_b32_e32 v20, v4
	v_mov_b32_e32 v21, v8
	v_sub_f32_e32 v25, v2, v3
	v_pk_mul_f32 v[2:3], v[106:107], v[20:21]
	v_mov_b32_e32 v4, v9
	v_add_f32_e32 v26, v3, v2
	v_pk_mul_f32 v[2:3], v[108:109], v[4:5]
	v_mov_b32_e32 v8, v5
	v_sub_f32_e32 v27, v2, v3
	v_pk_mul_f32 v[2:3], v[108:109], v[8:9]
	v_pk_mul_f32 v[12:13], v[102:103], v[12:13]
	v_add_f32_e32 v28, v3, v2
	v_pk_mul_f32 v[10:11], v[104:105], v[10:11]
	v_pk_mul_f32 v[6:7], v[104:105], v[6:7]
	v_cvt_pk_fp8_f32 v2, v15, v22
	v_sub_f32_e32 v15, v12, v13
	v_pk_mul_f32 v[12:13], v[102:103], v[16:17]
	v_sub_f32_e32 v10, v10, v11
	v_add_f32_e32 v11, v7, v6
	v_pk_mul_f32 v[6:7], v[98:99], v[18:19]
	v_add_f32_e32 v12, v13, v12
	v_sub_f32_e32 v13, v6, v7
	v_pk_mul_f32 v[6:7], v[98:99], v[20:21]
	v_pk_mul_f32 v[4:5], v[100:101], v[4:5]
	v_add_f32_e32 v6, v7, v6
	v_sub_f32_e32 v7, v4, v5
	v_pk_mul_f32 v[4:5], v[100:101], v[8:9]
	v_add_f32_e32 v8, v5, v4
	v_cvt_pk_fp8_f32 v3, v25, v26
	v_cvt_pk_fp8_f32 v4, v15, v12
	v_cvt_pk_fp8_f32 v5, v13, v6
	v_cvt_pk_fp8_f32 v2, v23, v24 op_sel:[0,0,1]
	v_cvt_pk_fp8_f32 v3, v27, v28 op_sel:[0,0,1]
	v_cvt_pk_fp8_f32 v4, v10, v11 op_sel:[0,0,1]
	v_cvt_pk_fp8_f32 v5, v7, v8 op_sel:[0,0,1]
	v_add_u32_e32 v98, s8, v14
	v_mov_b32_e32 v99, v0
	v_lshl_add_u64 v[6:7], v[178:179], 0, v[98:99]
	v_lshl_add_u64 v[8:9], v[6:7], 0, s[20:21]
	v_lshl_add_u64 v[8:9], v[8:9], 0, -8
	v_permlane16_swap_b32_e32 v2, v4
	v_permlane16_swap_b32_e32 v3, v5
	v_cndmask_b32_e64 v7, v9, v7, s[0:1]
	v_cndmask_b32_e64 v6, v8, v6, s[0:1]
	global_store_dwordx4 v[6:7], v[2:5], off
	s_mul_i32 s9, s85, 0x50
	s_nop 0
	v_ashrrev_i32_e32 v2, 6, v206
	v_add_u32_e32 v2, s22, v2
	v_cndmask_b32_e64 v2, v188, v2, s[4:5]
	v_lshlrev_b32_e32 v2, 4, v2
	v_ashrrev_i32_e32 v3, 31, v2
	v_lshlrev_b64 v[2:3], 2, v[2:3]
	v_lshl_add_u64 v[4:5], v[174:175], 0, v[2:3]
	v_lshl_add_u64 v[2:3], v[176:177], 0, v[2:3]
	global_load_dwordx4 v[18:21], v[4:5], off
	global_load_dwordx4 v[22:25], v[2:3], off
	v_ashrrev_i32_e32 v2, 6, v205
	v_add_u32_e32 v2, s22, v2
	v_cndmask_b32_e64 v2, v187, v2, s[4:5]
	v_lshlrev_b32_e32 v2, 4, v2
	v_ashrrev_i32_e32 v3, 31, v2
	v_lshlrev_b64 v[2:3], 2, v[2:3]
	v_lshl_add_u64 v[4:5], v[174:175], 0, v[2:3]
	v_lshl_add_u64 v[2:3], v[176:177], 0, v[2:3]
	global_load_dwordx4 v[26:29], v[4:5], off
	global_load_dwordx4 v[30:33], v[2:3], off
	v_ashrrev_i32_e32 v2, 6, v204
	v_add_u32_e32 v2, s22, v2
	v_cndmask_b32_e64 v2, v186, v2, s[4:5]
	v_lshlrev_b32_e32 v2, 4, v2
	v_ashrrev_i32_e32 v3, 31, v2
	v_lshlrev_b64 v[2:3], 2, v[2:3]
	v_lshl_add_u64 v[4:5], v[174:175], 0, v[2:3]
	v_lshl_add_u64 v[2:3], v[176:177], 0, v[2:3]
	global_load_dwordx4 v[10:13], v[4:5], off
	global_load_dwordx4 v[14:17], v[2:3], off
	v_ashrrev_i32_e32 v2, 6, v189
	v_add_u32_e32 v2, s22, v2
	v_cndmask_b32_e64 v2, v183, v2, s[4:5]
	v_lshlrev_b32_e32 v2, 4, v2
	v_ashrrev_i32_e32 v3, 31, v2
	v_lshlrev_b64 v[6:7], 2, v[2:3]
	v_lshl_add_u64 v[2:3], v[174:175], 0, v[6:7]
	v_lshl_add_u64 v[6:7], v[176:177], 0, v[6:7]
	global_load_dwordx4 v[2:5], v[2:3], off
	s_waitcnt vmcnt(6)
	v_pk_mul_f32 v[100:101], v[180:181], v[18:19] op_sel_hi:[0,1]
	global_load_dwordx4 v[6:9], v[6:7], off
	s_waitcnt vmcnt(6)
	v_pk_mul_f32 v[22:23], v[180:181], v[22:23] op_sel_hi:[0,1]
	v_mov_b32_e32 v102, v100
	v_mov_b32_e32 v103, v22
	v_pk_mul_f32 v[18:19], v[94:95], v[102:103]
	v_mov_b32_e32 v104, v22
	v_mov_b32_e32 v105, v100
	v_sub_f32_e32 v99, v18, v19
	v_pk_mul_f32 v[18:19], v[94:95], v[104:105]
	v_mov_b32_e32 v22, v101
	v_pk_mul_f32 v[20:21], v[180:181], v[20:21] op_sel_hi:[0,1]
	v_pk_mul_f32 v[24:25], v[180:181], v[24:25] op_sel_hi:[0,1]
	v_add_f32_e32 v106, v19, v18
	v_pk_mul_f32 v[18:19], v[96:97], v[22:23]
	v_mov_b32_e32 v100, v23
	v_sub_f32_e32 v107, v18, v19
	v_pk_mul_f32 v[18:19], v[96:97], v[100:101]
	v_mov_b32_e32 v94, v20
	v_mov_b32_e32 v95, v24
	v_add_f32_e32 v108, v19, v18
	v_pk_mul_f32 v[18:19], v[90:91], v[94:95]
	v_mov_b32_e32 v96, v24
	v_mov_b32_e32 v97, v20
	v_sub_f32_e32 v109, v18, v19
	v_pk_mul_f32 v[18:19], v[90:91], v[96:97]
	v_mov_b32_e32 v24, v21
	v_add_f32_e32 v90, v19, v18
	v_pk_mul_f32 v[18:19], v[92:93], v[24:25]
	v_mov_b32_e32 v20, v25
	v_sub_f32_e32 v91, v18, v19
	v_pk_mul_f32 v[18:19], v[92:93], v[20:21]
	v_pk_mul_f32 v[22:23], v[88:89], v[22:23]
	v_add_f32_e32 v92, v19, v18
	v_cvt_pk_fp8_f32 v19, v109, v90
	v_pk_mul_f32 v[20:21], v[84:85], v[20:21]
	v_cvt_pk_fp8_f32 v18, v99, v106
	v_cvt_pk_fp8_f32 v19, v91, v92 op_sel:[0,0,1]
	v_pk_mul_f32 v[90:91], v[86:87], v[102:103]
	v_pk_mul_f32 v[86:87], v[86:87], v[104:105]
	v_sub_f32_e32 v90, v90, v91
	v_add_f32_e32 v86, v87, v86
	v_sub_f32_e32 v87, v22, v23
	v_pk_mul_f32 v[22:23], v[88:89], v[100:101]
	v_cvt_pk_fp8_f32 v18, v107, v108 op_sel:[0,0,1]
	v_add_f32_e32 v88, v23, v22
	v_pk_mul_f32 v[22:23], v[82:83], v[94:95]
	s_waitcnt vmcnt(2)
	v_pk_mul_f32 v[14:15], v[180:181], v[14:15] op_sel_hi:[0,1]
	v_sub_f32_e32 v89, v22, v23
	v_pk_mul_f32 v[22:23], v[82:83], v[96:97]
	v_pk_mul_f32 v[12:13], v[180:181], v[12:13] op_sel_hi:[0,1]
	v_add_f32_e32 v82, v23, v22
	v_pk_mul_f32 v[22:23], v[84:85], v[24:25]
	v_pk_mul_f32 v[16:17], v[180:181], v[16:17] op_sel_hi:[0,1]
	v_sub_f32_e32 v22, v22, v23
	v_add_f32_e32 v23, v21, v20
	v_cvt_pk_fp8_f32 v20, v90, v86
	v_cvt_pk_fp8_f32 v21, v89, v82
	s_waitcnt vmcnt(1)
	v_pk_mul_f32 v[4:5], v[180:181], v[4:5] op_sel_hi:[0,1]
	v_cvt_pk_fp8_f32 v20, v87, v88 op_sel:[0,0,1]
	v_cvt_pk_fp8_f32 v21, v22, v23 op_sel:[0,0,1]
	v_add_u32_e32 v22, s9, v98
	v_mov_b32_e32 v23, v0
	v_lshl_add_u64 v[24:25], v[178:179], 0, v[22:23]
	v_lshl_add_u64 v[82:83], v[24:25], 0, s[20:21]
	v_lshl_add_u64 v[82:83], v[82:83], 0, -8
	v_permlane16_swap_b32_e32 v18, v20
	v_permlane16_swap_b32_e32 v19, v21
	v_cndmask_b32_e64 v25, v83, v25, s[0:1]
	v_cndmask_b32_e64 v24, v82, v24, s[0:1]
	global_store_dwordx4 v[24:25], v[18:21], off
	v_pk_mul_f32 v[24:25], v[180:181], v[26:27] op_sel_hi:[0,1]
	v_pk_mul_f32 v[26:27], v[180:181], v[32:33] op_sel_hi:[0,1]
	v_pk_mul_f32 v[20:21], v[180:181], v[28:29] op_sel_hi:[0,1]
	v_pk_mul_f32 v[28:29], v[180:181], v[30:31] op_sel_hi:[0,1]
	v_mov_b32_e32 v30, v24
	v_mov_b32_e32 v31, v28
	v_pk_mul_f32 v[18:19], v[78:79], v[30:31]
	v_mov_b32_e32 v32, v28
	v_mov_b32_e32 v33, v24
	v_sub_f32_e32 v23, v18, v19
	v_pk_mul_f32 v[18:19], v[78:79], v[32:33]
	v_mov_b32_e32 v28, v25
	v_add_f32_e32 v82, v19, v18
	v_pk_mul_f32 v[18:19], v[80:81], v[28:29]
	v_mov_b32_e32 v24, v29
	v_sub_f32_e32 v83, v18, v19
	v_pk_mul_f32 v[18:19], v[80:81], v[24:25]
	v_mov_b32_e32 v78, v20
	v_mov_b32_e32 v79, v26
	v_add_f32_e32 v84, v19, v18
	v_pk_mul_f32 v[18:19], v[74:75], v[78:79]
	v_mov_b32_e32 v80, v26
	v_mov_b32_e32 v81, v20
	v_sub_f32_e32 v85, v18, v19
	v_pk_mul_f32 v[18:19], v[74:75], v[80:81]
	v_mov_b32_e32 v26, v21
	v_add_f32_e32 v74, v19, v18
	v_pk_mul_f32 v[18:19], v[76:77], v[26:27]
	v_mov_b32_e32 v20, v27
	v_sub_f32_e32 v75, v18, v19
	v_pk_mul_f32 v[18:19], v[76:77], v[20:21]
	v_pk_mul_f32 v[30:31], v[70:71], v[30:31]
	v_add_f32_e32 v76, v19, v18
	v_pk_mul_f32 v[28:29], v[72:73], v[28:29]
	v_pk_mul_f32 v[24:25], v[72:73], v[24:25]
	v_cvt_pk_fp8_f32 v18, v23, v82
	v_sub_f32_e32 v23, v30, v31
	v_pk_mul_f32 v[30:31], v[70:71], v[32:33]
	v_sub_f32_e32 v28, v28, v29
	v_add_f32_e32 v29, v25, v24
	v_pk_mul_f32 v[24:25], v[66:67], v[78:79]
	v_add_f32_e32 v30, v31, v30
	v_sub_f32_e32 v31, v24, v25
	v_pk_mul_f32 v[24:25], v[66:67], v[80:81]
	v_pk_mul_f32 v[20:21], v[68:69], v[20:21]
	v_add_f32_e32 v32, v25, v24
	v_pk_mul_f32 v[24:25], v[68:69], v[26:27]
	v_sub_f32_e32 v24, v24, v25
	v_add_f32_e32 v25, v21, v20
	v_cvt_pk_fp8_f32 v19, v85, v74
	v_cvt_pk_fp8_f32 v20, v23, v30
	v_cvt_pk_fp8_f32 v21, v31, v32
	v_cvt_pk_fp8_f32 v18, v83, v84 op_sel:[0,0,1]
	v_cvt_pk_fp8_f32 v19, v75, v76 op_sel:[0,0,1]
	v_cvt_pk_fp8_f32 v20, v28, v29 op_sel:[0,0,1]
	v_cvt_pk_fp8_f32 v21, v24, v25 op_sel:[0,0,1]
	v_add_u32_e32 v22, s8, v22
	v_mov_b32_e32 v23, v0
	v_lshl_add_u64 v[24:25], v[178:179], 0, v[22:23]
	v_lshl_add_u64 v[26:27], v[24:25], 0, s[20:21]
	v_lshl_add_u64 v[26:27], v[26:27], 0, -8
	v_permlane16_swap_b32_e32 v18, v20
	v_permlane16_swap_b32_e32 v19, v21
	v_cndmask_b32_e64 v25, v27, v25, s[0:1]
	v_cndmask_b32_e64 v24, v26, v24, s[0:1]
	global_store_dwordx4 v[24:25], v[18:21], off
	v_mov_b32_e32 v24, v14
	v_mov_b32_e32 v26, v12
	v_pk_mul_f32 v[18:19], v[180:181], v[10:11] op_sel_hi:[0,1]
	v_mov_b32_e32 v20, v18
	v_mov_b32_e32 v21, v14
	v_pk_mul_f32 v[10:11], v[54:55], v[20:21]
	v_mov_b32_e32 v25, v18
	v_sub_f32_e32 v23, v10, v11
	v_pk_mul_f32 v[10:11], v[54:55], v[24:25]
	v_mov_b32_e32 v14, v19
	v_add_f32_e32 v30, v11, v10
	v_pk_mul_f32 v[10:11], v[56:57], v[14:15]
	v_mov_b32_e32 v18, v15
	v_sub_f32_e32 v31, v10, v11
	v_pk_mul_f32 v[10:11], v[56:57], v[18:19]
	v_mov_b32_e32 v27, v16
	v_add_f32_e32 v32, v11, v10
	v_pk_mul_f32 v[10:11], v[50:51], v[26:27]
	v_mov_b32_e32 v28, v16
	v_mov_b32_e32 v29, v12
	v_sub_f32_e32 v33, v10, v11
	v_pk_mul_f32 v[10:11], v[50:51], v[28:29]
	v_mov_b32_e32 v16, v13
	v_add_f32_e32 v50, v11, v10
	v_pk_mul_f32 v[10:11], v[52:53], v[16:17]
	v_mov_b32_e32 v12, v17
	v_sub_f32_e32 v51, v10, v11
	v_pk_mul_f32 v[10:11], v[52:53], v[12:13]
	v_pk_mul_f32 v[20:21], v[62:63], v[20:21]
	v_add_f32_e32 v52, v11, v10
	v_cvt_pk_fp8_f32 v10, v23, v30
	v_sub_f32_e32 v23, v20, v21
	v_pk_mul_f32 v[20:21], v[62:63], v[24:25]
	v_pk_mul_f32 v[14:15], v[64:65], v[14:15]
	v_add_f32_e32 v20, v21, v20
	v_sub_f32_e32 v21, v14, v15
	v_pk_mul_f32 v[14:15], v[64:65], v[18:19]
	v_pk_mul_f32 v[12:13], v[60:61], v[12:13]
	v_add_f32_e32 v18, v15, v14
	v_pk_mul_f32 v[14:15], v[58:59], v[26:27]
	v_sub_f32_e32 v19, v14, v15
	v_pk_mul_f32 v[14:15], v[58:59], v[28:29]
	v_cvt_pk_fp8_f32 v11, v33, v50
	v_add_f32_e32 v24, v15, v14
	v_pk_mul_f32 v[14:15], v[60:61], v[16:17]
	v_cvt_pk_fp8_f32 v10, v31, v32 op_sel:[0,0,1]
	v_sub_f32_e32 v14, v14, v15
	v_add_f32_e32 v15, v13, v12
	v_cvt_pk_fp8_f32 v12, v23, v20
	v_cvt_pk_fp8_f32 v13, v19, v24
	v_cvt_pk_fp8_f32 v11, v51, v52 op_sel:[0,0,1]
	s_waitcnt vmcnt(2)
	v_pk_mul_f32 v[6:7], v[180:181], v[6:7] op_sel_hi:[0,1]
	v_cvt_pk_fp8_f32 v12, v21, v18 op_sel:[0,0,1]
	v_cvt_pk_fp8_f32 v13, v14, v15 op_sel:[0,0,1]
	v_add_u32_e32 v14, s8, v22
	v_mov_b32_e32 v15, v0
	v_lshl_add_u64 v[16:17], v[178:179], 0, v[14:15]
	v_lshl_add_u64 v[18:19], v[16:17], 0, s[20:21]
	v_lshl_add_u64 v[18:19], v[18:19], 0, -8
	v_permlane16_swap_b32_e32 v10, v12
	v_permlane16_swap_b32_e32 v11, v13
	v_cndmask_b32_e64 v17, v19, v17, s[0:1]
	v_cndmask_b32_e64 v16, v18, v16, s[0:1]
	global_store_dwordx4 v[16:17], v[10:13], off
	v_mov_b32_e32 v16, v6
	v_pk_mul_f32 v[8:9], v[180:181], v[8:9] op_sel_hi:[0,1]
	v_pk_mul_f32 v[10:11], v[180:181], v[2:3] op_sel_hi:[0,1]
	v_mov_b32_e32 v12, v10
	v_mov_b32_e32 v13, v6
	v_pk_mul_f32 v[2:3], v[38:39], v[12:13]
	v_mov_b32_e32 v17, v10
	v_sub_f32_e32 v15, v2, v3
	v_pk_mul_f32 v[2:3], v[38:39], v[16:17]
	v_mov_b32_e32 v6, v11
	v_add_f32_e32 v22, v3, v2
	v_pk_mul_f32 v[2:3], v[40:41], v[6:7]
	v_mov_b32_e32 v10, v7
	v_sub_f32_e32 v23, v2, v3
	v_pk_mul_f32 v[2:3], v[40:41], v[10:11]
	v_mov_b32_e32 v18, v4
	v_mov_b32_e32 v19, v8
	v_add_f32_e32 v24, v3, v2
	v_pk_mul_f32 v[2:3], v[34:35], v[18:19]
	v_mov_b32_e32 v20, v8
	v_mov_b32_e32 v21, v4
	v_sub_f32_e32 v25, v2, v3
	v_pk_mul_f32 v[2:3], v[34:35], v[20:21]
	v_mov_b32_e32 v8, v5
	v_add_f32_e32 v26, v3, v2
	v_pk_mul_f32 v[2:3], v[36:37], v[8:9]
	v_mov_b32_e32 v4, v9
	v_sub_f32_e32 v27, v2, v3
	v_pk_mul_f32 v[2:3], v[36:37], v[4:5]
	v_pk_mul_f32 v[12:13], v[46:47], v[12:13]
	v_add_f32_e32 v28, v3, v2
	v_cvt_pk_fp8_f32 v2, v15, v22
	v_sub_f32_e32 v15, v12, v13
	v_pk_mul_f32 v[12:13], v[46:47], v[16:17]
	v_pk_mul_f32 v[6:7], v[48:49], v[6:7]
	v_add_f32_e32 v12, v13, v12
	v_sub_f32_e32 v13, v6, v7
	v_pk_mul_f32 v[6:7], v[48:49], v[10:11]
	v_pk_mul_f32 v[4:5], v[44:45], v[4:5]
	v_add_f32_e32 v10, v7, v6
	v_pk_mul_f32 v[6:7], v[42:43], v[18:19]
	v_sub_f32_e32 v11, v6, v7
	v_pk_mul_f32 v[6:7], v[42:43], v[20:21]
	v_cvt_pk_fp8_f32 v3, v25, v26
	v_add_f32_e32 v16, v7, v6
	v_pk_mul_f32 v[6:7], v[44:45], v[8:9]
	v_cvt_pk_fp8_f32 v2, v23, v24 op_sel:[0,0,1]
	v_sub_f32_e32 v6, v6, v7
	v_add_f32_e32 v7, v5, v4
	v_cvt_pk_fp8_f32 v4, v15, v12
	v_cvt_pk_fp8_f32 v5, v11, v16
	v_cvt_pk_fp8_f32 v3, v27, v28 op_sel:[0,0,1]
	v_cvt_pk_fp8_f32 v4, v13, v10 op_sel:[0,0,1]
	v_cvt_pk_fp8_f32 v5, v6, v7 op_sel:[0,0,1]
	v_add_u32_e32 v6, s8, v14
	v_mov_b32_e32 v7, v0
	v_lshl_add_u64 v[6:7], v[178:179], 0, v[6:7]
	v_lshl_add_u64 v[8:9], v[6:7], 0, s[20:21]
	v_lshl_add_u64 v[8:9], v[8:9], 0, -8
	v_permlane16_swap_b32_e32 v2, v4
	v_permlane16_swap_b32_e32 v3, v5
	v_cndmask_b32_e64 v7, v9, v7, s[0:1]
	v_cndmask_b32_e64 v6, v8, v6, s[0:1]
	global_store_dwordx4 v[6:7], v[2:5], off

.LBB0_482:
	s_or_b64 exec, exec, s[4:5]
	v_cmp_gt_u32_e32 vcc, s71, v3
	s_waitcnt lgkmcnt(0)
	s_barrier
	s_and_saveexec_b64 s[4:5], vcc
	s_cbranch_execz .LBB0_419
	v_and_b32_e32 v126, 31, v2
	v_lshrrev_b32_e32 v2, 1, v2
	v_and_b32_e32 v116, 16, v2
	global_load_dwordx4 v[112:115], v116, s[0:1]
	global_load_dwordx4 v[108:111], v116, s[0:1] offset:32
	global_load_dwordx4 v[104:107], v116, s[0:1] offset:64
	global_load_dwordx4 v[100:103], v116, s[0:1] offset:96
	global_load_dwordx4 v[96:99], v116, s[0:1] offset:128
	global_load_dwordx4 v[92:95], v116, s[0:1] offset:160
	global_load_dwordx4 v[88:91], v116, s[0:1] offset:192
	global_load_dwordx4 v[84:87], v116, s[0:1] offset:224
	global_load_dwordx4 v[80:83], v116, s[0:1] offset:256
	global_load_dwordx4 v[10:13], v116, s[0:1] offset:288
	ds_read2st64_b32 v[118:119], v14 offset1:1
	v_lshrrev_b32_e32 v117, 6, v3
	global_load_dwordx4 v[6:9], v116, s[0:1] offset:320
	global_load_dwordx4 v[2:5], v116, s[0:1] offset:352
	ds_read2st64_b32 v[120:121], v14 offset0:2 offset1:3
	ds_read2st64_b32 v[122:123], v14 offset0:4 offset1:5
	ds_read2st64_b32 v[124:125], v14 offset0:6 offset1:7
	s_waitcnt lgkmcnt(3)
	v_fma_f32 v119, v65, v1, -v119
	v_fma_f32 v118, v64, v1, -v118
	v_mul_f32_e32 v127, v119, v119
	v_fmac_f32_e32 v127, v118, v118
	s_waitcnt lgkmcnt(2)
	v_fma_f32 v120, v66, v1, -v120
	v_fmac_f32_e32 v127, v120, v120
	v_fma_f32 v121, v67, v1, -v121
	ds_read2st64_b32 v[64:65], v14 offset0:8 offset1:9
	v_fmac_f32_e32 v127, v121, v121
	s_waitcnt lgkmcnt(2)
	v_fma_f32 v122, v68, v1, -v122
	v_fmac_f32_e32 v127, v122, v122
	v_fma_f32 v123, v69, v1, -v123
	v_fmac_f32_e32 v127, v123, v123
	s_waitcnt lgkmcnt(1)
	v_fma_f32 v124, v70, v1, -v124
	v_fmac_f32_e32 v127, v124, v124
	v_fma_f32 v125, v71, v1, -v125
	ds_read2st64_b32 v[66:67], v14 offset0:10 offset1:11
	ds_read2st64_b32 v[68:69], v14 offset0:12 offset1:13
	ds_read2st64_b32 v[70:71], v14 offset0:14 offset1:15
	v_fmac_f32_e32 v127, v125, v125
	s_waitcnt lgkmcnt(3)
	v_fma_f32 v72, v72, v1, -v64
	v_fmac_f32_e32 v127, v72, v72
	v_fma_f32 v73, v73, v1, -v65
	v_fmac_f32_e32 v127, v73, v73
	s_waitcnt lgkmcnt(2)
	v_fma_f32 v74, v74, v1, -v66
	v_fmac_f32_e32 v127, v74, v74
	v_fma_f32 v75, v75, v1, -v67
	ds_read2st64_b32 v[64:65], v14 offset0:16 offset1:17
	v_fmac_f32_e32 v127, v75, v75
	s_waitcnt lgkmcnt(2)
	v_fma_f32 v76, v76, v1, -v68
	v_fmac_f32_e32 v127, v76, v76
	v_fma_f32 v77, v77, v1, -v69
	v_fmac_f32_e32 v127, v77, v77
	s_waitcnt lgkmcnt(1)
	v_fma_f32 v78, v78, v1, -v70
	v_fmac_f32_e32 v127, v78, v78
	v_fma_f32 v79, v79, v1, -v71
	ds_read2st64_b32 v[66:67], v14 offset0:18 offset1:19
	ds_read2st64_b32 v[68:69], v14 offset0:20 offset1:21
	ds_read2st64_b32 v[70:71], v14 offset0:22 offset1:23
	v_fmac_f32_e32 v127, v79, v79
	s_waitcnt lgkmcnt(3)
	v_fma_f32 v64, v48, v1, -v64
	v_fmac_f32_e32 v127, v64, v64
	v_fma_f32 v65, v49, v1, -v65
	v_fmac_f32_e32 v127, v65, v65
	s_waitcnt lgkmcnt(2)
	v_fma_f32 v66, v50, v1, -v66
	v_fmac_f32_e32 v127, v66, v66
	v_fma_f32 v67, v51, v1, -v67
	ds_read2st64_b32 v[48:49], v14 offset0:24 offset1:25
	v_fmac_f32_e32 v127, v67, v67
	s_waitcnt lgkmcnt(2)
	v_fma_f32 v68, v52, v1, -v68
	v_fmac_f32_e32 v127, v68, v68
	v_fma_f32 v69, v53, v1, -v69
	v_fmac_f32_e32 v127, v69, v69
	s_waitcnt lgkmcnt(1)
	v_fma_f32 v70, v54, v1, -v70
	v_fmac_f32_e32 v127, v70, v70
	v_fma_f32 v71, v55, v1, -v71
	ds_read2st64_b32 v[50:51], v14 offset0:26 offset1:27
	ds_read2st64_b32 v[52:53], v14 offset0:28 offset1:29
	ds_read2st64_b32 v[54:55], v14 offset0:30 offset1:31
	v_fmac_f32_e32 v127, v71, v71
	s_waitcnt lgkmcnt(3)
	v_fma_f32 v56, v56, v1, -v48
	v_fmac_f32_e32 v127, v56, v56
	v_fma_f32 v57, v57, v1, -v49
	v_fmac_f32_e32 v127, v57, v57
	s_waitcnt lgkmcnt(2)
	v_fma_f32 v58, v58, v1, -v50
	v_fmac_f32_e32 v127, v58, v58
	v_fma_f32 v59, v59, v1, -v51
	ds_read2st64_b32 v[48:49], v14 offset0:32 offset1:33
	v_fmac_f32_e32 v127, v59, v59
	s_waitcnt lgkmcnt(2)
	v_fma_f32 v60, v60, v1, -v52
	v_fmac_f32_e32 v127, v60, v60
	v_fma_f32 v61, v61, v1, -v53
	v_fmac_f32_e32 v127, v61, v61
	s_waitcnt lgkmcnt(1)
	v_fma_f32 v62, v62, v1, -v54
	v_fmac_f32_e32 v127, v62, v62
	v_fma_f32 v63, v63, v1, -v55
	ds_read2st64_b32 v[50:51], v14 offset0:34 offset1:35
	ds_read2st64_b32 v[52:53], v14 offset0:36 offset1:37
	ds_read2st64_b32 v[54:55], v14 offset0:38 offset1:39
	v_fmac_f32_e32 v127, v63, v63
	s_waitcnt lgkmcnt(3)
	v_fma_f32 v48, v32, v1, -v48
	v_fmac_f32_e32 v127, v48, v48
	v_fma_f32 v49, v33, v1, -v49
	v_fmac_f32_e32 v127, v49, v49
	s_waitcnt lgkmcnt(2)
	v_fma_f32 v50, v34, v1, -v50
	v_fmac_f32_e32 v127, v50, v50
	v_fma_f32 v51, v35, v1, -v51
	ds_read2st64_b32 v[32:33], v14 offset0:40 offset1:41
	v_fmac_f32_e32 v127, v51, v51
	s_waitcnt lgkmcnt(2)
	v_fma_f32 v52, v36, v1, -v52
	v_fmac_f32_e32 v127, v52, v52
	v_fma_f32 v53, v37, v1, -v53
	v_fmac_f32_e32 v127, v53, v53
	s_waitcnt lgkmcnt(1)
	v_fma_f32 v54, v38, v1, -v54
	v_fmac_f32_e32 v127, v54, v54
	v_fma_f32 v55, v39, v1, -v55
	ds_read2st64_b32 v[34:35], v14 offset0:42 offset1:43
	ds_read2st64_b32 v[36:37], v14 offset0:44 offset1:45
	ds_read2st64_b32 v[38:39], v14 offset0:46 offset1:47
	v_fmac_f32_e32 v127, v55, v55
	s_waitcnt lgkmcnt(3)
	v_fma_f32 v40, v40, v1, -v32
	v_fmac_f32_e32 v127, v40, v40
	v_fma_f32 v41, v41, v1, -v33
	v_fmac_f32_e32 v127, v41, v41
	s_waitcnt lgkmcnt(2)
	v_fma_f32 v42, v42, v1, -v34
	v_fmac_f32_e32 v127, v42, v42
	v_fma_f32 v43, v43, v1, -v35
	ds_read2st64_b32 v[32:33], v14 offset0:48 offset1:49
	v_fmac_f32_e32 v127, v43, v43
	s_waitcnt lgkmcnt(2)
	v_fma_f32 v44, v44, v1, -v36
	v_fmac_f32_e32 v127, v44, v44
	v_fma_f32 v45, v45, v1, -v37
	v_fmac_f32_e32 v127, v45, v45
	s_waitcnt lgkmcnt(1)
	v_fma_f32 v46, v46, v1, -v38
	v_fmac_f32_e32 v127, v46, v46
	v_fma_f32 v47, v47, v1, -v39
	ds_read2st64_b32 v[34:35], v14 offset0:50 offset1:51
	ds_read2st64_b32 v[36:37], v14 offset0:52 offset1:53
	ds_read2st64_b32 v[38:39], v14 offset0:54 offset1:55
	v_fmac_f32_e32 v127, v47, v47
	s_waitcnt lgkmcnt(3)
	v_fma_f32 v128, v16, v1, -v32
	v_fmac_f32_e32 v127, v128, v128
	v_fma_f32 v129, v17, v1, -v33
	v_fmac_f32_e32 v127, v129, v129
	s_waitcnt lgkmcnt(2)
	v_fma_f32 v130, v18, v1, -v34
	v_fmac_f32_e32 v127, v130, v130
	v_fma_f32 v131, v19, v1, -v35
	ds_read2st64_b32 v[16:17], v14 offset0:56 offset1:57
	v_fmac_f32_e32 v127, v131, v131
	s_waitcnt lgkmcnt(2)
	v_fma_f32 v36, v20, v1, -v36
	v_fmac_f32_e32 v127, v36, v36
	v_fma_f32 v37, v21, v1, -v37
	v_fmac_f32_e32 v127, v37, v37
	s_waitcnt lgkmcnt(1)
	v_fma_f32 v38, v22, v1, -v38
	v_fmac_f32_e32 v127, v38, v38
	v_fma_f32 v39, v23, v1, -v39
	ds_read2st64_b32 v[18:19], v14 offset0:58 offset1:59
	ds_read2st64_b32 v[20:21], v14 offset0:60 offset1:61
	ds_read2st64_b32 v[14:15], v14 offset0:62 offset1:63
	v_fmac_f32_e32 v127, v39, v39
	s_waitcnt lgkmcnt(3)
	v_fma_f32 v132, v24, v1, -v16
	v_fmac_f32_e32 v127, v132, v132
	v_fma_f32 v133, v25, v1, -v17
	v_fmac_f32_e32 v127, v133, v133
	s_waitcnt lgkmcnt(2)
	v_fma_f32 v134, v26, v1, -v18
	v_fmac_f32_e32 v127, v134, v134
	v_fma_f32 v135, v27, v1, -v19
	v_fmac_f32_e32 v127, v135, v135
	s_waitcnt lgkmcnt(1)
	v_fma_f32 v136, v28, v1, -v20
	v_fmac_f32_e32 v127, v136, v136
	v_fma_f32 v137, v29, v1, -v21
	v_fmac_f32_e32 v127, v137, v137
	s_waitcnt lgkmcnt(0)
	v_fma_f32 v138, v30, v1, -v14
	v_fmac_f32_e32 v127, v138, v138
	v_fma_f32 v1, v31, v1, -v15
	v_fmac_f32_e32 v127, v1, v1
	v_mov_b32_e32 v14, v127
	s_nop 1
	v_permlane32_swap_b32_e32 v127, v14
	v_add_f32_e32 v14, v127, v14
	v_fmamk_f32 v14, v14, 0x3c000000, v210
	v_rsq_f32_e32 v26, v14
	global_load_dwordx4 v[28:31], v116, s[0:1] offset:384
	global_load_dwordx4 v[22:25], v116, s[0:1] offset:416
	global_load_dwordx4 v[18:21], v116, s[0:1] offset:448
	global_load_dwordx4 v[14:17], v116, s[0:1] offset:480
	v_mul_f32_e32 v32, v205, v26
	v_lshlrev_b32_e32 v26, 5, v117
	v_add3_u32 v26, v126, s16, v26
	v_ashrrev_i32_e32 v27, 31, v26
	v_lshlrev_b64 v[26:27], 10, v[26:27]
	v_lshl_add_u64 v[26:27], s[82:83], 0, v[26:27]
	v_lshl_add_u64 v[26:27], v[26:27], 0, s[24:25]
	v_mov_b32_e32 v117, v0
	v_lshl_add_u64 v[26:27], v[26:27], 0, v[116:117]
	v_mul_f32_e32 v116, 0x41800000, v32
	v_mul_f32_e32 v32, v118, v116
	s_waitcnt vmcnt(15)
	v_mul_f32_e32 v33, v112, v32
	v_mul_f32_e32 v32, v119, v116
	v_mul_f32_e32 v34, v113, v32
	v_cvt_pk_fp8_f32 v32, v33, v34
	v_mul_f32_e32 v35, v120, v116
	v_mul_f32_e32 v34, v121, v116
	v_mul_f32_e32 v33, v114, v35
	v_mul_f32_e32 v34, v115, v34
	v_cvt_pk_fp8_f32 v32, v33, v34 op_sel:[0,0,1]
	v_mul_f32_e32 v33, v122, v116
	v_mul_f32_e32 v34, v123, v116
	s_waitcnt vmcnt(14)
	v_mul_f32_e32 v33, v108, v33
	v_mul_f32_e32 v35, v109, v34
	v_cvt_pk_fp8_f32 v34, v33, v35
	v_mul_f32_e32 v108, v124, v116
	v_mul_f32_e32 v35, v125, v116
	v_mul_f32_e32 v33, v110, v108
	v_mul_f32_e32 v35, v111, v35
	v_cvt_pk_fp8_f32 v34, v33, v35 op_sel:[0,0,1]
	v_mul_f32_e32 v33, v72, v116
	s_waitcnt vmcnt(13)
	v_mul_f32_e32 v35, v104, v33
	v_mul_f32_e32 v33, v73, v116
	v_mul_f32_e32 v72, v105, v33
	v_cvt_pk_fp8_f32 v33, v35, v72
	v_mul_f32_e32 v73, v74, v116
	v_mul_f32_e32 v72, v75, v116
	v_mul_f32_e32 v35, v106, v73
	v_mul_f32_e32 v72, v107, v72
	v_cvt_pk_fp8_f32 v33, v35, v72 op_sel:[0,0,1]
	v_mul_f32_e32 v35, v76, v116
	s_waitcnt vmcnt(12)
	v_mul_f32_e32 v72, v100, v35
	v_mul_f32_e32 v35, v77, v116
	v_mul_f32_e32 v73, v101, v35
	v_cvt_pk_fp8_f32 v35, v72, v73
	v_mul_f32_e32 v74, v78, v116
	v_mul_f32_e32 v73, v79, v116
	v_mul_f32_e32 v72, v102, v74
	v_mul_f32_e32 v73, v103, v73
	v_cvt_pk_fp8_f32 v35, v72, v73 op_sel:[0,0,1]
	v_permlane32_swap_b32_e32 v32, v33
	v_mul_f32_e32 v1, v1, v116
	v_permlane32_swap_b32_e32 v34, v35
	global_store_dwordx4 v[26:27], v[32:35], off
	s_waitcnt vmcnt(1)
	v_mul_f32_e32 v1, v17, v1
	v_mul_f32_e32 v32, v64, v116
	v_mul_f32_e32 v33, v96, v32
	v_mul_f32_e32 v32, v65, v116
	v_mul_f32_e32 v34, v97, v32
	v_cvt_pk_fp8_f32 v32, v33, v34
	v_mul_f32_e32 v35, v66, v116
	v_mul_f32_e32 v34, v67, v116
	v_mul_f32_e32 v33, v98, v35
	v_mul_f32_e32 v34, v99, v34
	v_cvt_pk_fp8_f32 v32, v33, v34 op_sel:[0,0,1]
	v_mul_f32_e32 v33, v68, v116
	v_mul_f32_e32 v34, v69, v116
	v_mul_f32_e32 v33, v92, v33
	v_mul_f32_e32 v35, v93, v34
	v_cvt_pk_fp8_f32 v34, v33, v35
	v_mul_f32_e32 v64, v70, v116
	v_mul_f32_e32 v35, v71, v116
	v_mul_f32_e32 v33, v94, v64
	v_mul_f32_e32 v35, v95, v35
	v_cvt_pk_fp8_f32 v34, v33, v35 op_sel:[0,0,1]
	v_mul_f32_e32 v33, v56, v116
	v_mul_f32_e32 v35, v88, v33
	v_mul_f32_e32 v33, v57, v116
	v_mul_f32_e32 v56, v89, v33
	v_cvt_pk_fp8_f32 v33, v35, v56
	v_mul_f32_e32 v57, v58, v116
	v_mul_f32_e32 v56, v59, v116
	v_mul_f32_e32 v35, v90, v57
	v_mul_f32_e32 v56, v91, v56
	v_cvt_pk_fp8_f32 v33, v35, v56 op_sel:[0,0,1]
	v_mul_f32_e32 v35, v60, v116
	v_mul_f32_e32 v56, v84, v35
	v_mul_f32_e32 v35, v61, v116
	v_mul_f32_e32 v57, v85, v35
	v_cvt_pk_fp8_f32 v35, v56, v57
	v_mul_f32_e32 v58, v62, v116
	v_mul_f32_e32 v57, v63, v116
	v_mul_f32_e32 v56, v86, v58
	v_mul_f32_e32 v57, v87, v57
	v_cvt_pk_fp8_f32 v35, v56, v57 op_sel:[0,0,1]
	v_permlane32_swap_b32_e32 v32, v33
	s_nop 0
	v_permlane32_swap_b32_e32 v34, v35
	global_store_dwordx4 v[26:27], v[32:35], off offset:32
	s_nop 1
	v_mul_f32_e32 v32, v48, v116
	v_mul_f32_e32 v33, v80, v32
	v_mul_f32_e32 v32, v49, v116
	v_mul_f32_e32 v34, v81, v32
	v_cvt_pk_fp8_f32 v32, v33, v34
	v_mul_f32_e32 v35, v50, v116
	v_mul_f32_e32 v34, v51, v116
	v_mul_f32_e32 v33, v82, v35
	v_mul_f32_e32 v34, v83, v34
	v_cvt_pk_fp8_f32 v32, v33, v34 op_sel:[0,0,1]
	v_mul_f32_e32 v33, v52, v116
	v_mul_f32_e32 v10, v10, v33
	v_mul_f32_e32 v33, v53, v116
	v_mul_f32_e32 v11, v11, v33
	v_cvt_pk_fp8_f32 v34, v10, v11
	v_mul_f32_e32 v33, v54, v116
	v_mul_f32_e32 v11, v55, v116
	v_mul_f32_e32 v10, v12, v33
	v_mul_f32_e32 v11, v13, v11
	v_cvt_pk_fp8_f32 v34, v10, v11 op_sel:[0,0,1]
	v_mul_f32_e32 v10, v40, v116
	v_mul_f32_e32 v6, v6, v10
	v_mul_f32_e32 v10, v41, v116
	v_mul_f32_e32 v7, v7, v10
	v_cvt_pk_fp8_f32 v33, v6, v7
	v_mul_f32_e32 v10, v42, v116
	v_mul_f32_e32 v7, v43, v116
	v_mul_f32_e32 v6, v8, v10
	v_mul_f32_e32 v7, v9, v7
	v_cvt_pk_fp8_f32 v33, v6, v7 op_sel:[0,0,1]
	v_mul_f32_e32 v6, v44, v116
	v_mul_f32_e32 v2, v2, v6
	v_mul_f32_e32 v6, v45, v116
	v_mul_f32_e32 v3, v3, v6
	v_cvt_pk_fp8_f32 v35, v2, v3
	v_mul_f32_e32 v6, v46, v116
	v_mul_f32_e32 v3, v47, v116
	v_mul_f32_e32 v2, v4, v6
	v_mul_f32_e32 v3, v5, v3
	v_cvt_pk_fp8_f32 v35, v2, v3 op_sel:[0,0,1]
	v_mul_f32_e32 v2, v128, v116
	v_mul_f32_e32 v3, v28, v2
	v_mul_f32_e32 v2, v129, v116
	v_mul_f32_e32 v4, v29, v2
	v_cvt_pk_fp8_f32 v2, v3, v4
	v_mul_f32_e32 v5, v130, v116
	v_mul_f32_e32 v4, v131, v116
	v_mul_f32_e32 v3, v30, v5
	v_mul_f32_e32 v4, v31, v4
	v_cvt_pk_fp8_f32 v2, v3, v4 op_sel:[0,0,1]
	v_mul_f32_e32 v3, v36, v116
	v_mul_f32_e32 v4, v37, v116
	v_mul_f32_e32 v3, v22, v3
	v_mul_f32_e32 v5, v23, v4
	v_cvt_pk_fp8_f32 v4, v3, v5
	v_mul_f32_e32 v6, v38, v116
	v_mul_f32_e32 v5, v39, v116
	v_mul_f32_e32 v3, v24, v6
	v_mul_f32_e32 v5, v25, v5
	v_cvt_pk_fp8_f32 v4, v3, v5 op_sel:[0,0,1]
	v_mul_f32_e32 v3, v132, v116
	v_mul_f32_e32 v5, v18, v3
	v_mul_f32_e32 v3, v133, v116
	v_mul_f32_e32 v6, v19, v3
	v_cvt_pk_fp8_f32 v3, v5, v6
	v_mul_f32_e32 v7, v134, v116
	v_mul_f32_e32 v6, v135, v116
	v_mul_f32_e32 v5, v20, v7
	v_mul_f32_e32 v6, v21, v6
	v_cvt_pk_fp8_f32 v3, v5, v6 op_sel:[0,0,1]
	v_mul_f32_e32 v5, v136, v116
	v_mul_f32_e32 v6, v14, v5
	v_mul_f32_e32 v5, v137, v116
	v_mul_f32_e32 v7, v15, v5
	v_cvt_pk_fp8_f32 v5, v6, v7
	v_mul_f32_e32 v8, v138, v116
	v_mul_f32_e32 v6, v16, v8
	v_permlane32_swap_b32_e32 v32, v33
	v_cvt_pk_fp8_f32 v5, v6, v1 op_sel:[0,0,1]
	v_permlane32_swap_b32_e32 v34, v35
	v_permlane32_swap_b32_e32 v2, v3
	v_permlane32_swap_b32_e32 v4, v5
	global_store_dwordx4 v[26:27], v[32:35], off offset:64
	global_store_dwordx4 v[26:27], v[2:5], off offset:96
	s_branch .LBB0_419

.LBB0_556:
	v_cndmask_b32_e64 v34, 0, 1, s[4:5]
	s_lshl_b32 s4, s10, 6
	v_cmp_ne_u32_e32 vcc, 1, v34
	v_or_b32_e32 v34, s4, v108
	v_lshl_add_u32 v152, v34, 7, s58
	v_add_u32_e32 v38, v152, v120
	ds_read_b128 v[34:37], v38 offset:16384
	ds_read_b128 v[50:53], v38 offset:20480
	v_add_u32_e32 v148, v152, v121
	s_waitcnt vmcnt(3) lgkmcnt(1)
	v_mfma_f32_32x32x16_bf16 v[34:49], v[34:37], v[78:81], 0
	ds_read_b128 v[144:147], v148 offset:16384
	ds_read_b128 v[148:151], v148 offset:20480
	s_waitcnt lgkmcnt(2)
	v_mfma_f32_32x32x16_bf16 v[50:65], v[50:53], v[78:81], 0
	s_waitcnt vmcnt(2) lgkmcnt(1)
	v_mfma_f32_32x32x16_bf16 v[34:49], v[144:147], v[74:77], v[34:49]
	s_waitcnt lgkmcnt(0)
	v_mfma_f32_32x32x16_bf16 v[50:65], v[148:151], v[74:77], v[50:65]
	v_add_u32_e32 v148, v152, v122
	ds_read_b128 v[144:147], v148 offset:16384
	ds_read_b128 v[148:151], v148 offset:20480
	s_waitcnt vmcnt(1) lgkmcnt(1)
	v_mfma_f32_32x32x16_bf16 v[34:49], v[144:147], v[70:73], v[34:49]
	s_waitcnt lgkmcnt(0)
	v_mfma_f32_32x32x16_bf16 v[50:65], v[148:151], v[70:73], v[50:65]
	v_add_u32_e32 v148, v152, v123
	ds_read_b128 v[144:147], v148 offset:16384
	ds_read_b128 v[148:151], v148 offset:20480
	s_waitcnt vmcnt(0) lgkmcnt(1)
	v_mfma_f32_32x32x16_bf16 v[34:49], v[144:147], v[66:69], v[34:49]
	v_or_b32_e32 v145, s4, v82
	v_sub_u32_e32 v144, v109, v145
	v_sub_u32_e32 v147, 0, v144
	v_max_i32_e32 v147, v144, v147
	v_cvt_f32_u32_e32 v147, v147
	v_or_b32_e32 v146, 32, v145
	v_cmp_gt_i32_e64 s[4:5], 0, v144
	v_sub_u32_e32 v146, v109, v146
	s_waitcnt lgkmcnt(0)
	v_mfma_f32_32x32x16_bf16 v[50:65], v[148:151], v[66:69], v[50:65]
	v_cndmask_b32_e64 v144, v101, v103, s[4:5]
	v_mul_f32_e32 v144, v144, v147
	v_sub_u32_e32 v147, 0, v146
	v_max_i32_e32 v147, v146, v147
	v_cvt_f32_u32_e32 v147, v147
	v_cmp_gt_i32_e64 s[4:5], 0, v146
	v_exp_f32_e32 v144, v144
	s_nop 0
	v_cndmask_b32_e64 v146, v101, v103, s[4:5]
	v_mul_f32_e32 v146, v146, v147
	v_exp_f32_e32 v146, v146
	v_mul_f32_e32 v144, v34, v144
	v_mul_f32_e32 v34, v50, v146
	v_xad_u32 v50, v145, -1, v109
	v_sub_u32_e32 v147, 0, v50
	v_max_i32_e32 v147, v50, v147
	v_cvt_f32_u32_e32 v147, v147
	v_or_b32_e32 v146, 33, v145
	v_cmp_gt_i32_e64 s[4:5], 0, v50
	v_sub_u32_e32 v146, v109, v146
	s_nop 0
	v_cndmask_b32_e64 v50, v101, v103, s[4:5]
	v_mul_f32_e32 v50, v50, v147
	v_sub_u32_e32 v147, 0, v146
	v_max_i32_e32 v147, v146, v147
	v_cvt_f32_u32_e32 v147, v147
	v_cmp_gt_i32_e64 s[4:5], 0, v146
	v_exp_f32_e32 v50, v50
	s_nop 0
	v_cndmask_b32_e64 v146, v101, v103, s[4:5]
	v_mul_f32_e32 v146, v146, v147
	v_exp_f32_e32 v146, v146
	v_mul_f32_e32 v50, v35, v50
	v_mul_f32_e32 v35, v51, v146
	v_or_b32_e32 v51, 2, v145
	v_sub_u32_e32 v51, v109, v51
	v_sub_u32_e32 v147, 0, v51
	v_max_i32_e32 v147, v51, v147
	v_cvt_f32_u32_e32 v147, v147
	v_or_b32_e32 v146, 34, v145
	v_cmp_gt_i32_e64 s[4:5], 0, v51
	v_sub_u32_e32 v146, v109, v146
	s_nop 0
	v_cndmask_b32_e64 v51, v101, v103, s[4:5]
	v_mul_f32_e32 v51, v51, v147
	v_sub_u32_e32 v147, 0, v146
	v_max_i32_e32 v147, v146, v147
	v_cvt_f32_u32_e32 v147, v147
	v_cmp_gt_i32_e64 s[4:5], 0, v146
	v_exp_f32_e32 v51, v51
	s_nop 0
	v_cndmask_b32_e64 v146, v101, v103, s[4:5]
	v_mul_f32_e32 v146, v146, v147
	v_exp_f32_e32 v146, v146
	v_mul_f32_e32 v51, v36, v51
	v_mul_f32_e32 v36, v52, v146
	v_or_b32_e32 v52, 3, v145
	v_sub_u32_e32 v52, v109, v52
	v_sub_u32_e32 v147, 0, v52
	v_max_i32_e32 v147, v52, v147
	v_cvt_f32_u32_e32 v147, v147
	v_or_b32_e32 v146, 35, v145
	v_cmp_gt_i32_e64 s[4:5], 0, v52
	v_sub_u32_e32 v146, v109, v146
	s_nop 0
	v_cndmask_b32_e64 v52, v101, v103, s[4:5]
	v_mul_f32_e32 v52, v52, v147
	v_sub_u32_e32 v147, 0, v146
	v_max_i32_e32 v147, v146, v147
	v_cvt_f32_u32_e32 v147, v147
	v_cmp_gt_i32_e64 s[4:5], 0, v146
	v_exp_f32_e32 v52, v52
	s_nop 0
	v_cndmask_b32_e64 v146, v101, v103, s[4:5]
	v_mul_f32_e32 v146, v146, v147
	v_exp_f32_e32 v146, v146
	v_mul_f32_e32 v52, v37, v52
	v_mul_f32_e32 v37, v53, v146
	v_or_b32_e32 v53, 8, v145
	v_sub_u32_e32 v53, v109, v53
	v_sub_u32_e32 v147, 0, v53
	v_max_i32_e32 v147, v53, v147
	v_cvt_f32_u32_e32 v147, v147
	v_or_b32_e32 v146, 40, v145
	v_cmp_gt_i32_e64 s[4:5], 0, v53
	v_sub_u32_e32 v146, v109, v146
	s_nop 0
	v_cndmask_b32_e64 v53, v101, v103, s[4:5]
	v_mul_f32_e32 v53, v53, v147
	v_sub_u32_e32 v147, 0, v146
	v_max_i32_e32 v147, v146, v147
	v_cvt_f32_u32_e32 v147, v147
	v_cmp_gt_i32_e64 s[4:5], 0, v146
	v_exp_f32_e32 v53, v53
	s_nop 0
	v_cndmask_b32_e64 v146, v101, v103, s[4:5]
	v_mul_f32_e32 v146, v146, v147
	v_exp_f32_e32 v146, v146
	v_mul_f32_e32 v53, v38, v53
	v_mul_f32_e32 v38, v54, v146
	v_or_b32_e32 v54, 9, v145
	v_sub_u32_e32 v54, v109, v54
	v_sub_u32_e32 v147, 0, v54
	v_max_i32_e32 v147, v54, v147
	v_cvt_f32_u32_e32 v147, v147
	v_or_b32_e32 v146, 41, v145
	v_cmp_gt_i32_e64 s[4:5], 0, v54
	v_sub_u32_e32 v146, v109, v146
	s_nop 0
	v_cndmask_b32_e64 v54, v101, v103, s[4:5]
	v_mul_f32_e32 v54, v54, v147
	v_sub_u32_e32 v147, 0, v146
	v_max_i32_e32 v147, v146, v147
	v_cvt_f32_u32_e32 v147, v147
	v_cmp_gt_i32_e64 s[4:5], 0, v146
	v_exp_f32_e32 v54, v54
	s_nop 0
	v_cndmask_b32_e64 v146, v101, v103, s[4:5]
	v_mul_f32_e32 v146, v146, v147
	v_exp_f32_e32 v146, v146
	v_mul_f32_e32 v54, v39, v54
	v_mul_f32_e32 v39, v55, v146
	v_or_b32_e32 v55, 10, v145
	v_sub_u32_e32 v55, v109, v55
	v_sub_u32_e32 v147, 0, v55
	v_max_i32_e32 v147, v55, v147
	v_cvt_f32_u32_e32 v147, v147
	v_or_b32_e32 v146, 42, v145
	v_cmp_gt_i32_e64 s[4:5], 0, v55
	v_sub_u32_e32 v146, v109, v146
	s_nop 0
	v_cndmask_b32_e64 v55, v101, v103, s[4:5]
	v_mul_f32_e32 v55, v55, v147
	v_sub_u32_e32 v147, 0, v146
	v_max_i32_e32 v147, v146, v147
	v_cvt_f32_u32_e32 v147, v147
	v_cmp_gt_i32_e64 s[4:5], 0, v146
	v_exp_f32_e32 v55, v55
	s_nop 0
	v_cndmask_b32_e64 v146, v101, v103, s[4:5]
	v_mul_f32_e32 v146, v146, v147
	v_exp_f32_e32 v146, v146
	v_mul_f32_e32 v55, v40, v55
	v_mul_f32_e32 v40, v56, v146
	v_or_b32_e32 v56, 11, v145
	v_sub_u32_e32 v56, v109, v56
	v_sub_u32_e32 v147, 0, v56
	v_max_i32_e32 v147, v56, v147
	v_cvt_f32_u32_e32 v147, v147
	v_or_b32_e32 v146, 43, v145
	v_cmp_gt_i32_e64 s[4:5], 0, v56
	v_sub_u32_e32 v146, v109, v146
	s_nop 0
	v_cndmask_b32_e64 v56, v101, v103, s[4:5]
	v_mul_f32_e32 v56, v56, v147
	v_sub_u32_e32 v147, 0, v146
	v_max_i32_e32 v147, v146, v147
	v_cvt_f32_u32_e32 v147, v147
	v_cmp_gt_i32_e64 s[4:5], 0, v146
	v_exp_f32_e32 v56, v56
	s_nop 0
	v_cndmask_b32_e64 v146, v101, v103, s[4:5]
	v_mul_f32_e32 v146, v146, v147
	v_exp_f32_e32 v146, v146
	v_mul_f32_e32 v56, v41, v56
	v_mul_f32_e32 v41, v57, v146
	v_or_b32_e32 v57, 16, v145
	v_sub_u32_e32 v57, v109, v57
	v_sub_u32_e32 v147, 0, v57
	v_max_i32_e32 v147, v57, v147
	v_cvt_f32_u32_e32 v147, v147
	v_or_b32_e32 v146, 48, v145
	v_cmp_gt_i32_e64 s[4:5], 0, v57
	v_sub_u32_e32 v146, v109, v146
	s_nop 0
	v_cndmask_b32_e64 v57, v101, v103, s[4:5]
	v_mul_f32_e32 v57, v57, v147
	v_sub_u32_e32 v147, 0, v146
	v_max_i32_e32 v147, v146, v147
	v_cvt_f32_u32_e32 v147, v147
	v_cmp_gt_i32_e64 s[4:5], 0, v146
	v_exp_f32_e32 v57, v57
	s_nop 0
	v_cndmask_b32_e64 v146, v101, v103, s[4:5]
	v_mul_f32_e32 v146, v146, v147
	v_exp_f32_e32 v146, v146
	v_mul_f32_e32 v57, v42, v57
	v_mul_f32_e32 v42, v58, v146
	v_or_b32_e32 v58, 17, v145
	v_sub_u32_e32 v58, v109, v58
	v_sub_u32_e32 v147, 0, v58
	v_max_i32_e32 v147, v58, v147
	v_cvt_f32_u32_e32 v147, v147
	v_or_b32_e32 v146, 49, v145
	v_cmp_gt_i32_e64 s[4:5], 0, v58
	v_sub_u32_e32 v146, v109, v146
	s_nop 0
	v_cndmask_b32_e64 v58, v101, v103, s[4:5]
	v_mul_f32_e32 v58, v58, v147
	v_sub_u32_e32 v147, 0, v146
	v_max_i32_e32 v147, v146, v147
	v_cvt_f32_u32_e32 v147, v147
	v_cmp_gt_i32_e64 s[4:5], 0, v146
	v_exp_f32_e32 v58, v58
	s_nop 0
	v_cndmask_b32_e64 v146, v101, v103, s[4:5]
	v_mul_f32_e32 v146, v146, v147
	v_exp_f32_e32 v146, v146
	v_mul_f32_e32 v43, v43, v58
	v_mul_f32_e32 v58, v59, v146
	v_or_b32_e32 v59, 18, v145
	v_sub_u32_e32 v59, v109, v59
	v_sub_u32_e32 v147, 0, v59
	v_max_i32_e32 v147, v59, v147
	v_cvt_f32_u32_e32 v147, v147
	v_or_b32_e32 v146, 50, v145
	v_cmp_gt_i32_e64 s[4:5], 0, v59
	v_sub_u32_e32 v146, v109, v146
	s_nop 0
	v_cndmask_b32_e64 v59, v101, v103, s[4:5]
	v_mul_f32_e32 v59, v59, v147
	v_sub_u32_e32 v147, 0, v146
	v_exp_f32_e32 v59, v59
	v_max_i32_e32 v147, v146, v147
	v_cvt_f32_u32_e32 v147, v147
	v_cmp_gt_i32_e64 s[4:5], 0, v146
	v_mul_f32_e32 v59, v44, v59
	v_or_b32_e32 v44, 19, v145
	v_cndmask_b32_e64 v146, v101, v103, s[4:5]
	v_mul_f32_e32 v146, v146, v147
	v_sub_u32_e32 v44, v109, v44
	v_exp_f32_e32 v146, v146
	v_sub_u32_e32 v147, 0, v44
	v_max_i32_e32 v147, v44, v147
	v_cvt_f32_u32_e32 v147, v147
	v_mul_f32_e32 v60, v60, v146
	v_or_b32_e32 v146, 51, v145
	v_cmp_gt_i32_e64 s[4:5], 0, v44
	v_sub_u32_e32 v146, v109, v146
	s_nop 0
	v_cndmask_b32_e64 v44, v101, v103, s[4:5]
	v_mul_f32_e32 v44, v44, v147
	v_sub_u32_e32 v147, 0, v146
	v_max_i32_e32 v147, v146, v147
	v_cvt_f32_u32_e32 v147, v147
	v_cmp_gt_i32_e64 s[4:5], 0, v146
	v_exp_f32_e32 v44, v44
	s_nop 0
	v_cndmask_b32_e64 v146, v101, v103, s[4:5]
	v_mul_f32_e32 v146, v146, v147
	v_exp_f32_e32 v146, v146
	v_mul_f32_e32 v147, v45, v44
	v_or_b32_e32 v44, 24, v145
	v_sub_u32_e32 v44, v109, v44
	v_mul_f32_e32 v61, v61, v146
	v_sub_u32_e32 v146, 0, v44
	v_max_i32_e32 v146, v44, v146
	v_cvt_f32_u32_e32 v146, v146
	v_or_b32_e32 v45, 56, v145
	v_cmp_gt_i32_e64 s[4:5], 0, v44
	v_sub_u32_e32 v45, v109, v45
	s_nop 0
	v_cndmask_b32_e64 v44, v101, v103, s[4:5]
	v_mul_f32_e32 v44, v44, v146
	v_sub_u32_e32 v146, 0, v45
	v_max_i32_e32 v146, v45, v146
	v_exp_f32_e32 v44, v44
	v_cvt_f32_u32_e32 v146, v146
	v_cmp_gt_i32_e64 s[4:5], 0, v45
	s_nop 1
	v_cndmask_b32_e64 v45, v101, v103, s[4:5]
	v_mul_f32_e32 v45, v45, v146
	v_mul_f32_e32 v146, v46, v44
	v_or_b32_e32 v44, 25, v145
	v_sub_u32_e32 v44, v109, v44
	v_exp_f32_e32 v45, v45
	v_sub_u32_e32 v46, 0, v44
	v_max_i32_e32 v46, v44, v46
	v_cvt_f32_u32_e32 v46, v46
	v_mul_f32_e32 v62, v62, v45
	v_or_b32_e32 v45, 57, v145
	v_cmp_gt_i32_e64 s[4:5], 0, v44
	v_sub_u32_e32 v45, v109, v45
	s_nop 0
	v_cndmask_b32_e64 v44, v101, v103, s[4:5]
	v_mul_f32_e32 v44, v44, v46
	v_sub_u32_e32 v46, 0, v45
	v_exp_f32_e32 v44, v44
	v_max_i32_e32 v46, v45, v46
	v_cvt_f32_u32_e32 v46, v46
	v_cmp_gt_i32_e64 s[4:5], 0, v45
	v_mul_f32_e32 v148, v47, v44
	v_or_b32_e32 v44, 26, v145
	v_cndmask_b32_e64 v45, v101, v103, s[4:5]
	v_mul_f32_e32 v45, v45, v46
	v_sub_u32_e32 v44, v109, v44
	v_exp_f32_e32 v45, v45
	v_sub_u32_e32 v46, 0, v44
	v_max_i32_e32 v46, v44, v46
	v_cvt_f32_u32_e32 v46, v46
	v_mul_f32_e32 v63, v63, v45
	v_or_b32_e32 v45, 58, v145
	v_cmp_gt_i32_e64 s[4:5], 0, v44
	v_sub_u32_e32 v45, v109, v45
	s_nop 0
	v_cndmask_b32_e64 v44, v101, v103, s[4:5]
	v_mul_f32_e32 v44, v44, v46
	v_sub_u32_e32 v46, 0, v45
	v_exp_f32_e32 v44, v44
	v_max_i32_e32 v46, v45, v46
	v_cvt_f32_u32_e32 v46, v46
	v_cmp_gt_i32_e64 s[4:5], 0, v45
	v_mul_f32_e32 v149, v48, v44
	v_or_b32_e32 v44, 27, v145
	v_cndmask_b32_e64 v45, v101, v103, s[4:5]
	v_mul_f32_e32 v45, v45, v46
	v_sub_u32_e32 v44, v109, v44
	v_exp_f32_e32 v45, v45
	v_sub_u32_e32 v46, 0, v44
	v_max_i32_e32 v46, v44, v46
	v_cvt_f32_u32_e32 v46, v46
	v_mul_f32_e32 v64, v64, v45
	v_or_b32_e32 v45, 59, v145
	v_cmp_gt_i32_e64 s[4:5], 0, v44
	v_sub_u32_e32 v45, v109, v45
	s_nop 0
	v_cndmask_b32_e64 v44, v101, v103, s[4:5]
	v_mul_f32_e32 v44, v44, v46
	v_sub_u32_e32 v46, 0, v45
	v_max_i32_e32 v46, v45, v46
	v_cvt_f32_u32_e32 v46, v46
	v_cmp_gt_i32_e64 s[4:5], 0, v45
	v_exp_f32_e32 v44, v44
	s_nop 0
	v_cndmask_b32_e64 v45, v101, v103, s[4:5]
	v_mul_f32_e32 v45, v45, v46
	v_exp_f32_e32 v45, v45
	v_mul_f32_e32 v145, v49, v44
	v_cvt_pk_bf16_f32 v44, v144, v50
	v_mul_f32_e32 v65, v65, v45
	v_cvt_pk_bf16_f32 v45, v51, v52
	v_cvt_pk_bf16_f32 v46, v53, v54
	v_cvt_pk_bf16_f32 v47, v55, v56
	v_cvt_pk_bf16_f32 v48, v57, v43
	v_cvt_pk_bf16_f32 v49, v59, v147
	v_cvt_pk_bf16_f32 v50, v146, v148
	v_cvt_pk_bf16_f32 v51, v149, v145
	v_cvt_pk_bf16_f32 v34, v34, v35
	v_cvt_pk_bf16_f32 v35, v36, v37
	v_cvt_pk_bf16_f32 v36, v38, v39
	v_cvt_pk_bf16_f32 v37, v40, v41
	v_cvt_pk_bf16_f32 v38, v42, v58
	v_cvt_pk_bf16_f32 v39, v60, v61
	v_cvt_pk_bf16_f32 v40, v62, v63
	v_cvt_pk_bf16_f32 v41, v64, v65
	v_lshl_add_u32 v42, s10, 13, v110
	ds_read_b64_tr_b16 v[52:53], v42 offset:0
	ds_read_b64_tr_b16 v[54:55], v42 offset:0x400
	ds_read_b64_tr_b16 v[56:57], v42 offset:0x800
	ds_read_b64_tr_b16 v[58:59], v42 offset:0xc00
	ds_read_b64_tr_b16 v[60:61], v42 offset:0x1000
	ds_read_b64_tr_b16 v[62:63], v42 offset:0x1400
	ds_read_b64_tr_b16 v[144:145], v42 offset:0x1800
	ds_read_b64_tr_b16 v[146:147], v42 offset:0x1c00
	s_waitcnt lgkmcnt(0)
	v_permlane32_swap_b32_e32 v44, v46
	v_permlane32_swap_b32_e32 v45, v47
	v_permlane32_swap_b32_e32 v48, v50
	v_permlane32_swap_b32_e32 v49, v51
	v_permlane32_swap_b32_e32 v34, v36
	v_permlane32_swap_b32_e32 v35, v37
	v_permlane32_swap_b32_e32 v38, v40
	v_permlane32_swap_b32_e32 v39, v41
	v_mfma_f32_32x32x16_bf16 v[18:33], v[52:55], v[44:47], v[18:33]
	ds_read_b64_tr_b16 v[52:53], v42 offset:0x200
	ds_read_b64_tr_b16 v[54:55], v42 offset:0x600
	v_mfma_f32_32x32x16_bf16 v[18:33], v[56:59], v[48:51], v[18:33]
	ds_read_b64_tr_b16 v[56:57], v42 offset:0xa00
	ds_read_b64_tr_b16 v[58:59], v42 offset:0xe00
	v_mfma_f32_32x32x16_bf16 v[18:33], v[60:63], v[34:37], v[18:33]
	ds_read_b64_tr_b16 v[60:61], v42 offset:0x1200
	ds_read_b64_tr_b16 v[62:63], v42 offset:0x1600
	v_mfma_f32_32x32x16_bf16 v[18:33], v[144:147], v[38:41], v[18:33]
	ds_read_b64_tr_b16 v[144:145], v42 offset:0x1a00
	ds_read_b64_tr_b16 v[146:147], v42 offset:0x1e00
	s_waitcnt lgkmcnt(0)
	v_mfma_f32_32x32x16_bf16 v[2:17], v[52:55], v[44:47], v[2:17]
	s_mov_b64 s[4:5], 0
	s_and_b64 vcc, exec, vcc
	s_mov_b32 s10, 1
	v_mfma_f32_32x32x16_bf16 v[2:17], v[56:59], v[48:51], v[2:17]
	v_mfma_f32_32x32x16_bf16 v[2:17], v[60:63], v[34:37], v[2:17]
	v_mfma_f32_32x32x16_bf16 v[2:17], v[144:147], v[38:41], v[2:17]
	s_cbranch_vccz .LBB0_556
	v_mul_f32_e32 v34, v101, v111
	v_exp_f32_e32 v50, v34
	v_mul_f32_e32 v34, v103, v112
	v_exp_f32_e32 v51, v34
	v_lshlrev_b32_e32 v35, 16, v78
	v_and_b32_e32 v36, 0xffff0000, v78
	v_mul_f32_e32 v34, v50, v35
	v_mul_f32_e32 v37, v50, v36
	v_mul_f32_e32 v36, v51, v36
	v_cvt_pk_bf16_f32 v34, v34, v37
	v_mul_f32_e32 v35, v51, v35
	v_cvt_pk_bf16_f32 v38, v35, v36
	v_lshlrev_b32_e32 v36, 16, v79
	v_and_b32_e32 v37, 0xffff0000, v79
	v_mul_f32_e32 v35, v50, v36
	v_mul_f32_e32 v39, v50, v37
	v_mul_f32_e32 v37, v51, v37
	v_cvt_pk_bf16_f32 v35, v35, v39
	v_mul_f32_e32 v36, v51, v36
	v_cvt_pk_bf16_f32 v39, v36, v37
	v_lshlrev_b32_e32 v37, 16, v80
	v_and_b32_e32 v40, 0xffff0000, v80
	v_mul_f32_e32 v36, v50, v37
	v_mul_f32_e32 v41, v50, v40
	v_cvt_pk_bf16_f32 v36, v36, v41
	v_mul_f32_e32 v37, v51, v37
	v_mul_f32_e32 v40, v51, v40
	v_lshlrev_b32_e32 v41, 16, v81
	v_and_b32_e32 v42, 0xffff0000, v81
	v_cvt_pk_bf16_f32 v40, v37, v40
	v_mul_f32_e32 v37, v50, v41
	v_mul_f32_e32 v43, v50, v42
	v_mul_f32_e32 v41, v51, v41
	v_mul_f32_e32 v42, v51, v42
	v_cvt_pk_bf16_f32 v37, v37, v43
	v_cvt_pk_bf16_f32 v41, v41, v42
	ds_read_b128 v[42:45], v134 offset:32768
	ds_read_b128 v[46:49], v134 offset:40960
	s_waitcnt lgkmcnt(1)
	v_mfma_f32_32x32x16_bf16 v[18:33], v[42:45], v[34:37], v[18:33]
	s_mov_b64 s[4:5], 0x1400
	s_waitcnt lgkmcnt(0)
	v_mfma_f32_32x32x16_bf16 v[18:33], v[46:49], v[38:41], v[18:33]
	ds_read_b128 v[42:45], v134 offset:36864
	ds_read_b128 v[46:49], v134 offset:45056
	s_waitcnt lgkmcnt(1)
	v_mfma_f32_32x32x16_bf16 v[2:17], v[42:45], v[34:37], v[2:17]
	v_lshlrev_b32_e32 v35, 16, v74
	v_and_b32_e32 v36, 0xffff0000, v74
	v_mul_f32_e32 v34, v50, v35
	v_mul_f32_e32 v37, v50, v36
	v_mul_f32_e32 v36, v51, v36
	v_cvt_pk_bf16_f32 v34, v34, v37
	v_mul_f32_e32 v35, v51, v35
	s_waitcnt lgkmcnt(0)
	v_mfma_f32_32x32x16_bf16 v[2:17], v[46:49], v[38:41], v[2:17]
	v_cvt_pk_bf16_f32 v38, v35, v36
	v_lshlrev_b32_e32 v36, 16, v75
	v_and_b32_e32 v37, 0xffff0000, v75
	v_mul_f32_e32 v35, v50, v36
	v_mul_f32_e32 v39, v50, v37
	v_mul_f32_e32 v37, v51, v37
	v_cvt_pk_bf16_f32 v35, v35, v39
	v_mul_f32_e32 v36, v51, v36
	v_cvt_pk_bf16_f32 v39, v36, v37
	v_lshlrev_b32_e32 v37, 16, v76
	v_and_b32_e32 v40, 0xffff0000, v76
	v_mul_f32_e32 v36, v50, v37
	v_mul_f32_e32 v41, v50, v40
	v_cvt_pk_bf16_f32 v36, v36, v41
	v_mul_f32_e32 v37, v51, v37
	v_mul_f32_e32 v40, v51, v40
	v_lshlrev_b32_e32 v41, 16, v77
	v_and_b32_e32 v42, 0xffff0000, v77
	v_cvt_pk_bf16_f32 v40, v37, v40
	v_mul_f32_e32 v37, v50, v41
	v_mul_f32_e32 v43, v50, v42
	v_mul_f32_e32 v41, v51, v41
	v_mul_f32_e32 v42, v51, v42
	v_cvt_pk_bf16_f32 v37, v37, v43
	v_cvt_pk_bf16_f32 v41, v41, v42
	ds_read_b128 v[42:45], v135 offset:32768
	ds_read_b128 v[46:49], v135 offset:40960
	s_waitcnt lgkmcnt(1)
	v_mfma_f32_32x32x16_bf16 v[18:33], v[42:45], v[34:37], v[18:33]
	s_waitcnt lgkmcnt(0)
	v_mfma_f32_32x32x16_bf16 v[18:33], v[46:49], v[38:41], v[18:33]
	ds_read_b128 v[42:45], v135 offset:36864
	ds_read_b128 v[46:49], v135 offset:45056
	s_waitcnt lgkmcnt(1)
	v_mfma_f32_32x32x16_bf16 v[2:17], v[42:45], v[34:37], v[2:17]
	v_lshlrev_b32_e32 v35, 16, v70
	v_and_b32_e32 v36, 0xffff0000, v70
	v_mul_f32_e32 v34, v50, v35
	v_mul_f32_e32 v37, v50, v36
	v_mul_f32_e32 v36, v51, v36
	v_cvt_pk_bf16_f32 v34, v34, v37
	v_mul_f32_e32 v35, v51, v35
	s_waitcnt lgkmcnt(0)
	v_mfma_f32_32x32x16_bf16 v[2:17], v[46:49], v[38:41], v[2:17]
	v_cvt_pk_bf16_f32 v38, v35, v36
	v_lshlrev_b32_e32 v36, 16, v71
	v_and_b32_e32 v37, 0xffff0000, v71
	v_mul_f32_e32 v35, v50, v36
	v_mul_f32_e32 v39, v50, v37
	v_mul_f32_e32 v37, v51, v37
	v_cvt_pk_bf16_f32 v35, v35, v39
	v_mul_f32_e32 v36, v51, v36
	v_cvt_pk_bf16_f32 v39, v36, v37
	v_lshlrev_b32_e32 v37, 16, v72
	v_and_b32_e32 v40, 0xffff0000, v72
	v_mul_f32_e32 v36, v50, v37
	v_mul_f32_e32 v41, v50, v40
	v_cvt_pk_bf16_f32 v36, v36, v41
	v_mul_f32_e32 v37, v51, v37
	v_mul_f32_e32 v40, v51, v40
	v_lshlrev_b32_e32 v41, 16, v73
	v_and_b32_e32 v42, 0xffff0000, v73
	v_cvt_pk_bf16_f32 v40, v37, v40
	v_mul_f32_e32 v37, v50, v41
	v_mul_f32_e32 v43, v50, v42
	v_mul_f32_e32 v41, v51, v41
	v_mul_f32_e32 v42, v51, v42
	v_cvt_pk_bf16_f32 v37, v37, v43
	v_cvt_pk_bf16_f32 v41, v41, v42
	ds_read_b128 v[42:45], v136 offset:32768
	ds_read_b128 v[46:49], v136 offset:40960
	s_waitcnt lgkmcnt(1)
	v_mfma_f32_32x32x16_bf16 v[18:33], v[42:45], v[34:37], v[18:33]
	s_waitcnt lgkmcnt(0)
	v_mfma_f32_32x32x16_bf16 v[18:33], v[46:49], v[38:41], v[18:33]
	ds_read_b128 v[42:45], v136 offset:36864
	ds_read_b128 v[46:49], v136 offset:45056
	s_waitcnt lgkmcnt(1)
	v_mfma_f32_32x32x16_bf16 v[2:17], v[42:45], v[34:37], v[2:17]
	v_lshlrev_b32_e32 v35, 16, v66
	v_and_b32_e32 v36, 0xffff0000, v66
	v_mul_f32_e32 v34, v50, v35
	v_mul_f32_e32 v37, v50, v36
	v_mul_f32_e32 v36, v51, v36
	v_cvt_pk_bf16_f32 v34, v34, v37
	v_mul_f32_e32 v35, v51, v35
	s_waitcnt lgkmcnt(0)
	v_mfma_f32_32x32x16_bf16 v[2:17], v[46:49], v[38:41], v[2:17]
	v_cvt_pk_bf16_f32 v38, v35, v36
	v_lshlrev_b32_e32 v36, 16, v67
	v_and_b32_e32 v37, 0xffff0000, v67
	v_mul_f32_e32 v35, v50, v36
	v_mul_f32_e32 v39, v50, v37
	v_mul_f32_e32 v37, v51, v37
	v_cvt_pk_bf16_f32 v35, v35, v39
	v_mul_f32_e32 v36, v51, v36
	v_cvt_pk_bf16_f32 v39, v36, v37
	v_lshlrev_b32_e32 v37, 16, v68
	v_and_b32_e32 v40, 0xffff0000, v68
	v_mul_f32_e32 v36, v50, v37
	v_mul_f32_e32 v41, v50, v40
	v_cvt_pk_bf16_f32 v36, v36, v41
	v_mul_f32_e32 v37, v51, v37
	v_mul_f32_e32 v40, v51, v40
	v_lshlrev_b32_e32 v41, 16, v69
	v_and_b32_e32 v42, 0xffff0000, v69
	v_cvt_pk_bf16_f32 v40, v37, v40
	v_mul_f32_e32 v37, v50, v41
	v_mul_f32_e32 v43, v50, v42
	v_mul_f32_e32 v41, v51, v41
	v_mul_f32_e32 v42, v51, v42
	v_cvt_pk_bf16_f32 v37, v37, v43
	v_cvt_pk_bf16_f32 v41, v41, v42
	ds_read_b128 v[42:45], v137 offset:32768
	ds_read_b128 v[46:49], v137 offset:40960
	s_waitcnt lgkmcnt(1)
	v_mfma_f32_32x32x16_bf16 v[18:33], v[42:45], v[34:37], v[18:33]
	s_waitcnt lgkmcnt(0)
	v_mfma_f32_32x32x16_bf16 v[18:33], v[46:49], v[38:41], v[18:33]
	ds_read_b128 v[42:45], v137 offset:36864
	ds_read_b128 v[46:49], v137 offset:45056
	s_waitcnt lgkmcnt(1)
	v_mfma_f32_32x32x16_bf16 v[2:17], v[42:45], v[34:37], v[2:17]
	v_lshl_add_u64 v[34:35], s[22:23], 1, v[106:107]
	v_lshlrev_b32_e32 v36, 1, v82
	v_mov_b32_e32 v37, v0
	v_lshl_add_u64 v[34:35], v[34:35], 0, v[36:37]
	v_lshl_add_u64 v[36:37], v[34:35], 0, s[4:5]
	v_add_co_u32_e32 v34, vcc, s78, v34
	s_lshl_b64 s[4:5], s[24:25], 2
	s_nop 0
	v_addc_co_u32_e32 v35, vcc, 0, v35, vcc
	global_load_dwordx2 v[80:81], v[34:35], off offset:1024
	global_load_dwordx2 v[76:77], v[36:37], off offset:16
	global_load_dwordx2 v[74:75], v[36:37], off offset:32
	global_load_dwordx2 v[72:73], v[36:37], off offset:48
	global_load_dwordx2 v[70:71], v[36:37], off offset:64
	global_load_dwordx2 v[68:69], v[36:37], off offset:80
	global_load_dwordx2 v[66:67], v[36:37], off offset:96
	global_load_dwordx2 v[64:65], v[36:37], off offset:112
	ds_read_b32 v34, v0 offset:640
	ds_read_b32 v35, v0 offset:644
	s_waitcnt lgkmcnt(2)
	v_mfma_f32_32x32x16_bf16 v[2:17], v[46:49], v[38:41], v[2:17]
	v_mul_f32_e32 v78, v19, v19
	v_fmac_f32_e32 v78, v18, v18
	s_waitcnt lgkmcnt(1)
	v_readfirstlane_b32 s11, v34
	s_waitcnt lgkmcnt(0)
	v_readfirstlane_b32 s10, v35
	s_add_u32 s11, s11, s4
	s_addc_u32 s10, s10, s5
	s_lshl_b64 s[4:5], s[22:23], 2
	s_add_u32 s4, s11, s4
	s_addc_u32 s5, s10, s5
	v_lshlrev_b32_e32 v34, 2, v82
	global_load_dwordx4 v[144:147], v34, s[4:5]
	global_load_dwordx4 v[58:61], v34, s[4:5] offset:32
	global_load_dwordx4 v[54:57], v34, s[4:5] offset:64
	global_load_dwordx4 v[50:53], v34, s[4:5] offset:96
	global_load_dwordx4 v[46:49], v34, s[4:5] offset:128
	global_load_dwordx4 v[42:45], v34, s[4:5] offset:160
	global_load_dwordx4 v[38:41], v34, s[4:5] offset:192
	s_nop 0
	global_load_dwordx4 v[34:37], v34, s[4:5] offset:224
	v_fmac_f32_e32 v78, v20, v20
	v_fmac_f32_e32 v78, v21, v21
	v_fmac_f32_e32 v78, v22, v22
	v_fmac_f32_e32 v78, v23, v23
	v_fmac_f32_e32 v78, v24, v24
	v_fmac_f32_e32 v78, v25, v25
	v_fmac_f32_e32 v78, v26, v26
	v_fmac_f32_e32 v78, v27, v27
	v_fmac_f32_e32 v78, v28, v28
	v_fmac_f32_e32 v78, v29, v29
	v_fmac_f32_e32 v78, v30, v30
	v_fmac_f32_e32 v78, v31, v31
	v_fmac_f32_e32 v78, v32, v32
	v_fmac_f32_e32 v78, v33, v33
	v_fmac_f32_e32 v78, v2, v2
	v_fmac_f32_e32 v78, v3, v3
	v_fmac_f32_e32 v78, v4, v4
	v_fmac_f32_e32 v78, v5, v5
	v_fmac_f32_e32 v78, v6, v6
	v_fmac_f32_e32 v78, v7, v7
	v_fmac_f32_e32 v78, v8, v8
	v_fmac_f32_e32 v78, v9, v9
	v_fmac_f32_e32 v78, v10, v10
	v_fmac_f32_e32 v78, v11, v11
	v_fmac_f32_e32 v78, v12, v12
	v_fmac_f32_e32 v78, v13, v13
	v_fmac_f32_e32 v78, v14, v14
	v_fmac_f32_e32 v78, v15, v15
	v_pk_mul_f32 v[62:63], v[16:17], v[16:17]
	s_and_b64 vcc, exec, s[20:21]
	v_add_f32_e32 v62, v78, v62
	v_add_f32_e32 v62, v62, v63
	v_mov_b32_e32 v63, v62
	s_nop 1
	v_permlane32_swap_b32_e32 v62, v63
	v_add_f32_e32 v62, v62, v63
	v_fmamk_f32 v62, v62, 0x3c800000, v210
	v_rsq_f32_e32 v78, v62
	v_lshlrev_b64 v[62:63], 10, v[104:105]
	v_lshl_add_u64 v[62:63], s[82:83], 0, v[62:63]
	v_lshl_add_u64 v[62:63], v[62:63], 0, s[22:23]
	v_mul_f32_e32 v78, 0x41800000, v78
	v_mul_f32_e32 v150, v78, v18
	v_lshl_add_u64 v[62:63], v[62:63], 0, v[84:85]
	s_waitcnt vmcnt(15)
	v_lshlrev_b32_e32 v105, 16, v80
	v_mul_f32_e32 v79, 0xbfb8aa3b, v105
	v_exp_f32_e32 v79, v79
	v_and_b32_e32 v107, 0xffff0000, v80
	v_mul_f32_e32 v18, 0xbfb8aa3b, v107
	v_exp_f32_e32 v18, v18
	v_add_f32_e32 v79, 1.0, v79
	v_rcp_f32_e32 v151, v79
	v_lshlrev_b32_e32 v149, 16, v81
	v_add_f32_e32 v18, 1.0, v18
	v_and_b32_e32 v81, 0xffff0000, v81
	s_waitcnt vmcnt(7)
	v_mov_b32_e32 v104, v144
	v_pk_mul_f32 v[104:105], v[150:151], v[104:105]
	v_mov_b32_e32 v106, v145
	v_mul_f32_e32 v79, v104, v105
	v_rcp_f32_e32 v105, v18
	v_mul_f32_e32 v104, v78, v19
	v_mov_b32_e32 v148, v146
	v_mov_b32_e32 v80, v147
	v_pk_mul_f32 v[18:19], v[104:105], v[106:107]
	v_mul_f32_e32 v106, v78, v22
	v_mul_f32_e32 v101, v18, v19
	v_mul_f32_e32 v18, 0xbfb8aa3b, v149
	v_exp_f32_e32 v18, v18
	v_lshlrev_b32_e32 v105, 16, v77
	s_waitcnt vmcnt(6)
	v_mov_b32_e32 v104, v60
	v_and_b32_e32 v77, 0xffff0000, v77
	v_add_f32_e32 v18, 1.0, v18
	v_rcp_f32_e32 v19, v18
	v_mul_f32_e32 v18, v78, v20
	s_waitcnt vmcnt(5)
	v_mov_b32_e32 v60, v57
	v_pk_mul_f32 v[18:19], v[18:19], v[148:149]
	s_nop 0
	v_mul_f32_e32 v20, v18, v19
	v_mul_f32_e32 v18, 0xbfb8aa3b, v81
	v_exp_f32_e32 v18, v18
	s_nop 0
	v_add_f32_e32 v18, 1.0, v18
	v_rcp_f32_e32 v19, v18
	v_mul_f32_e32 v18, v78, v21
	v_lshlrev_b32_e32 v21, 16, v76
	v_pk_mul_f32 v[18:19], v[18:19], v[80:81]
	s_nop 0
	v_mul_f32_e32 v19, v18, v19
	v_cvt_pk_fp8_f32 v18, v79, v101
	v_and_b32_e32 v81, 0xffff0000, v76
	v_mov_b32_e32 v80, v59
	v_mov_b32_e32 v76, v61
	v_cvt_pk_fp8_f32 v18, v20, v19 op_sel:[0,0,1]
	v_mul_f32_e32 v19, 0xbfb8aa3b, v21
	v_exp_f32_e32 v19, v19
	v_mov_b32_e32 v20, v58
	v_lshlrev_b32_e32 v59, 16, v75
	v_and_b32_e32 v61, 0xffff0000, v75
	v_add_f32_e32 v19, 1.0, v19
	v_rcp_f32_e32 v107, v19
	v_mov_b32_e32 v58, v56
	v_pk_mul_f32 v[20:21], v[106:107], v[20:21]
	s_nop 0
	v_mul_f32_e32 v19, v20, v21
	v_mul_f32_e32 v20, 0xbfb8aa3b, v81
	v_exp_f32_e32 v20, v20
	s_nop 0
	v_add_f32_e32 v20, 1.0, v20
	v_rcp_f32_e32 v21, v20
	v_mul_f32_e32 v20, v78, v23
	v_pk_mul_f32 v[20:21], v[20:21], v[80:81]
	s_nop 0
	v_mul_f32_e32 v22, v20, v21
	v_mul_f32_e32 v20, 0xbfb8aa3b, v105
	v_exp_f32_e32 v20, v20
	s_nop 0
	v_add_f32_e32 v20, 1.0, v20
	v_rcp_f32_e32 v21, v20
	v_mul_f32_e32 v20, v78, v24
	v_mov_b32_e32 v24, v55
	v_pk_mul_f32 v[20:21], v[20:21], v[104:105]
	s_nop 0
	v_mul_f32_e32 v23, v20, v21
	v_mul_f32_e32 v20, 0xbfb8aa3b, v77
	v_exp_f32_e32 v20, v20
	s_nop 0
	v_add_f32_e32 v20, 1.0, v20
	v_rcp_f32_e32 v21, v20
	v_mul_f32_e32 v20, v78, v25
	v_and_b32_e32 v25, 0xffff0000, v74
	v_pk_mul_f32 v[20:21], v[20:21], v[76:77]
	s_nop 0
	v_mul_f32_e32 v21, v20, v21
	v_cvt_pk_fp8_f32 v20, v19, v22
	v_mov_b32_e32 v22, v54
	v_mul_f32_e32 v54, v78, v30
	v_cvt_pk_fp8_f32 v20, v23, v21 op_sel:[0,0,1]
	v_lshlrev_b32_e32 v23, 16, v74
	v_mul_f32_e32 v19, 0xbfb8aa3b, v23
	v_exp_f32_e32 v19, v19
	v_mul_f32_e32 v74, v78, v26
	s_waitcnt vmcnt(4)
	v_mov_b32_e32 v26, v52
	v_add_f32_e32 v19, 1.0, v19
	v_rcp_f32_e32 v75, v19
	v_mul_f32_e32 v19, 0xbfb8aa3b, v25
	v_exp_f32_e32 v19, v19
	v_pk_mul_f32 v[22:23], v[74:75], v[22:23]
	s_nop 0
	v_mul_f32_e32 v21, v22, v23
	v_add_f32_e32 v19, 1.0, v19
	v_rcp_f32_e32 v23, v19
	v_mul_f32_e32 v19, 0xbfb8aa3b, v59
	v_exp_f32_e32 v19, v19
	v_mul_f32_e32 v22, v78, v27
	v_pk_mul_f32 v[22:23], v[22:23], v[24:25]
	v_lshlrev_b32_e32 v27, 16, v73
	v_add_f32_e32 v19, 1.0, v19
	v_mul_f32_e32 v24, v22, v23
	v_rcp_f32_e32 v23, v19
	v_mul_f32_e32 v19, 0xbfb8aa3b, v61
	v_exp_f32_e32 v19, v19
	v_mul_f32_e32 v22, v78, v28
	v_pk_mul_f32 v[22:23], v[22:23], v[58:59]
	v_mov_b32_e32 v28, v53
	v_add_f32_e32 v19, 1.0, v19
	v_mul_f32_e32 v25, v22, v23
	v_rcp_f32_e32 v23, v19
	v_mul_f32_e32 v22, v78, v29
	v_cvt_pk_fp8_f32 v19, v21, v24
	v_pk_mul_f32 v[22:23], v[22:23], v[60:61]
	v_mov_b32_e32 v24, v51
	v_mul_f32_e32 v22, v22, v23
	v_lshlrev_b32_e32 v23, 16, v72
	v_mul_f32_e32 v21, 0xbfb8aa3b, v23
	v_exp_f32_e32 v21, v21
	v_cvt_pk_fp8_f32 v19, v25, v22 op_sel:[0,0,1]
	v_and_b32_e32 v25, 0xffff0000, v72
	v_mov_b32_e32 v22, v50
	v_add_f32_e32 v21, 1.0, v21
	v_rcp_f32_e32 v55, v21
	v_mul_f32_e32 v21, 0xbfb8aa3b, v25
	v_exp_f32_e32 v21, v21
	v_and_b32_e32 v29, 0xffff0000, v73
	v_pk_mul_f32 v[22:23], v[54:55], v[22:23]
	v_permlane32_swap_b32_e32 v18, v19
	v_add_f32_e32 v21, 1.0, v21
	v_mul_f32_e32 v30, v22, v23
	v_rcp_f32_e32 v23, v21
	v_mul_f32_e32 v21, 0xbfb8aa3b, v27
	v_exp_f32_e32 v21, v21
	v_mul_f32_e32 v22, v78, v31
	v_pk_mul_f32 v[22:23], v[22:23], v[24:25]
	v_add_f32_e32 v21, 1.0, v21
	v_mul_f32_e32 v24, v22, v23
	v_rcp_f32_e32 v23, v21
	v_mul_f32_e32 v21, 0xbfb8aa3b, v29
	v_exp_f32_e32 v21, v21
	v_mul_f32_e32 v22, v78, v32
	v_pk_mul_f32 v[22:23], v[22:23], v[26:27]
	v_mul_f32_e32 v26, v78, v2
	v_add_f32_e32 v21, 1.0, v21
	v_mul_f32_e32 v25, v22, v23
	v_rcp_f32_e32 v23, v21
	v_cvt_pk_fp8_f32 v21, v30, v24
	v_mul_f32_e32 v22, v78, v33
	v_pk_mul_f32 v[22:23], v[22:23], v[28:29]
	s_waitcnt vmcnt(3)
	v_mov_b32_e32 v24, v49
	v_mul_f32_e32 v22, v22, v23
	v_cvt_pk_fp8_f32 v21, v25, v22 op_sel:[0,0,1]
	v_lshlrev_b32_e32 v23, 16, v71
	v_mov_b32_e32 v22, v48
	v_and_b32_e32 v25, 0xffff0000, v71
	v_permlane32_swap_b32_e32 v20, v21
	global_store_dwordx4 v[62:63], v[18:21], off offset:768
	s_nop 1
	v_lshlrev_b32_e32 v19, 16, v70
	v_mul_f32_e32 v18, 0xbfb8aa3b, v19
	v_exp_f32_e32 v18, v18
	v_and_b32_e32 v21, 0xffff0000, v70
	v_mul_f32_e32 v2, 0xbfb8aa3b, v21
	v_exp_f32_e32 v2, v2
	v_add_f32_e32 v18, 1.0, v18
	v_rcp_f32_e32 v27, v18
	v_mov_b32_e32 v18, v46
	v_add_f32_e32 v2, 1.0, v2
	v_mov_b32_e32 v20, v47
	v_pk_mul_f32 v[18:19], v[26:27], v[18:19]
	s_nop 0
	v_mul_f32_e32 v26, v18, v19
	v_rcp_f32_e32 v19, v2
	v_mul_f32_e32 v18, v78, v3
	v_pk_mul_f32 v[2:3], v[18:19], v[20:21]
	s_nop 0
	v_mul_f32_e32 v18, v2, v3
	v_mul_f32_e32 v2, 0xbfb8aa3b, v23
	v_exp_f32_e32 v2, v2
	v_and_b32_e32 v19, 0xffff0000, v68
	v_lshlrev_b32_e32 v21, 16, v69
	s_waitcnt vmcnt(3)
	v_mov_b32_e32 v20, v44
	v_add_f32_e32 v2, 1.0, v2
	v_rcp_f32_e32 v3, v2
	v_mul_f32_e32 v2, v78, v4
	v_pk_mul_f32 v[2:3], v[2:3], v[22:23]
	s_nop 0
	v_mul_f32_e32 v4, v2, v3
	v_mul_f32_e32 v2, 0xbfb8aa3b, v25
	v_exp_f32_e32 v2, v2
	v_and_b32_e32 v23, 0xffff0000, v69
	v_mov_b32_e32 v22, v45
	v_add_f32_e32 v2, 1.0, v2
	v_rcp_f32_e32 v3, v2
	v_mul_f32_e32 v2, v78, v5
	v_lshlrev_b32_e32 v5, 16, v68
	v_pk_mul_f32 v[2:3], v[2:3], v[24:25]
	s_nop 0
	v_mul_f32_e32 v3, v2, v3
	v_cvt_pk_fp8_f32 v2, v26, v18
	v_mul_f32_e32 v24, v78, v6
	v_mov_b32_e32 v18, v43
	v_cvt_pk_fp8_f32 v2, v4, v3 op_sel:[0,0,1]
	v_mul_f32_e32 v3, 0xbfb8aa3b, v5
	v_exp_f32_e32 v3, v3
	v_mov_b32_e32 v4, v42
	v_add_f32_e32 v3, 1.0, v3
	v_rcp_f32_e32 v25, v3
	s_nop 0
	v_pk_mul_f32 v[4:5], v[24:25], v[4:5]
	s_nop 0
	v_mul_f32_e32 v3, v4, v5
	v_mul_f32_e32 v4, 0xbfb8aa3b, v19
	v_exp_f32_e32 v4, v4
	s_nop 0
	v_add_f32_e32 v4, 1.0, v4
	v_rcp_f32_e32 v5, v4
	v_mul_f32_e32 v4, v78, v7
	v_pk_mul_f32 v[4:5], v[4:5], v[18:19]
	s_nop 0
	v_mul_f32_e32 v6, v4, v5
	v_mul_f32_e32 v4, 0xbfb8aa3b, v21
	v_exp_f32_e32 v4, v4
	v_lshlrev_b32_e32 v19, 16, v67
	s_waitcnt vmcnt(2)
	v_mov_b32_e32 v18, v40
	v_add_f32_e32 v4, 1.0, v4
	v_rcp_f32_e32 v5, v4
	v_mul_f32_e32 v4, v78, v8
	v_mov_b32_e32 v8, v39
	v_pk_mul_f32 v[4:5], v[4:5], v[20:21]
	s_nop 0
	v_mul_f32_e32 v7, v4, v5
	v_mul_f32_e32 v4, 0xbfb8aa3b, v23
	v_exp_f32_e32 v4, v4
	v_and_b32_e32 v21, 0xffff0000, v67
	v_mov_b32_e32 v20, v41
	v_add_f32_e32 v4, 1.0, v4
	v_rcp_f32_e32 v5, v4
	v_mul_f32_e32 v4, v78, v9
	v_and_b32_e32 v9, 0xffff0000, v66
	v_pk_mul_f32 v[4:5], v[4:5], v[22:23]
	s_nop 0
	v_mul_f32_e32 v5, v4, v5
	v_cvt_pk_fp8_f32 v4, v3, v6
	v_mul_f32_e32 v22, v78, v10
	v_mov_b32_e32 v6, v38
	s_waitcnt vmcnt(1)
	v_mov_b32_e32 v10, v36
	v_cvt_pk_fp8_f32 v4, v7, v5 op_sel:[0,0,1]
	v_lshlrev_b32_e32 v7, 16, v66
	v_mul_f32_e32 v3, 0xbfb8aa3b, v7
	v_exp_f32_e32 v3, v3
	s_nop 0
	v_add_f32_e32 v3, 1.0, v3
	v_rcp_f32_e32 v23, v3
	v_mul_f32_e32 v3, 0xbfb8aa3b, v9
	v_exp_f32_e32 v3, v3
	v_pk_mul_f32 v[6:7], v[22:23], v[6:7]
	s_nop 0
	v_mul_f32_e32 v5, v6, v7
	v_add_f32_e32 v3, 1.0, v3
	v_rcp_f32_e32 v7, v3
	v_mul_f32_e32 v3, 0xbfb8aa3b, v19
	v_exp_f32_e32 v3, v3
	v_mul_f32_e32 v6, v78, v11
	v_pk_mul_f32 v[6:7], v[6:7], v[8:9]
	v_lshlrev_b32_e32 v11, 16, v65
	v_add_f32_e32 v3, 1.0, v3
	v_mul_f32_e32 v8, v6, v7
	v_rcp_f32_e32 v7, v3
	v_mul_f32_e32 v3, 0xbfb8aa3b, v21
	v_exp_f32_e32 v3, v3
	v_mul_f32_e32 v6, v78, v12
	v_pk_mul_f32 v[6:7], v[6:7], v[18:19]
	v_mul_f32_e32 v18, v78, v14
	v_add_f32_e32 v3, 1.0, v3
	v_mul_f32_e32 v9, v6, v7
	v_rcp_f32_e32 v7, v3
	v_mul_f32_e32 v6, v78, v13
	v_cvt_pk_fp8_f32 v3, v5, v8
	v_pk_mul_f32 v[6:7], v[6:7], v[20:21]
	v_mov_b32_e32 v8, v35
	v_mul_f32_e32 v6, v6, v7
	v_lshlrev_b32_e32 v7, 16, v64
	v_mul_f32_e32 v5, 0xbfb8aa3b, v7
	v_exp_f32_e32 v5, v5
	v_cvt_pk_fp8_f32 v3, v9, v6 op_sel:[0,0,1]
	v_and_b32_e32 v9, 0xffff0000, v64
	v_mov_b32_e32 v6, v34
	v_add_f32_e32 v5, 1.0, v5
	v_rcp_f32_e32 v19, v5
	v_mul_f32_e32 v5, 0xbfb8aa3b, v9
	v_exp_f32_e32 v5, v5
	v_and_b32_e32 v13, 0xffff0000, v65
	v_pk_mul_f32 v[6:7], v[18:19], v[6:7]
	v_mov_b32_e32 v12, v37
	v_add_f32_e32 v5, 1.0, v5
	v_mul_f32_e32 v14, v6, v7
	v_rcp_f32_e32 v7, v5
	v_mul_f32_e32 v5, 0xbfb8aa3b, v11
	v_exp_f32_e32 v5, v5
	v_mul_f32_e32 v6, v78, v15
	v_pk_mul_f32 v[6:7], v[6:7], v[8:9]
	v_permlane32_swap_b32_e32 v2, v3
	v_add_f32_e32 v5, 1.0, v5
	v_mul_f32_e32 v8, v6, v7
	v_rcp_f32_e32 v7, v5
	v_mul_f32_e32 v5, 0xbfb8aa3b, v13
	v_exp_f32_e32 v5, v5
	v_mul_f32_e32 v6, v78, v16
	v_pk_mul_f32 v[6:7], v[6:7], v[10:11]
	v_add_f32_e32 v5, 1.0, v5
	v_mul_f32_e32 v9, v6, v7
	v_rcp_f32_e32 v7, v5
	v_cvt_pk_fp8_f32 v5, v14, v8
	v_mul_f32_e32 v6, v78, v17
	v_pk_mul_f32 v[6:7], v[6:7], v[12:13]
	s_nop 0
	v_mul_f32_e32 v6, v6, v7
	v_cvt_pk_fp8_f32 v5, v9, v6 op_sel:[0,0,1]
	s_nop 1
	v_permlane32_swap_b32_e32 v4, v5
	global_store_dwordx4 v[62:63], v[2:5], off offset:800
	s_cbranch_vccz .LBB0_550
	s_waitcnt vmcnt(0)
	s_barrier
	s_and_saveexec_b64 s[4:5], s[0:1]
	s_cbranch_execz .LBB0_549
	s_mov_b64 s[10:11], exec
	v_mbcnt_lo_u32_b32 v2, s10, 0
	buffer_wbl2 sc1
	s_waitcnt vmcnt(0)
	s_waitcnt vmcnt(0)
	v_mbcnt_hi_u32_b32 v2, s11, v2
	v_cmp_eq_u32_e32 vcc, 0, v2
	s_and_b64 s[14:15], exec, vcc
	s_mov_b64 exec, s[14:15]
	s_cbranch_execz .LBB0_549
	s_bcnt1_i32_b64 s10, s[10:11]
	v_mov_b32_e32 v2, s10
	global_atomic_add v0, v2, s[84:85]
	s_branch .LBB0_549

.LBB0_599:
	v_add_u32_e32 v1, s26, v114
	v_add_u32_e32 v105, 1, v1
	v_max_i32_e32 v106, 1, v1
	v_min_i32_e32 v105, s14, v105
	v_sub_u32_e32 v105, v105, v106
	v_add_u32_e32 v105, 1, v105
	v_cvt_f32_i32_e32 v105, v105
	ds_read_b128 v[72:75], v124 offset:3696
	ds_read_b128 v[76:79], v124 offset:4224
	v_div_scale_f32 v107, s[10:11], v105, v105, 1.0
	v_rcp_f32_e32 v141, v107
	s_waitcnt lgkmcnt(1)
	v_lshlrev_b32_e32 v2, 16, v72
	v_and_b32_e32 v3, 0xffff0000, v72
	v_lshlrev_b32_e32 v72, 16, v73
	v_fma_f32 v142, -v107, v141, 1.0
	v_fmac_f32_e32 v141, v142, v141
	v_div_scale_f32 v142, vcc, 1.0, v105, 1.0
	v_mul_f32_e32 v143, v142, v141
	v_fma_f32 v144, -v107, v143, v142
	v_fmac_f32_e32 v143, v144, v141
	v_and_b32_e32 v73, 0xffff0000, v73
	v_lshlrev_b32_e32 v80, 16, v74
	v_and_b32_e32 v74, 0xffff0000, v74
	v_lshlrev_b32_e32 v81, 16, v75
	v_and_b32_e32 v75, 0xffff0000, v75
	v_fma_f32 v107, -v107, v143, v142
	v_add_f32_e32 v3, 0, v3
	v_add_f32_e32 v72, 0, v72
	v_add_f32_e32 v73, 0, v73
	v_add_f32_e32 v80, 0, v80
	v_add_f32_e32 v74, 0, v74
	v_add_f32_e32 v81, 0, v81
	v_add_f32_e32 v75, 0, v75
	s_waitcnt lgkmcnt(0)
	v_lshlrev_b32_e32 v101, 16, v76
	v_and_b32_e32 v76, 0xffff0000, v76
	v_lshlrev_b32_e32 v103, 16, v77
	v_and_b32_e32 v77, 0xffff0000, v77
	v_lshlrev_b32_e32 v104, 16, v78
	v_and_b32_e32 v78, 0xffff0000, v78
	v_lshlrev_b32_e32 v106, 16, v79
	v_and_b32_e32 v79, 0xffff0000, v79
	v_div_fmas_f32 v107, v107, v141, v143
	v_add_f32_e32 v2, 0, v2
	v_add_f32_e32 v3, v3, v76
	v_add_f32_e32 v72, v72, v103
	v_add_f32_e32 v73, v73, v77
	v_add_f32_e32 v80, v80, v104
	v_add_f32_e32 v74, v74, v78
	v_add_f32_e32 v81, v81, v106
	v_add_f32_e32 v75, v75, v79
	v_div_fixup_f32 v105, v107, v105, 1.0
	v_add_f32_e32 v2, v2, v101
	v_fma_f32 v3, v105, v3, -v76
	v_fma_f32 v76, v105, v72, -v103
	v_fma_f32 v73, v105, v73, -v77
	v_fma_f32 v77, v105, v80, -v104
	v_fma_f32 v74, v105, v74, -v78
	v_fma_f32 v78, v105, v81, -v106
	v_fma_f32 v75, v105, v75, -v79
	v_fma_f32 v2, v105, v2, -v101
	v_cvt_pk_bf16_f32 v72, v2, v3
	v_cvt_pk_bf16_f32 v73, v76, v73
	v_cvt_pk_bf16_f32 v74, v77, v74
	v_cvt_pk_bf16_f32 v75, v78, v75
	ds_read_b128 v[76:79], v124 offset:3296
	ds_write_b128 v124, v[72:75] offset:45056
	ds_read_b128 v[72:75], v124 offset:3824
	s_waitcnt lgkmcnt(2)
	v_and_b32_e32 v3, 0xffff0000, v76
	v_lshlrev_b32_e32 v81, 16, v79
	v_and_b32_e32 v79, 0xffff0000, v79
	v_lshlrev_b32_e32 v2, 16, v76
	v_add_f32_e32 v3, 0, v3
	v_lshlrev_b32_e32 v76, 16, v77
	v_add_f32_e32 v101, 0, v79
	s_waitcnt lgkmcnt(0)
	v_lshlrev_b32_e32 v79, 16, v72
	v_and_b32_e32 v72, 0xffff0000, v72
	v_add_f32_e32 v76, 0, v76
	v_and_b32_e32 v77, 0xffff0000, v77
	v_add_f32_e32 v3, v3, v72
	v_lshlrev_b32_e32 v72, 16, v73
	v_add_f32_e32 v77, 0, v77
	v_lshlrev_b32_e32 v80, 16, v78
	v_add_f32_e32 v103, v76, v72
	v_and_b32_e32 v72, 0xffff0000, v73
	v_add_f32_e32 v80, 0, v80
	v_and_b32_e32 v78, 0xffff0000, v78
	v_add_f32_e32 v104, v77, v72
	v_lshlrev_b32_e32 v72, 16, v74
	v_add_f32_e32 v78, 0, v78
	v_add_f32_e32 v80, v80, v72
	v_and_b32_e32 v72, 0xffff0000, v74
	v_add_f32_e32 v2, 0, v2
	v_add_f32_e32 v81, 0, v81
	v_add_f32_e32 v105, v78, v72
	v_lshlrev_b32_e32 v72, 16, v75
	v_add_f32_e32 v2, v2, v79
	ds_read_b128 v[76:79], v124 offset:4352
	v_add_f32_e32 v81, v81, v72
	v_and_b32_e32 v72, 0xffff0000, v75
	v_add_f32_e32 v101, v101, v72
	ds_read_b128 v[72:75], v124 offset:4880
	s_waitcnt lgkmcnt(1)
	v_lshlrev_b32_e32 v106, 16, v76
	v_and_b32_e32 v76, 0xffff0000, v76
	v_add_f32_e32 v3, v3, v76
	v_lshlrev_b32_e32 v107, 16, v77
	s_waitcnt lgkmcnt(0)
	v_lshlrev_b32_e32 v143, 16, v72
	v_and_b32_e32 v72, 0xffff0000, v72
	v_add_f32_e32 v103, v103, v107
	v_lshlrev_b32_e32 v141, 16, v78
	v_add_f32_e32 v3, v3, v72
	v_lshlrev_b32_e32 v72, 16, v73
	v_and_b32_e32 v77, 0xffff0000, v77
	v_add_f32_e32 v80, v80, v141
	v_add_f32_e32 v72, v103, v72
	v_lshlrev_b32_e32 v103, 16, v74
	v_add_f32_e32 v104, v104, v77
	v_and_b32_e32 v73, 0xffff0000, v73
	v_add_f32_e32 v80, v80, v103
	v_add_u32_e32 v103, 2, v1
	v_add_f32_e32 v73, v104, v73
	v_max_i32_e32 v104, 2, v1
	v_min_i32_e32 v103, s14, v103
	v_sub_u32_e32 v103, v103, v104
	v_add_u32_e32 v103, 2, v103
	v_cvt_f32_i32_e32 v103, v103
	v_and_b32_e32 v78, 0xffff0000, v78
	v_add_f32_e32 v105, v105, v78
	v_and_b32_e32 v74, 0xffff0000, v74
	v_add_f32_e32 v2, v2, v106
	v_add_f32_e32 v74, v105, v74
	v_div_scale_f32 v105, s[10:11], v103, v103, 1.0
	v_add_f32_e32 v2, v2, v143
	v_rcp_f32_e32 v143, v105
	v_lshlrev_b32_e32 v142, 16, v79
	v_and_b32_e32 v79, 0xffff0000, v79
	v_add_f32_e32 v101, v101, v79
	v_lshlrev_b32_e32 v104, 16, v75
	v_and_b32_e32 v75, 0xffff0000, v75
	v_add_f32_e32 v75, v101, v75
	v_fma_f32 v101, -v105, v143, 1.0
	v_add_f32_e32 v81, v81, v142
	v_fmac_f32_e32 v143, v101, v143
	v_div_scale_f32 v101, vcc, 1.0, v103, 1.0
	v_add_f32_e32 v81, v81, v104
	v_mul_f32_e32 v104, v101, v143
	v_fma_f32 v144, -v105, v104, v101
	v_fmac_f32_e32 v104, v144, v143
	v_fma_f32 v101, -v105, v104, v101
	v_div_fmas_f32 v101, v101, v143, v104
	v_div_fixup_f32 v101, v101, v103, 1.0
	v_fma_f32 v3, v101, v3, -v76
	v_fma_f32 v76, v101, v72, -v107
	v_fma_f32 v73, v101, v73, -v77
	v_fma_f32 v77, v101, v80, -v141
	v_fma_f32 v74, v101, v74, -v78
	v_fma_f32 v78, v101, v81, -v142
	v_fma_f32 v75, v101, v75, -v79
	v_fma_f32 v2, v101, v2, -v106
	v_cvt_pk_bf16_f32 v72, v2, v3
	v_cvt_pk_bf16_f32 v73, v76, v73
	v_cvt_pk_bf16_f32 v74, v77, v74
	v_cvt_pk_bf16_f32 v75, v78, v75
	ds_read_b128 v[76:79], v124 offset:2368
	ds_write_b128 v124, v[72:75] offset:45184
	ds_read_b128 v[72:75], v124 offset:2896
	s_waitcnt lgkmcnt(2)
	v_and_b32_e32 v3, 0xffff0000, v76
	v_lshlrev_b32_e32 v81, 16, v79
	v_and_b32_e32 v79, 0xffff0000, v79
	v_lshlrev_b32_e32 v2, 16, v76
	v_add_f32_e32 v3, 0, v3
	v_lshlrev_b32_e32 v76, 16, v77
	v_add_f32_e32 v101, 0, v79
	s_waitcnt lgkmcnt(0)
	v_lshlrev_b32_e32 v79, 16, v72
	v_and_b32_e32 v72, 0xffff0000, v72
	v_add_f32_e32 v76, 0, v76
	v_and_b32_e32 v77, 0xffff0000, v77
	v_add_f32_e32 v3, v3, v72
	v_lshlrev_b32_e32 v72, 16, v73
	v_add_f32_e32 v77, 0, v77
	v_lshlrev_b32_e32 v80, 16, v78
	v_add_f32_e32 v103, v76, v72
	v_and_b32_e32 v72, 0xffff0000, v73
	v_add_f32_e32 v80, 0, v80
	v_and_b32_e32 v78, 0xffff0000, v78
	v_add_f32_e32 v104, v77, v72
	v_lshlrev_b32_e32 v72, 16, v74
	v_add_f32_e32 v2, 0, v2
	v_add_f32_e32 v78, 0, v78
	v_add_f32_e32 v80, v80, v72
	v_and_b32_e32 v72, 0xffff0000, v74
	v_add_f32_e32 v2, v2, v79
	v_add_f32_e32 v105, v78, v72
	ds_read_b128 v[76:79], v124 offset:3424
	v_add_f32_e32 v81, 0, v81
	v_lshlrev_b32_e32 v72, 16, v75
	v_add_f32_e32 v81, v81, v72
	v_and_b32_e32 v72, 0xffff0000, v75
	v_add_f32_e32 v101, v101, v72
	ds_read_b128 v[72:75], v124 offset:3952
	s_waitcnt lgkmcnt(1)
	v_lshlrev_b32_e32 v106, 16, v76
	v_and_b32_e32 v76, 0xffff0000, v76
	v_add_f32_e32 v3, v3, v76
	v_lshlrev_b32_e32 v76, 16, v77
	v_add_f32_e32 v76, v103, v76
	v_lshlrev_b32_e32 v103, 16, v78
	v_add_f32_e32 v80, v80, v103
	v_lshlrev_b32_e32 v103, 16, v79
	v_and_b32_e32 v79, 0xffff0000, v79
	v_add_f32_e32 v101, v101, v79
	s_waitcnt lgkmcnt(0)
	v_lshlrev_b32_e32 v79, 16, v72
	v_and_b32_e32 v72, 0xffff0000, v72
	v_and_b32_e32 v77, 0xffff0000, v77
	v_add_f32_e32 v3, v3, v72
	v_lshlrev_b32_e32 v72, 16, v73
	v_add_f32_e32 v77, v104, v77
	v_add_f32_e32 v81, v81, v103
	v_add_f32_e32 v103, v76, v72
	v_and_b32_e32 v72, 0xffff0000, v73
	v_and_b32_e32 v78, 0xffff0000, v78
	v_add_f32_e32 v104, v77, v72
	v_lshlrev_b32_e32 v72, 16, v74
	v_add_f32_e32 v2, v2, v106
	v_add_f32_e32 v78, v105, v78
	v_add_f32_e32 v80, v80, v72
	v_and_b32_e32 v72, 0xffff0000, v74
	v_add_f32_e32 v2, v2, v79
	v_add_f32_e32 v105, v78, v72
	v_lshlrev_b32_e32 v72, 16, v75
	ds_read_b128 v[76:79], v124 offset:4480
	v_add_f32_e32 v81, v81, v72
	v_and_b32_e32 v72, 0xffff0000, v75
	v_add_f32_e32 v101, v101, v72
	ds_read_b128 v[72:75], v124 offset:5008
	s_waitcnt lgkmcnt(1)
	v_lshlrev_b32_e32 v141, 16, v77
	v_lshlrev_b32_e32 v106, 16, v76
	v_and_b32_e32 v107, 0xffff0000, v76
	v_add_f32_e32 v76, v103, v141
	v_and_b32_e32 v103, 0xffff0000, v77
	v_and_b32_e32 v142, 0xffff0000, v78
	v_add_f32_e32 v3, v3, v107
	v_add_f32_e32 v77, v104, v103
	v_lshlrev_b32_e32 v104, 16, v78
	v_add_f32_e32 v78, v105, v142
	v_lshlrev_b32_e32 v105, 16, v79
	v_and_b32_e32 v143, 0xffff0000, v79
	s_waitcnt lgkmcnt(0)
	v_lshlrev_b32_e32 v79, 16, v72
	v_and_b32_e32 v72, 0xffff0000, v72
	v_add_f32_e32 v3, v3, v72
	v_lshlrev_b32_e32 v72, 16, v73
	v_add_f32_e32 v144, v76, v72
	v_and_b32_e32 v72, 0xffff0000, v73
	v_add_f32_e32 v80, v80, v104
	v_add_f32_e32 v145, v77, v72
	v_lshlrev_b32_e32 v72, 16, v74
	v_add_f32_e32 v2, v2, v106
	v_add_f32_e32 v80, v80, v72
	v_and_b32_e32 v72, 0xffff0000, v74
	v_add_f32_e32 v2, v2, v79
	v_add_f32_e32 v146, v78, v72
	ds_read_b128 v[76:79], v124 offset:5536
	v_add_f32_e32 v81, v81, v105
	v_lshlrev_b32_e32 v72, 16, v75
	v_add_f32_e32 v101, v101, v143
	v_add_f32_e32 v81, v81, v72
	v_and_b32_e32 v72, 0xffff0000, v75
	v_add_f32_e32 v101, v101, v72
	ds_read_b128 v[72:75], v124 offset:6064
	s_waitcnt lgkmcnt(1)
	v_lshlrev_b32_e32 v147, 16, v76
	v_and_b32_e32 v76, 0xffff0000, v76
	v_add_f32_e32 v3, v3, v76
	v_lshlrev_b32_e32 v76, 16, v77
	v_add_f32_e32 v76, v144, v76
	v_lshlrev_b32_e32 v144, 16, v78
	v_add_f32_e32 v80, v80, v144
	v_lshlrev_b32_e32 v144, 16, v79
	v_and_b32_e32 v79, 0xffff0000, v79
	v_and_b32_e32 v77, 0xffff0000, v77
	v_add_f32_e32 v79, v101, v79
	s_waitcnt lgkmcnt(0)
	v_lshlrev_b32_e32 v101, 16, v72
	v_and_b32_e32 v72, 0xffff0000, v72
	v_add_f32_e32 v77, v145, v77
	v_add_f32_e32 v3, v3, v72
	v_lshlrev_b32_e32 v72, 16, v73
	v_and_b32_e32 v73, 0xffff0000, v73
	v_add_f32_e32 v72, v76, v72
	v_add_f32_e32 v73, v77, v73
	v_lshlrev_b32_e32 v76, 16, v74
	v_add_u32_e32 v77, 4, v1
	v_add_f32_e32 v76, v80, v76
	v_max_i32_e32 v80, 4, v1
	v_min_i32_e32 v77, s14, v77
	v_sub_u32_e32 v77, v77, v80
	v_add_u32_e32 v77, 4, v77
	v_cvt_f32_i32_e32 v77, v77
	v_add_f32_e32 v2, v2, v147
	v_add_f32_e32 v2, v2, v101
	v_and_b32_e32 v78, 0xffff0000, v78
	v_div_scale_f32 v80, s[10:11], v77, v77, 1.0
	v_rcp_f32_e32 v101, v80
	v_add_f32_e32 v78, v146, v78
	v_and_b32_e32 v74, 0xffff0000, v74
	v_add_f32_e32 v74, v78, v74
	v_lshlrev_b32_e32 v78, 16, v75
	v_and_b32_e32 v75, 0xffff0000, v75
	v_add_f32_e32 v75, v79, v75
	v_fma_f32 v79, -v80, v101, 1.0
	v_add_f32_e32 v81, v81, v144
	v_fmac_f32_e32 v101, v79, v101
	v_div_scale_f32 v79, vcc, 1.0, v77, 1.0
	v_add_f32_e32 v78, v81, v78
	v_mul_f32_e32 v81, v79, v101
	v_fma_f32 v144, -v80, v81, v79
	v_fmac_f32_e32 v81, v144, v101
	v_fma_f32 v79, -v80, v81, v79
	v_div_fmas_f32 v79, v79, v101, v81
	v_div_fixup_f32 v77, v79, v77, 1.0
	v_fma_f32 v79, v77, v72, -v141
	v_fma_f32 v73, v77, v73, -v103
	v_fma_f32 v76, v77, v76, -v104
	v_fma_f32 v74, v77, v74, -v142
	v_fma_f32 v78, v77, v78, -v105
	v_fma_f32 v75, v77, v75, -v143
	v_fma_f32 v2, v77, v2, -v106
	v_fma_f32 v3, v77, v3, -v107
	v_cvt_pk_bf16_f32 v72, v2, v3
	v_cvt_pk_bf16_f32 v73, v79, v73
	v_cvt_pk_bf16_f32 v74, v76, v74
	v_cvt_pk_bf16_f32 v75, v78, v75
	ds_read_b128 v[76:79], v124 offset:384
	ds_write_b128 v124, v[72:75] offset:45312
	ds_read_b128 v[72:75], v124 offset:912
	s_waitcnt lgkmcnt(2)
	v_and_b32_e32 v3, 0xffff0000, v76
	v_lshlrev_b32_e32 v81, 16, v79
	v_and_b32_e32 v79, 0xffff0000, v79
	v_lshlrev_b32_e32 v2, 16, v76
	v_add_f32_e32 v3, 0, v3
	v_lshlrev_b32_e32 v76, 16, v77
	v_add_f32_e32 v101, 0, v79
	s_waitcnt lgkmcnt(0)
	v_lshlrev_b32_e32 v79, 16, v72
	v_and_b32_e32 v72, 0xffff0000, v72
	v_add_f32_e32 v76, 0, v76
	v_and_b32_e32 v77, 0xffff0000, v77
	v_add_f32_e32 v3, v3, v72
	v_lshlrev_b32_e32 v72, 16, v73
	v_add_f32_e32 v77, 0, v77
	v_lshlrev_b32_e32 v80, 16, v78
	v_add_f32_e32 v103, v76, v72
	v_and_b32_e32 v72, 0xffff0000, v73
	v_add_f32_e32 v80, 0, v80
	v_and_b32_e32 v78, 0xffff0000, v78
	v_add_f32_e32 v104, v77, v72
	v_lshlrev_b32_e32 v72, 16, v74
	v_add_f32_e32 v2, 0, v2
	v_add_f32_e32 v78, 0, v78
	v_add_f32_e32 v80, v80, v72
	v_and_b32_e32 v72, 0xffff0000, v74
	v_add_f32_e32 v2, v2, v79
	v_add_f32_e32 v105, v78, v72
	ds_read_b128 v[76:79], v124 offset:1440
	v_add_f32_e32 v81, 0, v81
	v_lshlrev_b32_e32 v72, 16, v75
	v_add_f32_e32 v81, v81, v72
	v_and_b32_e32 v72, 0xffff0000, v75
	v_add_f32_e32 v101, v101, v72
	ds_read_b128 v[72:75], v124 offset:1968
	s_waitcnt lgkmcnt(1)
	v_lshlrev_b32_e32 v106, 16, v76
	v_and_b32_e32 v76, 0xffff0000, v76
	v_add_f32_e32 v3, v3, v76
	v_lshlrev_b32_e32 v76, 16, v77
	v_add_f32_e32 v76, v103, v76
	v_lshlrev_b32_e32 v103, 16, v78
	v_add_f32_e32 v80, v80, v103
	v_lshlrev_b32_e32 v103, 16, v79
	v_and_b32_e32 v79, 0xffff0000, v79
	v_add_f32_e32 v101, v101, v79
	s_waitcnt lgkmcnt(0)
	v_lshlrev_b32_e32 v79, 16, v72
	v_and_b32_e32 v72, 0xffff0000, v72
	v_and_b32_e32 v77, 0xffff0000, v77
	v_add_f32_e32 v3, v3, v72
	v_lshlrev_b32_e32 v72, 16, v73
	v_add_f32_e32 v77, v104, v77
	v_add_f32_e32 v81, v81, v103
	v_add_f32_e32 v103, v76, v72
	v_and_b32_e32 v72, 0xffff0000, v73
	v_and_b32_e32 v78, 0xffff0000, v78
	v_add_f32_e32 v104, v77, v72
	v_lshlrev_b32_e32 v72, 16, v74
	v_add_f32_e32 v2, v2, v106
	v_add_f32_e32 v78, v105, v78
	v_add_f32_e32 v80, v80, v72
	v_and_b32_e32 v72, 0xffff0000, v74
	v_add_f32_e32 v2, v2, v79
	v_add_f32_e32 v105, v78, v72
	ds_read_b128 v[76:79], v124 offset:2496
	v_lshlrev_b32_e32 v72, 16, v75
	v_add_f32_e32 v81, v81, v72
	v_and_b32_e32 v72, 0xffff0000, v75
	v_add_f32_e32 v101, v101, v72
	ds_read_b128 v[72:75], v124 offset:3024
	s_waitcnt lgkmcnt(1)
	v_lshlrev_b32_e32 v106, 16, v76
	v_and_b32_e32 v76, 0xffff0000, v76
	v_add_f32_e32 v3, v3, v76
	v_lshlrev_b32_e32 v76, 16, v77
	v_add_f32_e32 v76, v103, v76
	v_lshlrev_b32_e32 v103, 16, v78
	v_add_f32_e32 v80, v80, v103
	v_lshlrev_b32_e32 v103, 16, v79
	v_and_b32_e32 v79, 0xffff0000, v79
	v_add_f32_e32 v101, v101, v79
	s_waitcnt lgkmcnt(0)
	v_lshlrev_b32_e32 v79, 16, v72
	v_and_b32_e32 v72, 0xffff0000, v72
	v_and_b32_e32 v77, 0xffff0000, v77
	v_add_f32_e32 v3, v3, v72
	v_lshlrev_b32_e32 v72, 16, v73
	v_add_f32_e32 v77, v104, v77
	v_add_f32_e32 v81, v81, v103
	v_add_f32_e32 v103, v76, v72
	v_and_b32_e32 v72, 0xffff0000, v73
	v_and_b32_e32 v78, 0xffff0000, v78
	v_add_f32_e32 v104, v77, v72
	v_lshlrev_b32_e32 v72, 16, v74
	v_add_f32_e32 v2, v2, v106
	v_add_f32_e32 v78, v105, v78
	v_add_f32_e32 v80, v80, v72
	v_and_b32_e32 v72, 0xffff0000, v74
	v_add_f32_e32 v2, v2, v79
	v_add_f32_e32 v105, v78, v72
	ds_read_b128 v[76:79], v124 offset:3552
	v_lshlrev_b32_e32 v72, 16, v75
	v_add_f32_e32 v81, v81, v72
	v_and_b32_e32 v72, 0xffff0000, v75
	v_add_f32_e32 v101, v101, v72
	ds_read_b128 v[72:75], v124 offset:4080
	s_waitcnt lgkmcnt(1)
	v_lshlrev_b32_e32 v106, 16, v76
	v_and_b32_e32 v76, 0xffff0000, v76
	v_add_f32_e32 v3, v3, v76
	v_lshlrev_b32_e32 v76, 16, v77
	v_add_f32_e32 v76, v103, v76
	v_lshlrev_b32_e32 v103, 16, v78
	v_add_f32_e32 v80, v80, v103
	v_lshlrev_b32_e32 v103, 16, v79
	v_and_b32_e32 v79, 0xffff0000, v79
	v_add_f32_e32 v101, v101, v79
	s_waitcnt lgkmcnt(0)
	v_lshlrev_b32_e32 v79, 16, v72
	v_and_b32_e32 v72, 0xffff0000, v72
	v_and_b32_e32 v77, 0xffff0000, v77
	v_add_f32_e32 v3, v3, v72
	v_lshlrev_b32_e32 v72, 16, v73
	v_add_f32_e32 v77, v104, v77
	v_add_f32_e32 v81, v81, v103
	v_add_f32_e32 v103, v76, v72
	v_and_b32_e32 v72, 0xffff0000, v73
	v_and_b32_e32 v78, 0xffff0000, v78
	v_add_f32_e32 v104, v77, v72
	v_lshlrev_b32_e32 v72, 16, v74
	v_add_f32_e32 v2, v2, v106
	v_add_f32_e32 v78, v105, v78
	v_add_f32_e32 v80, v80, v72
	v_and_b32_e32 v72, 0xffff0000, v74
	v_add_f32_e32 v2, v2, v79
	v_add_f32_e32 v105, v78, v72
	v_lshlrev_b32_e32 v72, 16, v75
	ds_read_b128 v[76:79], v124 offset:4608
	v_add_f32_e32 v81, v81, v72
	v_and_b32_e32 v72, 0xffff0000, v75
	v_add_f32_e32 v101, v101, v72
	ds_read_b128 v[72:75], v124 offset:5136
	s_waitcnt lgkmcnt(1)
	v_lshlrev_b32_e32 v141, 16, v77
	v_lshlrev_b32_e32 v106, 16, v76
	v_and_b32_e32 v107, 0xffff0000, v76
	v_add_f32_e32 v76, v103, v141
	v_and_b32_e32 v103, 0xffff0000, v77
	v_and_b32_e32 v142, 0xffff0000, v78
	v_add_f32_e32 v3, v3, v107
	v_add_f32_e32 v77, v104, v103
	v_lshlrev_b32_e32 v104, 16, v78
	v_add_f32_e32 v78, v105, v142
	v_lshlrev_b32_e32 v105, 16, v79
	v_and_b32_e32 v143, 0xffff0000, v79
	s_waitcnt lgkmcnt(0)
	v_lshlrev_b32_e32 v79, 16, v72
	v_and_b32_e32 v72, 0xffff0000, v72
	v_add_f32_e32 v3, v3, v72
	v_lshlrev_b32_e32 v72, 16, v73
	v_add_f32_e32 v144, v76, v72
	v_and_b32_e32 v72, 0xffff0000, v73
	v_add_f32_e32 v80, v80, v104
	v_add_f32_e32 v145, v77, v72
	v_lshlrev_b32_e32 v72, 16, v74
	v_add_f32_e32 v2, v2, v106
	v_add_f32_e32 v80, v80, v72
	v_and_b32_e32 v72, 0xffff0000, v74
	v_add_f32_e32 v2, v2, v79
	v_add_f32_e32 v146, v78, v72
	ds_read_b128 v[76:79], v124 offset:5664
	v_add_f32_e32 v81, v81, v105
	v_lshlrev_b32_e32 v72, 16, v75
	v_add_f32_e32 v101, v101, v143
	v_add_f32_e32 v81, v81, v72
	v_and_b32_e32 v72, 0xffff0000, v75
	v_add_f32_e32 v101, v101, v72
	ds_read_b128 v[72:75], v124 offset:6192
	s_waitcnt lgkmcnt(1)
	v_lshlrev_b32_e32 v147, 16, v76
	v_and_b32_e32 v76, 0xffff0000, v76
	v_add_f32_e32 v3, v3, v76
	v_lshlrev_b32_e32 v76, 16, v77
	v_add_f32_e32 v76, v144, v76
	v_lshlrev_b32_e32 v144, 16, v78
	v_add_f32_e32 v80, v80, v144
	v_lshlrev_b32_e32 v144, 16, v79
	v_and_b32_e32 v79, 0xffff0000, v79
	v_add_f32_e32 v101, v101, v79
	s_waitcnt lgkmcnt(0)
	v_lshlrev_b32_e32 v79, 16, v72
	v_and_b32_e32 v72, 0xffff0000, v72
	v_and_b32_e32 v77, 0xffff0000, v77
	v_add_f32_e32 v3, v3, v72
	v_lshlrev_b32_e32 v72, 16, v73
	v_add_f32_e32 v77, v145, v77
	v_add_f32_e32 v81, v81, v144
	v_add_f32_e32 v144, v76, v72
	v_and_b32_e32 v72, 0xffff0000, v73
	v_and_b32_e32 v78, 0xffff0000, v78
	v_add_f32_e32 v145, v77, v72
	v_lshlrev_b32_e32 v72, 16, v74
	v_add_f32_e32 v2, v2, v147
	v_add_f32_e32 v78, v146, v78
	v_add_f32_e32 v80, v80, v72
	v_and_b32_e32 v72, 0xffff0000, v74
	v_add_f32_e32 v2, v2, v79
	v_add_f32_e32 v146, v78, v72
	ds_read_b128 v[76:79], v124 offset:6720
	v_lshlrev_b32_e32 v72, 16, v75
	v_add_f32_e32 v81, v81, v72
	v_and_b32_e32 v72, 0xffff0000, v75
	v_add_f32_e32 v101, v101, v72
	ds_read_b128 v[72:75], v124 offset:7248
	s_waitcnt lgkmcnt(1)
	v_lshlrev_b32_e32 v147, 16, v76
	v_and_b32_e32 v76, 0xffff0000, v76
	v_add_f32_e32 v3, v3, v76
	v_lshlrev_b32_e32 v76, 16, v77
	v_add_f32_e32 v76, v144, v76
	v_lshlrev_b32_e32 v144, 16, v78
	v_add_f32_e32 v80, v80, v144
	v_lshlrev_b32_e32 v144, 16, v79
	v_and_b32_e32 v79, 0xffff0000, v79
	v_add_f32_e32 v101, v101, v79
	s_waitcnt lgkmcnt(0)
	v_lshlrev_b32_e32 v79, 16, v72
	v_and_b32_e32 v72, 0xffff0000, v72
	v_and_b32_e32 v77, 0xffff0000, v77
	v_add_f32_e32 v3, v3, v72
	v_lshlrev_b32_e32 v72, 16, v73
	v_add_f32_e32 v77, v145, v77
	v_add_f32_e32 v81, v81, v144
	v_add_f32_e32 v144, v76, v72
	v_and_b32_e32 v72, 0xffff0000, v73
	v_and_b32_e32 v78, 0xffff0000, v78
	v_add_f32_e32 v145, v77, v72
	v_lshlrev_b32_e32 v72, 16, v74
	v_add_f32_e32 v2, v2, v147
	v_add_f32_e32 v78, v146, v78
	v_add_f32_e32 v80, v80, v72
	v_and_b32_e32 v72, 0xffff0000, v74
	v_add_f32_e32 v2, v2, v79
	v_add_f32_e32 v146, v78, v72
	ds_read_b128 v[76:79], v124 offset:7776
	v_lshlrev_b32_e32 v72, 16, v75
	v_add_f32_e32 v81, v81, v72
	v_and_b32_e32 v72, 0xffff0000, v75
	v_add_f32_e32 v101, v101, v72
	ds_read_b128 v[72:75], v124 offset:8304
	s_waitcnt lgkmcnt(1)
	v_lshlrev_b32_e32 v147, 16, v76
	v_and_b32_e32 v76, 0xffff0000, v76
	v_add_f32_e32 v3, v3, v76
	v_lshlrev_b32_e32 v76, 16, v77
	v_add_f32_e32 v76, v144, v76
	v_lshlrev_b32_e32 v144, 16, v78
	v_add_f32_e32 v80, v80, v144
	v_lshlrev_b32_e32 v144, 16, v79
	v_and_b32_e32 v79, 0xffff0000, v79
	v_and_b32_e32 v77, 0xffff0000, v77
	v_add_f32_e32 v79, v101, v79
	s_waitcnt lgkmcnt(0)
	v_lshlrev_b32_e32 v101, 16, v72
	v_and_b32_e32 v72, 0xffff0000, v72
	v_add_f32_e32 v77, v145, v77
	v_add_f32_e32 v3, v3, v72
	v_lshlrev_b32_e32 v72, 16, v73
	v_and_b32_e32 v73, 0xffff0000, v73
	v_add_f32_e32 v73, v77, v73
	v_add_u32_e32 v77, 8, v1
	v_max_i32_e32 v1, 8, v1
	v_min_i32_e32 v77, s14, v77
	v_sub_u32_e32 v1, v77, v1
	v_add_u32_e32 v1, 8, v1
	v_cvt_f32_i32_e32 v1, v1
	v_and_b32_e32 v78, 0xffff0000, v78
	v_add_f32_e32 v78, v146, v78
	v_add_f32_e32 v72, v76, v72
	v_lshlrev_b32_e32 v76, 16, v74
	v_and_b32_e32 v74, 0xffff0000, v74
	v_add_f32_e32 v74, v78, v74
	v_div_scale_f32 v78, s[10:11], v1, v1, 1.0
	v_add_f32_e32 v76, v80, v76
	v_rcp_f32_e32 v80, v78
	v_lshlrev_b32_e32 v77, 16, v75
	v_and_b32_e32 v75, 0xffff0000, v75
	v_add_f32_e32 v75, v79, v75
	v_fma_f32 v79, -v78, v80, 1.0
	v_add_f32_e32 v81, v81, v144
	v_fmac_f32_e32 v80, v79, v80
	v_div_scale_f32 v79, vcc, 1.0, v1, 1.0
	v_add_f32_e32 v2, v2, v147
	v_add_f32_e32 v77, v81, v77
	v_mul_f32_e32 v81, v79, v80
	v_add_f32_e32 v2, v2, v101
	v_fma_f32 v101, -v78, v81, v79
	v_fmac_f32_e32 v81, v101, v80
	v_fma_f32 v78, -v78, v81, v79
	v_div_fmas_f32 v78, v78, v80, v81
	v_div_fixup_f32 v1, v78, v1, 1.0
	v_fma_f32 v73, v1, v73, -v103
	v_fma_f32 v74, v1, v74, -v142
	v_fma_f32 v2, v1, v2, -v106
	v_fma_f32 v3, v1, v3, -v107
	v_fma_f32 v78, v1, v72, -v141
	v_fma_f32 v76, v1, v76, -v104
	v_fma_f32 v77, v1, v77, -v105
	v_fma_f32 v1, v1, v75, -v143
	v_cvt_pk_bf16_f32 v72, v2, v3
	v_cvt_pk_bf16_f32 v73, v78, v73
	v_cvt_pk_bf16_f32 v74, v76, v74
	v_cvt_pk_bf16_f32 v75, v77, v1
	ds_write_b128 v124, v[72:75] offset:45440
	s_waitcnt lgkmcnt(0)
	s_barrier
	ds_read_b128 v[72:75], v140 offset:45056
	ds_read_b128 v[162:165], v140 offset:45120
	s_waitcnt lgkmcnt(1)
	v_mfma_f32_16x16x32_bf16 v[76:79], v[4:7], v[72:75], 0
	ds_read_b128 v[146:149], v140 offset:53504
	v_or_b32_e32 v1, s26, v115
	v_add_u32_e32 v2, s27, v1
	v_mfma_f32_16x16x32_bf16 v[104:107], v[8:11], v[72:75], 0
	v_ashrrev_i32_e32 v3, 31, v2
	v_lshlrev_b64 v[2:3], 10, v[2:3]
	v_lshl_add_u64 v[2:3], v[98:99], 0, v[2:3]
	s_waitcnt lgkmcnt(1)
	v_mfma_f32_16x16x32_bf16 v[76:79], v[20:23], v[162:165], v[76:79]
	v_mfma_f32_16x16x32_bf16 v[104:107], v[24:27], v[162:165], v[104:107]
	v_mfma_f32_16x16x32_bf16 v[142:145], v[12:15], v[72:75], 0
	s_nop 5
	v_mul_f32_e64 v80, v76, v56
	v_mul_f32_e64 v81, v77, v57
	v_cvt_pk_fp8_f32 v76, v80, v81
	v_mfma_f32_16x16x32_bf16 v[72:75], v[16:19], v[72:75], 0
	v_mul_f32_e64 v80, v104, v64
	v_mul_f32_e64 v81, v105, v65
	v_cvt_pk_fp8_f32 v77, v80, v81
	v_mfma_f32_16x16x32_bf16 v[142:145], v[28:31], v[162:165], v[142:145]
	v_mul_f32_e64 v78, v78, v58
	v_mul_f32_e64 v79, v79, v59
	v_cvt_pk_fp8_f32 v76, v78, v79 op_sel:[0,0,1]
	v_mfma_f32_16x16x32_bf16 v[72:75], v[32:35], v[162:165], v[72:75]
	ds_read_b128 v[162:165], v140 offset:53568
	v_pk_mul_f32 v[78:79], v[106:107], v[66:67]
	s_nop 1
	v_pk_mul_f32 v[80:81], v[142:143], v[60:61]
	s_waitcnt lgkmcnt(1)
	v_mfma_f32_16x16x32_bf16 v[150:153], v[4:7], v[146:149], 0
	v_cvt_pk_fp8_f32 v77, v78, v79 op_sel:[0,0,1]
	v_cvt_pk_fp8_f32 v78, v80, v81
	v_mfma_f32_16x16x32_bf16 v[154:157], v[8:11], v[146:149], 0
	v_mul_f32_e64 v72, v72, v68
	v_mul_f32_e64 v73, v73, v69
	v_cvt_pk_fp8_f32 v79, v72, v73
	s_waitcnt lgkmcnt(0)
	v_mfma_f32_16x16x32_bf16 v[150:153], v[20:23], v[162:165], v[150:153]
	v_mul_f32_e64 v72, v144, v62
	v_mul_f32_e64 v73, v145, v63
	v_cvt_pk_fp8_f32 v78, v72, v73 op_sel:[0,0,1]
	v_mfma_f32_16x16x32_bf16 v[154:157], v[24:27], v[162:165], v[154:157]
	v_mul_f32_e64 v72, v74, v70
	v_mul_f32_e64 v73, v75, v71
	s_nop 1
	v_pk_mul_f32 v[74:75], v[150:151], v[56:57]
	v_cvt_pk_fp8_f32 v79, v72, v73 op_sel:[0,0,1]
	v_mfma_f32_16x16x32_bf16 v[158:161], v[12:15], v[146:149], 0
	v_cvt_pk_fp8_f32 v72, v74, v75
	v_pk_mul_f32 v[74:75], v[154:155], v[64:65]
	v_mfma_f32_16x16x32_bf16 v[146:149], v[16:19], v[146:149], 0
	v_cvt_pk_fp8_f32 v73, v74, v75
	v_permlane32_swap_b32_e32 v76, v78
	v_mfma_f32_16x16x32_bf16 v[158:161], v[28:31], v[162:165], v[158:161]
	v_permlane32_swap_b32_e32 v77, v79
	v_pk_mul_f32 v[74:75], v[152:153], v[58:59]
	v_mfma_f32_16x16x32_bf16 v[146:149], v[32:35], v[162:165], v[146:149]
	v_permlane16_swap_b32_e32 v76, v77
	v_permlane16_swap_b32_e32 v78, v79
	v_cvt_pk_fp8_f32 v72, v74, v75 op_sel:[0,0,1]
	v_pk_mul_f32 v[74:75], v[156:157], v[66:67]
	global_store_dwordx4 v[2:3], v[76:79], off offset:512
	v_cvt_pk_fp8_f32 v73, v74, v75 op_sel:[0,0,1]
	v_pk_mul_f32 v[76:77], v[158:159], v[60:61]
	v_cvt_pk_fp8_f32 v74, v76, v77
	v_pk_mul_f32 v[76:77], v[146:147], v[68:69]
	v_add_co_u32_e32 v2, vcc, 0x4000, v2
	v_cvt_pk_fp8_f32 v75, v76, v77
	v_pk_mul_f32 v[76:77], v[160:161], v[62:63]
	v_addc_co_u32_e32 v3, vcc, 0, v3, vcc
	v_cvt_pk_fp8_f32 v74, v76, v77 op_sel:[0,0,1]
	v_pk_mul_f32 v[76:77], v[148:149], v[70:71]
	s_andn2_b64 vcc, exec, s[20:21]
	v_cvt_pk_fp8_f32 v75, v76, v77 op_sel:[0,0,1]
	v_permlane32_swap_b32_e32 v72, v74
	s_nop 0
	v_permlane32_swap_b32_e32 v73, v75
	s_nop 1
	v_permlane16_swap_b32_e32 v72, v73
	v_permlane16_swap_b32_e32 v74, v75
	global_store_dwordx4 v[2:3], v[72:75], off offset:512
	s_cbranch_vccnz .LBB0_578
	s_waitcnt vmcnt(0)
	s_barrier
	s_and_saveexec_b64 s[94:95], s[0:1]
	s_cbranch_execz .LBB0_577
	s_mov_b64 s[10:11], exec
	v_mbcnt_lo_u32_b32 v1, s10, 0
	buffer_wbl2 sc1
	s_waitcnt vmcnt(0)
	s_waitcnt vmcnt(0)
	v_mbcnt_hi_u32_b32 v1, s11, v1
	v_cmp_eq_u32_e32 vcc, 0, v1
	s_and_b64 s[14:15], exec, vcc
	s_mov_b64 exec, s[14:15]
	s_cbranch_execz .LBB0_577
	s_bcnt1_i32_b64 s10, s[10:11]
	v_mov_b32_e32 v1, s10
	global_atomic_add v0, v1, s[84:85]
	s_branch .LBB0_577

.LBB0_783:
	s_sub_i32 s11, s10, 24
	s_min_i32 s6, s11, s2
	s_ashr_i32 s7, s6, 31
	s_lshl_b64 s[6:7], s[6:7], 11
	s_waitcnt lgkmcnt(0)
	v_lshl_add_u64 v[60:61], v[34:35], 0, s[6:7]
	global_load_dwordx2 v[66:67], v[60:61], off
	global_load_dwordx2 v[64:65], v[60:61], off offset:512
	global_load_dwordx2 v[62:63], v[60:61], off offset:1024
	s_nop 0
	global_load_dwordx2 v[60:61], v[60:61], off offset:1536
	s_waitcnt vmcnt(4)
	v_and_b32_e32 v77, 0xffff0000, v58
	v_and_b32_e32 v75, 0xffff0000, v59
	v_lshlrev_b32_e32 v76, 16, v58
	v_lshlrev_b32_e32 v74, 16, v59
	v_lshlrev_b32_e32 v72, 16, v56
	v_and_b32_e32 v73, 0xffff0000, v56
	v_lshlrev_b32_e32 v70, 16, v57
	v_and_b32_e32 v71, 0xffff0000, v57
	v_lshlrev_b32_e32 v68, 16, v54
	v_and_b32_e32 v69, 0xffff0000, v54
	v_lshlrev_b32_e32 v58, 16, v55
	v_and_b32_e32 v59, 0xffff0000, v55
	v_lshlrev_b32_e32 v56, 16, v52
	v_and_b32_e32 v57, 0xffff0000, v52
	v_lshlrev_b32_e32 v54, 16, v53
	v_and_b32_e32 v55, 0xffff0000, v53
	v_mul_f32_e32 v52, v77, v77
	v_mul_f32_e32 v53, v75, v75
	v_fmac_f32_e32 v52, v76, v76
	v_fmac_f32_e32 v53, v74, v74
	v_add_f32_e32 v52, v52, v53
	v_mul_f32_e32 v53, v73, v73
	v_mul_f32_e32 v80, v71, v71
	v_fmac_f32_e32 v53, v72, v72
	v_fmac_f32_e32 v80, v70, v70
	v_add_f32_e32 v53, v53, v80
	v_add_f32_e32 v52, v52, v53
	v_mul_f32_e32 v53, v69, v69
	v_mul_f32_e32 v80, v59, v59
	v_fmac_f32_e32 v53, v68, v68
	v_fmac_f32_e32 v80, v58, v58
	v_add_f32_e32 v53, v53, v80
	v_add_f32_e32 v52, v52, v53
	v_mul_f32_e32 v53, v57, v57
	v_mul_f32_e32 v80, v55, v55
	v_fmac_f32_e32 v53, v56, v56
	v_fmac_f32_e32 v80, v54, v54
	v_add_f32_e32 v53, v53, v80
	v_add_f32_e32 v52, v52, v53
	s_sub_i32 s13, s10, 48
	s_cmp_ge_i32 s13, s67
	s_waitcnt lgkmcnt(0)
	s_nop 1
	v_add_f32_dpp v52, v52, v52 quad_perm:[1,0,3,2] row_mask:0xf bank_mask:0xf
	s_waitcnt lgkmcnt(0)
	s_nop 1
	v_add_f32_dpp v52, v52, v52 quad_perm:[2,3,0,1] row_mask:0xf bank_mask:0xf
	s_waitcnt lgkmcnt(0)
	s_nop 1
	v_add_f32_dpp v52, v52, v52 row_half_mirror row_mask:0xf bank_mask:0xf
	s_waitcnt lgkmcnt(0)
	s_nop 1
	v_add_f32_dpp v52, v52, v52 row_mirror row_mask:0xf bank_mask:0xf
	s_waitcnt lgkmcnt(0)
	s_nop 1
	v_add_f32_dpp v52, v52, v52 row_bcast:15 row_mask:0xa bank_mask:0xf
	s_cbranch_scc1 .LBB0_789
	s_waitcnt lgkmcnt(0)
	s_nop 1
	v_add_f32_dpp v52, v52, v52 row_bcast:31 row_mask:0xc bank_mask:0xf
	s_nop 0
	v_readlane_b32 s101, v52, 63
	s_nop 1
	v_mov_b32_e32 v52, s101
	v_fmamk_f32 v52, v52, 0x3a800000, v210
	v_rsq_f32_e32 v52, v52
	s_add_i32 s6, s88, s10
	s_sub_i32 s6, s6, 48
	s_ashr_i32 s7, s6, 31
	v_pk_mul_f32 v[76:77], v[52:53], v[76:77] op_sel_hi:[0,1]
	v_pk_mul_f32 v[74:75], v[52:53], v[74:75] op_sel_hi:[0,1]
	v_pk_fma_f32 v[76:77], v[76:77], v[20:21], v[2:3]
	v_mov_b32_e32 v53, v0
	v_cvt_pk_fp8_f32 v53, v76, v77
	v_pk_fma_f32 v[74:75], v[74:75], v[18:19], v[4:5]
	s_lshl_b64 s[6:7], s[6:7], 10
	v_pk_mul_f32 v[72:73], v[52:53], v[72:73] op_sel_hi:[0,1]
	v_cvt_pk_fp8_f32 v53, v74, v75 op_sel:[0,0,1]
	v_pk_fma_f32 v[72:73], v[72:73], v[24:25], v[6:7]
	v_lshl_add_u64 v[80:81], v[112:113], 0, s[6:7]
	v_cvt_pk_fp8_f32 v76, v72, v73
	v_pk_mul_f32 v[70:71], v[52:53], v[70:71] op_sel_hi:[0,1]
	v_pk_fma_f32 v[70:71], v[70:71], v[22:23], v[8:9]
	v_pk_mul_f32 v[68:69], v[52:53], v[68:69] op_sel_hi:[0,1]
	v_cvt_pk_fp8_f32 v76, v70, v71 op_sel:[0,0,1]
	v_pk_fma_f32 v[68:69], v[68:69], v[28:29], v[10:11]
	v_pk_mul_f32 v[56:57], v[52:53], v[56:57] op_sel_hi:[0,1]
	v_cvt_pk_fp8_f32 v70, v68, v69
	v_pk_fma_f32 v[56:57], v[56:57], v[32:33], v[14:15]
	v_cvt_pk_fp8_f32 v68, v56, v57
	v_pk_mul_f32 v[58:59], v[52:53], v[58:59] op_sel_hi:[0,1]
	v_pk_fma_f32 v[58:59], v[58:59], v[26:27], v[12:13]
	v_pk_mul_f32 v[54:55], v[52:53], v[54:55] op_sel_hi:[0,1]
	v_cvt_pk_fp8_f32 v70, v58, v59 op_sel:[0,0,1]
	v_pk_fma_f32 v[54:55], v[54:55], v[30:31], v[16:17]
	s_nop 0
	v_cvt_pk_fp8_f32 v68, v54, v55 op_sel:[0,0,1]
	global_store_dword v[80:81], v53, off
	global_store_dword v[80:81], v76, off offset:256
	global_store_dword v[80:81], v70, off offset:512
	global_store_dword v[80:81], v68, off offset:768
	s_and_saveexec_b64 s[6:7], s[4:5]
	s_cbranch_execz .LBB0_788
	s_sub_i32 s14, s9, 32
	s_and_b32 s14, s14, 0x3ffffff0
	v_lshl_add_u32 v53, s14, 2, v161
	ds_read_b32 v54, v53
	s_cmpk_lt_i32 s13, 0x80
	s_cbranch_scc1 .LBB0_787
	s_waitcnt lgkmcnt(0)
	ds_read2st64_b32 v[54:55], v79 offset1:4
	s_waitcnt lgkmcnt(0)
	v_add_f32_e32 v54, 0, v54
	v_add_f32_e32 v56, v54, v55
	ds_read2st64_b32 v[54:55], v79 offset0:8 offset1:12
	s_waitcnt lgkmcnt(0)
	v_add_f32_e32 v54, v56, v54
	v_add_f32_e32 v56, v54, v55
	ds_read2st64_b32 v[54:55], v79 offset0:16 offset1:20
	s_waitcnt lgkmcnt(0)
	v_add_f32_e32 v54, v56, v54
	v_add_f32_e32 v56, v54, v55
	ds_read2st64_b32 v[54:55], v79 offset0:24 offset1:28
	s_waitcnt lgkmcnt(0)
	v_add_f32_e32 v54, v56, v54
	v_add_f32_e32 v54, v54, v55

.LBB0_789:
	s_add_i32 s6, s10, -16
	s_min_i32 s6, s6, s2
	s_ashr_i32 s7, s6, 31
	s_lshl_b64 s[6:7], s[6:7], 11
	s_waitcnt lgkmcnt(0)
	v_lshl_add_u64 v[52:53], v[34:35], 0, s[6:7]
	global_load_dwordx2 v[58:59], v[52:53], off
	global_load_dwordx2 v[56:57], v[52:53], off offset:512
	global_load_dwordx2 v[54:55], v[52:53], off offset:1024
	s_nop 0
	global_load_dwordx2 v[52:53], v[52:53], off offset:1536
	v_and_b32_e32 v77, 0xffff0000, v50
	v_and_b32_e32 v75, 0xffff0000, v51
	v_lshlrev_b32_e32 v76, 16, v50
	v_lshlrev_b32_e32 v74, 16, v51
	v_lshlrev_b32_e32 v72, 16, v48
	v_and_b32_e32 v73, 0xffff0000, v48
	v_lshlrev_b32_e32 v70, 16, v49
	v_and_b32_e32 v71, 0xffff0000, v49
	v_lshlrev_b32_e32 v68, 16, v46
	v_and_b32_e32 v69, 0xffff0000, v46
	v_lshlrev_b32_e32 v50, 16, v47
	v_and_b32_e32 v51, 0xffff0000, v47
	v_lshlrev_b32_e32 v48, 16, v44
	v_and_b32_e32 v49, 0xffff0000, v44
	v_lshlrev_b32_e32 v46, 16, v45
	v_and_b32_e32 v47, 0xffff0000, v45
	v_mul_f32_e32 v44, v77, v77
	v_mul_f32_e32 v45, v75, v75
	v_fmac_f32_e32 v44, v76, v76
	v_fmac_f32_e32 v45, v74, v74
	v_add_f32_e32 v44, v44, v45
	v_mul_f32_e32 v45, v73, v73
	v_mul_f32_e32 v80, v71, v71
	v_fmac_f32_e32 v45, v72, v72
	v_fmac_f32_e32 v80, v70, v70
	v_add_f32_e32 v45, v45, v80
	v_add_f32_e32 v44, v44, v45
	v_mul_f32_e32 v45, v69, v69
	v_mul_f32_e32 v80, v51, v51
	v_fmac_f32_e32 v45, v68, v68
	v_fmac_f32_e32 v80, v50, v50
	v_add_f32_e32 v45, v45, v80
	v_add_f32_e32 v44, v44, v45
	v_mul_f32_e32 v45, v49, v49
	v_mul_f32_e32 v80, v47, v47
	v_fmac_f32_e32 v45, v48, v48
	v_fmac_f32_e32 v80, v46, v46
	v_add_f32_e32 v45, v45, v80
	v_add_f32_e32 v44, v44, v45
	s_sub_i32 s13, s10, 40
	s_cmp_ge_i32 s13, s67
	s_waitcnt lgkmcnt(0)
	s_nop 1
	v_add_f32_dpp v44, v44, v44 quad_perm:[1,0,3,2] row_mask:0xf bank_mask:0xf
	s_waitcnt lgkmcnt(0)
	s_nop 1
	v_add_f32_dpp v44, v44, v44 quad_perm:[2,3,0,1] row_mask:0xf bank_mask:0xf
	s_waitcnt lgkmcnt(0)
	s_nop 1
	v_add_f32_dpp v44, v44, v44 row_half_mirror row_mask:0xf bank_mask:0xf
	s_waitcnt lgkmcnt(0)
	s_nop 1
	v_add_f32_dpp v44, v44, v44 row_mirror row_mask:0xf bank_mask:0xf
	s_waitcnt lgkmcnt(0)
	s_nop 1
	v_add_f32_dpp v44, v44, v44 row_bcast:15 row_mask:0xa bank_mask:0xf
	s_cbranch_scc1 .LBB0_795
	s_waitcnt lgkmcnt(0)
	s_nop 1
	v_add_f32_dpp v44, v44, v44 row_bcast:31 row_mask:0xc bank_mask:0xf
	s_nop 0
	v_readlane_b32 s101, v44, 63
	s_nop 1
	v_mov_b32_e32 v44, s101
	v_fmamk_f32 v44, v44, 0x3a800000, v210
	v_rsq_f32_e32 v44, v44
	s_add_i32 s6, s88, s10
	s_sub_i32 s6, s6, 40
	s_ashr_i32 s7, s6, 31
	v_pk_mul_f32 v[76:77], v[44:45], v[76:77] op_sel_hi:[0,1]
	v_pk_mul_f32 v[74:75], v[44:45], v[74:75] op_sel_hi:[0,1]
	v_pk_fma_f32 v[76:77], v[76:77], v[20:21], v[2:3]
	v_mov_b32_e32 v45, v0
	v_cvt_pk_fp8_f32 v45, v76, v77
	v_pk_fma_f32 v[74:75], v[74:75], v[18:19], v[4:5]
	s_lshl_b64 s[6:7], s[6:7], 10
	v_pk_mul_f32 v[72:73], v[44:45], v[72:73] op_sel_hi:[0,1]
	v_cvt_pk_fp8_f32 v45, v74, v75 op_sel:[0,0,1]
	v_pk_fma_f32 v[72:73], v[72:73], v[24:25], v[6:7]
	v_lshl_add_u64 v[80:81], v[112:113], 0, s[6:7]
	v_cvt_pk_fp8_f32 v76, v72, v73
	v_pk_mul_f32 v[70:71], v[44:45], v[70:71] op_sel_hi:[0,1]
	v_pk_fma_f32 v[70:71], v[70:71], v[22:23], v[8:9]
	v_pk_mul_f32 v[68:69], v[44:45], v[68:69] op_sel_hi:[0,1]
	v_cvt_pk_fp8_f32 v76, v70, v71 op_sel:[0,0,1]
	v_pk_fma_f32 v[68:69], v[68:69], v[28:29], v[10:11]
	v_pk_mul_f32 v[48:49], v[44:45], v[48:49] op_sel_hi:[0,1]
	v_cvt_pk_fp8_f32 v70, v68, v69
	v_pk_fma_f32 v[48:49], v[48:49], v[32:33], v[14:15]
	v_cvt_pk_fp8_f32 v68, v48, v49
	v_pk_mul_f32 v[50:51], v[44:45], v[50:51] op_sel_hi:[0,1]
	v_pk_fma_f32 v[50:51], v[50:51], v[26:27], v[12:13]
	v_pk_mul_f32 v[46:47], v[44:45], v[46:47] op_sel_hi:[0,1]
	v_cvt_pk_fp8_f32 v70, v50, v51 op_sel:[0,0,1]
	v_pk_fma_f32 v[46:47], v[46:47], v[30:31], v[16:17]
	s_nop 0
	v_cvt_pk_fp8_f32 v68, v46, v47 op_sel:[0,0,1]
	global_store_dword v[80:81], v45, off
	global_store_dword v[80:81], v76, off offset:256
	global_store_dword v[80:81], v70, off offset:512
	global_store_dword v[80:81], v68, off offset:768
	s_and_saveexec_b64 s[6:7], s[4:5]
	s_cbranch_execz .LBB0_794
	s_add_i32 s14, s9, -16
	s_and_b32 s14, s14, 0x3ffffff0
	v_lshl_add_u32 v45, s14, 2, v161
	ds_read_b32 v46, v45
	s_cmpk_lt_i32 s13, 0x80
	s_cbranch_scc1 .LBB0_793
	s_waitcnt lgkmcnt(0)
	ds_read2st64_b32 v[46:47], v79 offset0:2 offset1:6
	s_waitcnt lgkmcnt(0)
	v_add_f32_e32 v46, 0, v46
	v_add_f32_e32 v48, v46, v47
	ds_read2st64_b32 v[46:47], v79 offset0:10 offset1:14
	s_waitcnt lgkmcnt(0)
	v_add_f32_e32 v46, v48, v46
	v_add_f32_e32 v48, v46, v47
	ds_read2st64_b32 v[46:47], v79 offset0:18 offset1:22
	s_waitcnt lgkmcnt(0)
	v_add_f32_e32 v46, v48, v46
	v_add_f32_e32 v48, v46, v47
	ds_read2st64_b32 v[46:47], v79 offset0:26 offset1:30
	s_waitcnt lgkmcnt(0)
	v_add_f32_e32 v46, v48, v46
	v_add_f32_e32 v46, v46, v47

.LBB0_795:
	s_add_i32 s6, s10, -8
	s_min_i32 s6, s6, s2
	s_ashr_i32 s7, s6, 31
	s_lshl_b64 s[6:7], s[6:7], 11
	s_waitcnt lgkmcnt(0)
	v_lshl_add_u64 v[44:45], v[34:35], 0, s[6:7]
	global_load_dwordx2 v[50:51], v[44:45], off
	global_load_dwordx2 v[48:49], v[44:45], off offset:512
	global_load_dwordx2 v[46:47], v[44:45], off offset:1024
	s_nop 0
	global_load_dwordx2 v[44:45], v[44:45], off offset:1536
	v_and_b32_e32 v77, 0xffff0000, v42
	v_and_b32_e32 v75, 0xffff0000, v43
	v_lshlrev_b32_e32 v76, 16, v42
	v_lshlrev_b32_e32 v74, 16, v43
	v_lshlrev_b32_e32 v72, 16, v40
	v_and_b32_e32 v73, 0xffff0000, v40
	v_lshlrev_b32_e32 v70, 16, v41
	v_and_b32_e32 v71, 0xffff0000, v41
	v_lshlrev_b32_e32 v68, 16, v38
	v_and_b32_e32 v69, 0xffff0000, v38
	v_lshlrev_b32_e32 v42, 16, v39
	v_and_b32_e32 v43, 0xffff0000, v39
	v_lshlrev_b32_e32 v40, 16, v36
	v_and_b32_e32 v41, 0xffff0000, v36
	v_lshlrev_b32_e32 v38, 16, v37
	v_and_b32_e32 v39, 0xffff0000, v37
	v_mul_f32_e32 v36, v77, v77
	v_mul_f32_e32 v37, v75, v75
	v_fmac_f32_e32 v36, v76, v76
	v_fmac_f32_e32 v37, v74, v74
	v_add_f32_e32 v36, v36, v37
	v_mul_f32_e32 v37, v73, v73
	v_mul_f32_e32 v80, v71, v71
	v_fmac_f32_e32 v37, v72, v72
	v_fmac_f32_e32 v80, v70, v70
	v_add_f32_e32 v37, v37, v80
	v_add_f32_e32 v36, v36, v37
	v_mul_f32_e32 v37, v69, v69
	v_mul_f32_e32 v80, v43, v43
	v_fmac_f32_e32 v37, v68, v68
	v_fmac_f32_e32 v80, v42, v42
	v_add_f32_e32 v37, v37, v80
	v_add_f32_e32 v36, v36, v37
	v_mul_f32_e32 v37, v41, v41
	v_mul_f32_e32 v80, v39, v39
	v_fmac_f32_e32 v37, v40, v40
	v_fmac_f32_e32 v80, v38, v38
	v_add_f32_e32 v37, v37, v80
	v_add_f32_e32 v36, v36, v37
	s_sub_i32 s13, s10, 32
	s_cmp_ge_i32 s13, s67
	s_waitcnt lgkmcnt(0)
	s_nop 1
	v_add_f32_dpp v36, v36, v36 quad_perm:[1,0,3,2] row_mask:0xf bank_mask:0xf
	s_waitcnt lgkmcnt(0)
	s_nop 1
	v_add_f32_dpp v36, v36, v36 quad_perm:[2,3,0,1] row_mask:0xf bank_mask:0xf
	s_waitcnt lgkmcnt(0)
	s_nop 1
	v_add_f32_dpp v36, v36, v36 row_half_mirror row_mask:0xf bank_mask:0xf
	s_waitcnt lgkmcnt(0)
	s_nop 1
	v_add_f32_dpp v36, v36, v36 row_mirror row_mask:0xf bank_mask:0xf
	s_waitcnt lgkmcnt(0)
	s_nop 1
	v_add_f32_dpp v36, v36, v36 row_bcast:15 row_mask:0xa bank_mask:0xf
	s_cbranch_scc1 .LBB0_801
	s_waitcnt lgkmcnt(0)
	s_nop 1
	v_add_f32_dpp v36, v36, v36 row_bcast:31 row_mask:0xc bank_mask:0xf
	s_nop 0
	v_readlane_b32 s101, v36, 63
	s_nop 1
	v_mov_b32_e32 v36, s101
	v_fmamk_f32 v36, v36, 0x3a800000, v210
	v_rsq_f32_e32 v36, v36
	s_add_i32 s6, s88, s10
	s_sub_i32 s6, s6, 32
	s_ashr_i32 s7, s6, 31
	v_pk_mul_f32 v[76:77], v[36:37], v[76:77] op_sel_hi:[0,1]
	v_pk_mul_f32 v[74:75], v[36:37], v[74:75] op_sel_hi:[0,1]
	v_pk_fma_f32 v[76:77], v[76:77], v[20:21], v[2:3]
	v_mov_b32_e32 v37, v0
	v_cvt_pk_fp8_f32 v37, v76, v77
	v_pk_fma_f32 v[74:75], v[74:75], v[18:19], v[4:5]
	s_lshl_b64 s[6:7], s[6:7], 10
	v_pk_mul_f32 v[72:73], v[36:37], v[72:73] op_sel_hi:[0,1]
	v_cvt_pk_fp8_f32 v37, v74, v75 op_sel:[0,0,1]
	v_pk_fma_f32 v[72:73], v[72:73], v[24:25], v[6:7]
	v_lshl_add_u64 v[80:81], v[112:113], 0, s[6:7]
	v_cvt_pk_fp8_f32 v76, v72, v73
	v_pk_mul_f32 v[70:71], v[36:37], v[70:71] op_sel_hi:[0,1]
	v_pk_fma_f32 v[70:71], v[70:71], v[22:23], v[8:9]
	v_pk_mul_f32 v[68:69], v[36:37], v[68:69] op_sel_hi:[0,1]
	v_cvt_pk_fp8_f32 v76, v70, v71 op_sel:[0,0,1]
	v_pk_fma_f32 v[68:69], v[68:69], v[28:29], v[10:11]
	v_pk_mul_f32 v[40:41], v[36:37], v[40:41] op_sel_hi:[0,1]
	v_cvt_pk_fp8_f32 v70, v68, v69
	v_pk_fma_f32 v[40:41], v[40:41], v[32:33], v[14:15]
	v_cvt_pk_fp8_f32 v68, v40, v41
	v_pk_mul_f32 v[42:43], v[36:37], v[42:43] op_sel_hi:[0,1]
	v_pk_fma_f32 v[42:43], v[42:43], v[26:27], v[12:13]
	v_pk_mul_f32 v[38:39], v[36:37], v[38:39] op_sel_hi:[0,1]
	v_cvt_pk_fp8_f32 v70, v42, v43 op_sel:[0,0,1]
	v_pk_fma_f32 v[38:39], v[38:39], v[30:31], v[16:17]
	s_nop 0
	v_cvt_pk_fp8_f32 v68, v38, v39 op_sel:[0,0,1]
	global_store_dword v[80:81], v37, off
	global_store_dword v[80:81], v76, off offset:256
	global_store_dword v[80:81], v70, off offset:512
	global_store_dword v[80:81], v68, off offset:768
	s_and_saveexec_b64 s[6:7], s[4:5]
	s_cbranch_execz .LBB0_800
	s_and_b32 s14, s9, 0x3ffffff0
	v_lshl_add_u32 v37, s14, 2, v161
	ds_read_b32 v38, v37
	s_cmpk_lt_i32 s13, 0x80
	s_cbranch_scc1 .LBB0_799
	s_waitcnt lgkmcnt(0)
	ds_read2st64_b32 v[38:39], v79 offset0:4 offset1:8
	s_waitcnt lgkmcnt(0)
	v_add_f32_e32 v38, 0, v38
	v_add_f32_e32 v40, v38, v39
	ds_read2st64_b32 v[38:39], v79 offset0:12 offset1:16
	s_waitcnt lgkmcnt(0)
	v_add_f32_e32 v38, v40, v38
	v_add_f32_e32 v40, v38, v39
	ds_read2st64_b32 v[38:39], v79 offset0:20 offset1:24
	s_waitcnt lgkmcnt(0)
	v_add_f32_e32 v38, v40, v38
	v_add_f32_e32 v40, v38, v39
	ds_read2st64_b32 v[38:39], v79 offset0:28 offset1:32
	s_waitcnt lgkmcnt(0)
	v_add_f32_e32 v38, v40, v38
	v_add_f32_e32 v38, v38, v39

.LBB0_801:
	s_min_i32 s6, s10, s2
	s_ashr_i32 s7, s6, 31
	s_lshl_b64 s[6:7], s[6:7], 11
	s_waitcnt lgkmcnt(0)
	v_lshl_add_u64 v[36:37], v[34:35], 0, s[6:7]
	global_load_dwordx2 v[42:43], v[36:37], off
	global_load_dwordx2 v[40:41], v[36:37], off offset:512
	global_load_dwordx2 v[38:39], v[36:37], off offset:1024
	s_nop 0
	global_load_dwordx2 v[36:37], v[36:37], off offset:1536
	s_waitcnt vmcnt(15)
	v_and_b32_e32 v77, 0xffff0000, v66
	v_and_b32_e32 v75, 0xffff0000, v67
	v_lshlrev_b32_e32 v76, 16, v66
	v_lshlrev_b32_e32 v74, 16, v67
	s_waitcnt vmcnt(14)
	v_lshlrev_b32_e32 v72, 16, v64
	v_and_b32_e32 v73, 0xffff0000, v64
	v_lshlrev_b32_e32 v70, 16, v65
	v_and_b32_e32 v71, 0xffff0000, v65
	s_waitcnt vmcnt(13)
	v_lshlrev_b32_e32 v68, 16, v62
	v_and_b32_e32 v69, 0xffff0000, v62
	v_lshlrev_b32_e32 v66, 16, v63
	v_and_b32_e32 v67, 0xffff0000, v63
	s_waitcnt vmcnt(12)
	v_lshlrev_b32_e32 v64, 16, v60
	v_and_b32_e32 v65, 0xffff0000, v60
	v_lshlrev_b32_e32 v62, 16, v61
	v_and_b32_e32 v63, 0xffff0000, v61
	v_mul_f32_e32 v60, v77, v77
	v_mul_f32_e32 v61, v75, v75
	v_fmac_f32_e32 v60, v76, v76
	v_fmac_f32_e32 v61, v74, v74
	v_add_f32_e32 v60, v60, v61
	v_mul_f32_e32 v61, v73, v73
	v_mul_f32_e32 v80, v71, v71
	v_fmac_f32_e32 v61, v72, v72
	v_fmac_f32_e32 v80, v70, v70
	v_add_f32_e32 v61, v61, v80
	v_add_f32_e32 v60, v60, v61
	v_mul_f32_e32 v61, v69, v69
	v_mul_f32_e32 v80, v67, v67
	v_fmac_f32_e32 v61, v68, v68
	v_fmac_f32_e32 v80, v66, v66
	v_add_f32_e32 v61, v61, v80
	v_add_f32_e32 v60, v60, v61
	v_mul_f32_e32 v61, v65, v65
	v_mul_f32_e32 v80, v63, v63
	v_fmac_f32_e32 v61, v64, v64
	v_fmac_f32_e32 v80, v62, v62
	v_add_f32_e32 v61, v61, v80
	v_add_f32_e32 v60, v60, v61
	s_cmp_ge_i32 s11, s67
	s_waitcnt lgkmcnt(0)
	s_nop 1
	v_add_f32_dpp v60, v60, v60 quad_perm:[1,0,3,2] row_mask:0xf bank_mask:0xf
	s_waitcnt lgkmcnt(0)
	s_nop 1
	v_add_f32_dpp v60, v60, v60 quad_perm:[2,3,0,1] row_mask:0xf bank_mask:0xf
	s_waitcnt lgkmcnt(0)
	s_nop 1
	v_add_f32_dpp v60, v60, v60 row_half_mirror row_mask:0xf bank_mask:0xf
	s_waitcnt lgkmcnt(0)
	s_nop 1
	v_add_f32_dpp v60, v60, v60 row_mirror row_mask:0xf bank_mask:0xf
	s_waitcnt lgkmcnt(0)
	s_nop 1
	v_add_f32_dpp v60, v60, v60 row_bcast:15 row_mask:0xa bank_mask:0xf
	s_cbranch_scc1 .LBB0_782
	s_waitcnt lgkmcnt(0)
	s_nop 1
	v_add_f32_dpp v60, v60, v60 row_bcast:31 row_mask:0xc bank_mask:0xf
	s_nop 0
	v_readlane_b32 s101, v60, 63
	s_nop 1
	v_mov_b32_e32 v60, s101
	v_fmamk_f32 v60, v60, 0x3a800000, v210
	v_rsq_f32_e32 v60, v60
	s_add_i32 s6, s88, s10
	s_sub_i32 s6, s6, 24
	s_ashr_i32 s7, s6, 31
	v_pk_mul_f32 v[76:77], v[60:61], v[76:77] op_sel_hi:[0,1]
	v_pk_mul_f32 v[74:75], v[60:61], v[74:75] op_sel_hi:[0,1]
	v_pk_fma_f32 v[76:77], v[76:77], v[20:21], v[2:3]
	v_mov_b32_e32 v61, v0
	v_cvt_pk_fp8_f32 v61, v76, v77
	v_pk_fma_f32 v[74:75], v[74:75], v[18:19], v[4:5]
	s_lshl_b64 s[6:7], s[6:7], 10
	v_pk_mul_f32 v[72:73], v[60:61], v[72:73] op_sel_hi:[0,1]
	v_cvt_pk_fp8_f32 v61, v74, v75 op_sel:[0,0,1]
	v_pk_fma_f32 v[72:73], v[72:73], v[24:25], v[6:7]
	v_lshl_add_u64 v[80:81], v[112:113], 0, s[6:7]
	v_cvt_pk_fp8_f32 v76, v72, v73
	v_pk_mul_f32 v[70:71], v[60:61], v[70:71] op_sel_hi:[0,1]
	v_pk_fma_f32 v[70:71], v[70:71], v[22:23], v[8:9]
	v_pk_mul_f32 v[68:69], v[60:61], v[68:69] op_sel_hi:[0,1]
	v_cvt_pk_fp8_f32 v76, v70, v71 op_sel:[0,0,1]
	v_pk_fma_f32 v[68:69], v[68:69], v[28:29], v[10:11]
	v_pk_mul_f32 v[64:65], v[60:61], v[64:65] op_sel_hi:[0,1]
	v_cvt_pk_fp8_f32 v70, v68, v69
	v_pk_fma_f32 v[64:65], v[64:65], v[32:33], v[14:15]
	v_cvt_pk_fp8_f32 v68, v64, v65
	v_pk_mul_f32 v[66:67], v[60:61], v[66:67] op_sel_hi:[0,1]
	v_pk_fma_f32 v[66:67], v[66:67], v[26:27], v[12:13]
	v_pk_mul_f32 v[62:63], v[60:61], v[62:63] op_sel_hi:[0,1]
	v_cvt_pk_fp8_f32 v70, v66, v67 op_sel:[0,0,1]
	v_pk_fma_f32 v[62:63], v[62:63], v[30:31], v[16:17]
	s_nop 0
	v_cvt_pk_fp8_f32 v68, v62, v63 op_sel:[0,0,1]
	global_store_dword v[80:81], v61, off
	global_store_dword v[80:81], v76, off offset:256
	global_store_dword v[80:81], v70, off offset:512
	global_store_dword v[80:81], v68, off offset:768
	s_and_saveexec_b64 s[6:7], s[4:5]
	s_cbranch_execz .LBB0_781
	s_add_i32 s13, s9, 16
	s_and_b32 s13, s13, 0x3ffffff0
	v_lshl_add_u32 v61, s13, 2, v161
	ds_read_b32 v62, v61
	s_cmpk_lt_i32 s11, 0x80
	s_cbranch_scc1 .LBB0_780
	s_waitcnt lgkmcnt(0)
	ds_read2st64_b32 v[62:63], v79 offset0:6 offset1:10
	s_waitcnt lgkmcnt(0)
	v_add_f32_e32 v62, 0, v62
	v_add_f32_e32 v64, v62, v63
	ds_read2st64_b32 v[62:63], v79 offset0:14 offset1:18
	s_waitcnt lgkmcnt(0)
	v_add_f32_e32 v62, v64, v62
	v_add_f32_e32 v64, v62, v63
	ds_read2st64_b32 v[62:63], v79 offset0:22 offset1:26
	s_waitcnt lgkmcnt(0)
	v_add_f32_e32 v62, v64, v62
	v_add_f32_e32 v64, v62, v63
	ds_read2st64_b32 v[62:63], v79 offset0:30 offset1:34
	s_waitcnt lgkmcnt(0)
	v_add_f32_e32 v62, v64, v62
	v_add_f32_e32 v62, v62, v63
	s_branch .LBB0_780

.LBB0_1064:
	s_mov_b32 s98, 0xbd38aa3b
	v_mbcnt_lo_u32_b32 v226, -1, 0
	v_mbcnt_hi_u32_b32 v226, -1, v226
	v_and_b32_e32 v226, 16, v226
	v_pk_mul_f32 v[8:9], v[158:159], v[154:155]
	v_pk_mul_f32 v[20:21], v[150:151], v[146:147]
	v_pk_mul_f32 v[12:13], v[150:151], s[98:99] op_sel_hi:[1,0]
	v_pk_mul_f32 v[16:17], v[152:153], s[98:99] op_sel_hi:[1,0]
	v_pk_mul_f32 v[10:11], v[158:159], s[98:99] op_sel_hi:[1,0]
	v_pk_mul_f32 v[14:15], v[160:161], s[98:99] op_sel_hi:[1,0]
	v_exp_f32_e32 v12, v12
	v_exp_f32_e32 v13, v13
	v_exp_f32_e32 v16, v16
	v_exp_f32_e32 v17, v17
	v_exp_f32_e32 v10, v10
	v_exp_f32_e32 v11, v11
	v_exp_f32_e32 v14, v14
	v_exp_f32_e32 v15, v15
	v_pk_fma_f32 v[12:13], v[12:13], v[212:213], v[212:213] op_sel:[0,1,1] op_sel_hi:[1,1,1]
	v_pk_fma_f32 v[16:17], v[16:17], v[212:213], v[212:213] op_sel:[0,1,1] op_sel_hi:[1,1,1]
	v_pk_fma_f32 v[10:11], v[10:11], v[212:213], v[212:213] op_sel:[0,1,1] op_sel_hi:[1,1,1]
	v_pk_fma_f32 v[14:15], v[14:15], v[212:213], v[212:213] op_sel:[0,1,1] op_sel_hi:[1,1,1]
	v_rcp_f32_e32 v12, v12
	v_rcp_f32_e32 v13, v13
	v_rcp_f32_e32 v16, v16
	v_rcp_f32_e32 v17, v17
	v_rcp_f32_e32 v10, v10
	v_rcp_f32_e32 v11, v11
	v_rcp_f32_e32 v14, v14
	v_rcp_f32_e32 v15, v15
	v_pk_mul_f32 v[8:9], v[8:9], v[10:11]
	v_pk_mul_f32 v[10:11], v[20:21], v[12:13]
	v_cvt_pk_fp8_f32 v12, v8, v9
	v_cvt_pk_fp8_f32 v13, v10, v11
	v_pk_mul_f32 v[4:5], v[160:161], v[156:157]
	v_pk_mul_f32 v[18:19], v[152:153], v[148:149]
	v_pk_mul_f32 v[4:5], v[4:5], v[14:15]
	v_pk_mul_f32 v[8:9], v[18:19], v[16:17]
	v_cvt_pk_fp8_f32 v12, v4, v5 op_sel:[0,0,1]
	v_cvt_pk_fp8_f32 v13, v8, v9 op_sel:[0,0,1]
	v_lshl_or_b32 v2, s86, 7, v173
	v_lshl_add_u32 v6, s87, 8, v196
	v_mov_b64_e32 v[4:5], s[84:85]
	v_ashrrev_i32_e32 v3, 31, v2
	v_mad_i64_i32 v[8:9], s[18:19], v6, s57, v[4:5]
	v_lshl_add_u64 v[8:9], v[8:9], 0, v[2:3]
	s_nop 15
	s_nop 15
	v_mov_b32_e32 v220, v12
	v_mov_b32_e32 v221, v13
	v_mov_b32_e32 v218, v8
	v_mov_b32_e32 v219, v9
	v_pk_mul_f32 v[10:11], v[142:143], v[138:139]
	v_pk_mul_f32 v[22:23], v[134:135], v[130:131]
	v_pk_mul_f32 v[14:15], v[134:135], s[98:99] op_sel_hi:[1,0]
	v_pk_mul_f32 v[18:19], v[136:137], s[98:99] op_sel_hi:[1,0]
	v_pk_mul_f32 v[12:13], v[142:143], s[98:99] op_sel_hi:[1,0]
	v_pk_mul_f32 v[16:17], v[144:145], s[98:99] op_sel_hi:[1,0]
	v_exp_f32_e32 v14, v14
	v_exp_f32_e32 v15, v15
	v_exp_f32_e32 v18, v18
	v_exp_f32_e32 v19, v19
	v_exp_f32_e32 v12, v12
	v_exp_f32_e32 v13, v13
	v_exp_f32_e32 v16, v16
	v_exp_f32_e32 v17, v17
	v_pk_fma_f32 v[14:15], v[14:15], v[212:213], v[212:213] op_sel:[0,1,1] op_sel_hi:[1,1,1]
	v_pk_fma_f32 v[18:19], v[18:19], v[212:213], v[212:213] op_sel:[0,1,1] op_sel_hi:[1,1,1]
	v_pk_fma_f32 v[12:13], v[12:13], v[212:213], v[212:213] op_sel:[0,1,1] op_sel_hi:[1,1,1]
	v_pk_fma_f32 v[16:17], v[16:17], v[212:213], v[212:213] op_sel:[0,1,1] op_sel_hi:[1,1,1]
	v_rcp_f32_e32 v14, v14
	v_rcp_f32_e32 v15, v15
	v_rcp_f32_e32 v18, v18
	v_rcp_f32_e32 v19, v19
	v_rcp_f32_e32 v12, v12
	v_rcp_f32_e32 v13, v13
	v_rcp_f32_e32 v16, v16
	v_rcp_f32_e32 v17, v17
	v_pk_mul_f32 v[10:11], v[10:11], v[12:13]
	v_pk_mul_f32 v[12:13], v[22:23], v[14:15]
	v_cvt_pk_fp8_f32 v14, v10, v11
	v_cvt_pk_fp8_f32 v15, v12, v13
	v_pk_mul_f32 v[8:9], v[144:145], v[140:141]
	v_pk_mul_f32 v[20:21], v[136:137], v[132:133]
	v_pk_mul_f32 v[8:9], v[8:9], v[16:17]
	v_pk_mul_f32 v[10:11], v[20:21], v[18:19]
	v_cvt_pk_fp8_f32 v14, v8, v9 op_sel:[0,0,1]
	v_cvt_pk_fp8_f32 v15, v10, v11 op_sel:[0,0,1]
	v_or_b32_e32 v7, 16, v6
	v_mad_i64_i32 v[8:9], s[18:19], v7, s57, v[4:5]
	v_lshl_add_u64 v[8:9], v[8:9], 0, v[2:3]
	v_mov_b32_e32 v222, v14
	v_mov_b32_e32 v223, v15
	v_lshl_add_u64 v[224:225], v[8:9], 0, -8
	v_cmp_ne_u32_e64 s[18:19], 0, v226
	s_nop 1
	v_permlane16_swap_b32_e32 v220, v222
	v_permlane16_swap_b32_e32 v221, v223
	v_cndmask_b32_e64 v224, v218, v224, s[18:19]
	v_cndmask_b32_e64 v225, v219, v225, s[18:19]
	global_store_dwordx4 v[224:225], v[220:223], off sc1
	v_pk_mul_f32 v[10:11], v[126:127], v[122:123]
	v_pk_mul_f32 v[22:23], v[118:119], v[114:115]
	v_pk_mul_f32 v[14:15], v[118:119], s[98:99] op_sel_hi:[1,0]
	v_pk_mul_f32 v[18:19], v[120:121], s[98:99] op_sel_hi:[1,0]
	v_pk_mul_f32 v[12:13], v[126:127], s[98:99] op_sel_hi:[1,0]
	v_pk_mul_f32 v[16:17], v[128:129], s[98:99] op_sel_hi:[1,0]
	v_exp_f32_e32 v14, v14
	v_exp_f32_e32 v15, v15
	v_exp_f32_e32 v18, v18
	v_exp_f32_e32 v19, v19
	v_exp_f32_e32 v12, v12
	v_exp_f32_e32 v13, v13
	v_exp_f32_e32 v16, v16
	v_exp_f32_e32 v17, v17
	v_pk_fma_f32 v[14:15], v[14:15], v[212:213], v[212:213] op_sel:[0,1,1] op_sel_hi:[1,1,1]
	v_pk_fma_f32 v[18:19], v[18:19], v[212:213], v[212:213] op_sel:[0,1,1] op_sel_hi:[1,1,1]
	v_pk_fma_f32 v[12:13], v[12:13], v[212:213], v[212:213] op_sel:[0,1,1] op_sel_hi:[1,1,1]
	v_pk_fma_f32 v[16:17], v[16:17], v[212:213], v[212:213] op_sel:[0,1,1] op_sel_hi:[1,1,1]
	v_rcp_f32_e32 v14, v14
	v_rcp_f32_e32 v15, v15
	v_rcp_f32_e32 v18, v18
	v_rcp_f32_e32 v19, v19
	v_rcp_f32_e32 v12, v12
	v_rcp_f32_e32 v13, v13
	v_rcp_f32_e32 v16, v16
	v_rcp_f32_e32 v17, v17
	v_pk_mul_f32 v[10:11], v[10:11], v[12:13]
	v_pk_mul_f32 v[12:13], v[22:23], v[14:15]
	v_cvt_pk_fp8_f32 v14, v10, v11
	v_cvt_pk_fp8_f32 v15, v12, v13
	v_pk_mul_f32 v[8:9], v[128:129], v[124:125]
	v_pk_mul_f32 v[20:21], v[120:121], v[116:117]
	v_pk_mul_f32 v[8:9], v[8:9], v[16:17]
	v_pk_mul_f32 v[10:11], v[20:21], v[18:19]
	v_cvt_pk_fp8_f32 v14, v8, v9 op_sel:[0,0,1]
	v_cvt_pk_fp8_f32 v15, v10, v11 op_sel:[0,0,1]
	v_or_b32_e32 v7, 32, v6
	v_mad_i64_i32 v[8:9], s[18:19], v7, s57, v[4:5]
	v_lshl_add_u64 v[8:9], v[8:9], 0, v[2:3]
	v_mov_b32_e32 v220, v14
	v_mov_b32_e32 v221, v15
	v_mov_b32_e32 v218, v8
	v_mov_b32_e32 v219, v9
	v_pk_mul_f32 v[10:11], v[110:111], v[106:107]
	v_pk_mul_f32 v[22:23], v[102:103], v[98:99]
	v_pk_mul_f32 v[14:15], v[102:103], s[98:99] op_sel_hi:[1,0]
	v_pk_mul_f32 v[18:19], v[104:105], s[98:99] op_sel_hi:[1,0]
	v_pk_mul_f32 v[12:13], v[110:111], s[98:99] op_sel_hi:[1,0]
	v_pk_mul_f32 v[16:17], v[112:113], s[98:99] op_sel_hi:[1,0]
	v_exp_f32_e32 v14, v14
	v_exp_f32_e32 v15, v15
	v_exp_f32_e32 v18, v18
	v_exp_f32_e32 v19, v19
	v_exp_f32_e32 v12, v12
	v_exp_f32_e32 v13, v13
	v_exp_f32_e32 v16, v16
	v_exp_f32_e32 v17, v17
	v_pk_fma_f32 v[14:15], v[14:15], v[212:213], v[212:213] op_sel:[0,1,1] op_sel_hi:[1,1,1]
	v_pk_fma_f32 v[18:19], v[18:19], v[212:213], v[212:213] op_sel:[0,1,1] op_sel_hi:[1,1,1]
	v_pk_fma_f32 v[12:13], v[12:13], v[212:213], v[212:213] op_sel:[0,1,1] op_sel_hi:[1,1,1]
	v_pk_fma_f32 v[16:17], v[16:17], v[212:213], v[212:213] op_sel:[0,1,1] op_sel_hi:[1,1,1]
	v_rcp_f32_e32 v14, v14
	v_rcp_f32_e32 v15, v15
	v_rcp_f32_e32 v18, v18
	v_rcp_f32_e32 v19, v19
	v_rcp_f32_e32 v12, v12
	v_rcp_f32_e32 v13, v13
	v_rcp_f32_e32 v16, v16
	v_rcp_f32_e32 v17, v17
	v_pk_mul_f32 v[10:11], v[10:11], v[12:13]
	v_pk_mul_f32 v[12:13], v[22:23], v[14:15]
	v_cvt_pk_fp8_f32 v14, v10, v11
	v_cvt_pk_fp8_f32 v15, v12, v13
	v_pk_mul_f32 v[8:9], v[112:113], v[108:109]
	v_pk_mul_f32 v[20:21], v[104:105], v[100:101]
	v_pk_mul_f32 v[8:9], v[8:9], v[16:17]
	v_pk_mul_f32 v[10:11], v[20:21], v[18:19]
	v_cvt_pk_fp8_f32 v14, v8, v9 op_sel:[0,0,1]
	v_cvt_pk_fp8_f32 v15, v10, v11 op_sel:[0,0,1]
	v_or_b32_e32 v7, 48, v6
	v_mad_i64_i32 v[8:9], s[18:19], v7, s57, v[4:5]
	v_lshl_add_u64 v[8:9], v[8:9], 0, v[2:3]
	v_mov_b32_e32 v222, v14
	v_mov_b32_e32 v223, v15
	v_lshl_add_u64 v[224:225], v[8:9], 0, -8
	v_cmp_ne_u32_e64 s[18:19], 0, v226
	s_nop 1
	v_permlane16_swap_b32_e32 v220, v222
	v_permlane16_swap_b32_e32 v221, v223
	v_cndmask_b32_e64 v224, v218, v224, s[18:19]
	v_cndmask_b32_e64 v225, v219, v225, s[18:19]
	global_store_dwordx4 v[224:225], v[220:223], off sc1
	v_pk_mul_f32 v[10:11], v[94:95], v[90:91]
	v_pk_mul_f32 v[22:23], v[86:87], v[82:83]
	v_pk_mul_f32 v[14:15], v[86:87], s[98:99] op_sel_hi:[1,0]
	v_pk_mul_f32 v[18:19], v[88:89], s[98:99] op_sel_hi:[1,0]
	v_pk_mul_f32 v[12:13], v[94:95], s[98:99] op_sel_hi:[1,0]
	v_pk_mul_f32 v[16:17], v[96:97], s[98:99] op_sel_hi:[1,0]
	v_exp_f32_e32 v14, v14
	v_exp_f32_e32 v15, v15
	v_exp_f32_e32 v18, v18
	v_exp_f32_e32 v19, v19
	v_exp_f32_e32 v12, v12
	v_exp_f32_e32 v13, v13
	v_exp_f32_e32 v16, v16
	v_exp_f32_e32 v17, v17
	v_pk_fma_f32 v[14:15], v[14:15], v[212:213], v[212:213] op_sel:[0,1,1] op_sel_hi:[1,1,1]
	v_pk_fma_f32 v[18:19], v[18:19], v[212:213], v[212:213] op_sel:[0,1,1] op_sel_hi:[1,1,1]
	v_pk_fma_f32 v[12:13], v[12:13], v[212:213], v[212:213] op_sel:[0,1,1] op_sel_hi:[1,1,1]
	v_pk_fma_f32 v[16:17], v[16:17], v[212:213], v[212:213] op_sel:[0,1,1] op_sel_hi:[1,1,1]
	v_rcp_f32_e32 v14, v14
	v_rcp_f32_e32 v15, v15
	v_rcp_f32_e32 v18, v18
	v_rcp_f32_e32 v19, v19
	v_rcp_f32_e32 v12, v12
	v_rcp_f32_e32 v13, v13
	v_rcp_f32_e32 v16, v16
	v_rcp_f32_e32 v17, v17
	v_pk_mul_f32 v[10:11], v[10:11], v[12:13]
	v_pk_mul_f32 v[12:13], v[22:23], v[14:15]
	v_cvt_pk_fp8_f32 v14, v10, v11
	v_cvt_pk_fp8_f32 v15, v12, v13
	v_pk_mul_f32 v[8:9], v[96:97], v[92:93]
	v_pk_mul_f32 v[20:21], v[88:89], v[84:85]
	v_pk_mul_f32 v[8:9], v[8:9], v[16:17]
	v_pk_mul_f32 v[10:11], v[20:21], v[18:19]
	v_cvt_pk_fp8_f32 v14, v8, v9 op_sel:[0,0,1]
	v_cvt_pk_fp8_f32 v15, v10, v11 op_sel:[0,0,1]
	v_add_u32_e32 v7, 0x80, v6
	v_mad_i64_i32 v[8:9], s[18:19], v7, s57, v[4:5]
	v_lshl_add_u64 v[8:9], v[8:9], 0, v[2:3]
	v_mov_b32_e32 v220, v14
	v_mov_b32_e32 v221, v15
	v_mov_b32_e32 v218, v8
	v_mov_b32_e32 v219, v9
	v_pk_mul_f32 v[10:11], v[78:79], v[74:75]
	v_pk_mul_f32 v[22:23], v[62:63], v[58:59]
	v_pk_mul_f32 v[14:15], v[62:63], s[98:99] op_sel_hi:[1,0]
	v_pk_mul_f32 v[18:19], v[64:65], s[98:99] op_sel_hi:[1,0]
	v_pk_mul_f32 v[12:13], v[78:79], s[98:99] op_sel_hi:[1,0]
	v_pk_mul_f32 v[16:17], v[80:81], s[98:99] op_sel_hi:[1,0]
	v_exp_f32_e32 v14, v14
	v_exp_f32_e32 v15, v15
	v_exp_f32_e32 v18, v18
	v_exp_f32_e32 v19, v19
	v_exp_f32_e32 v12, v12
	v_exp_f32_e32 v13, v13
	v_exp_f32_e32 v16, v16
	v_exp_f32_e32 v17, v17
	v_pk_fma_f32 v[14:15], v[14:15], v[212:213], v[212:213] op_sel:[0,1,1] op_sel_hi:[1,1,1]
	v_pk_fma_f32 v[18:19], v[18:19], v[212:213], v[212:213] op_sel:[0,1,1] op_sel_hi:[1,1,1]
	v_pk_fma_f32 v[12:13], v[12:13], v[212:213], v[212:213] op_sel:[0,1,1] op_sel_hi:[1,1,1]
	v_pk_fma_f32 v[16:17], v[16:17], v[212:213], v[212:213] op_sel:[0,1,1] op_sel_hi:[1,1,1]
	v_rcp_f32_e32 v14, v14
	v_rcp_f32_e32 v15, v15
	v_rcp_f32_e32 v18, v18
	v_rcp_f32_e32 v19, v19
	v_rcp_f32_e32 v12, v12
	v_rcp_f32_e32 v13, v13
	v_rcp_f32_e32 v16, v16
	v_rcp_f32_e32 v17, v17
	v_pk_mul_f32 v[10:11], v[10:11], v[12:13]
	v_pk_mul_f32 v[12:13], v[22:23], v[14:15]
	v_cvt_pk_fp8_f32 v14, v10, v11
	v_cvt_pk_fp8_f32 v15, v12, v13
	v_pk_mul_f32 v[8:9], v[80:81], v[76:77]
	v_pk_mul_f32 v[20:21], v[64:65], v[60:61]
	v_pk_mul_f32 v[8:9], v[8:9], v[16:17]
	v_pk_mul_f32 v[10:11], v[20:21], v[18:19]
	v_cvt_pk_fp8_f32 v14, v8, v9 op_sel:[0,0,1]
	v_cvt_pk_fp8_f32 v15, v10, v11 op_sel:[0,0,1]
	v_add_u32_e32 v7, 0x90, v6
	v_mad_i64_i32 v[8:9], s[18:19], v7, s57, v[4:5]
	v_lshl_add_u64 v[8:9], v[8:9], 0, v[2:3]
	v_mov_b32_e32 v222, v14
	v_mov_b32_e32 v223, v15
	v_lshl_add_u64 v[224:225], v[8:9], 0, -8
	v_cmp_ne_u32_e64 s[18:19], 0, v226
	s_nop 1
	v_permlane16_swap_b32_e32 v220, v222
	v_permlane16_swap_b32_e32 v221, v223
	v_cndmask_b32_e64 v224, v218, v224, s[18:19]
	v_cndmask_b32_e64 v225, v219, v225, s[18:19]
	global_store_dwordx4 v[224:225], v[220:223], off sc1
	v_pk_mul_f32 v[10:11], v[50:51], v[42:43]
	v_pk_mul_f32 v[22:23], v[66:67], v[70:71]
	v_pk_mul_f32 v[12:13], v[50:51], s[98:99] op_sel_hi:[1,0]
	v_pk_mul_f32 v[16:17], v[52:53], s[98:99] op_sel_hi:[1,0]
	v_pk_mul_f32 v[14:15], v[66:67], s[98:99] op_sel_hi:[1,0]
	v_pk_mul_f32 v[18:19], v[68:69], s[98:99] op_sel_hi:[1,0]
	v_exp_f32_e32 v12, v12
	v_exp_f32_e32 v13, v13
	v_exp_f32_e32 v16, v16
	v_exp_f32_e32 v17, v17
	v_exp_f32_e32 v14, v14
	v_exp_f32_e32 v15, v15
	v_exp_f32_e32 v18, v18
	v_exp_f32_e32 v19, v19
	v_pk_fma_f32 v[12:13], v[12:13], v[212:213], v[212:213] op_sel:[0,1,1] op_sel_hi:[1,1,1]
	v_pk_fma_f32 v[16:17], v[16:17], v[212:213], v[212:213] op_sel:[0,1,1] op_sel_hi:[1,1,1]
	v_pk_fma_f32 v[14:15], v[14:15], v[212:213], v[212:213] op_sel:[0,1,1] op_sel_hi:[1,1,1]
	v_pk_fma_f32 v[18:19], v[18:19], v[212:213], v[212:213] op_sel:[0,1,1] op_sel_hi:[1,1,1]
	v_rcp_f32_e32 v12, v12
	v_rcp_f32_e32 v13, v13
	v_rcp_f32_e32 v16, v16
	v_rcp_f32_e32 v17, v17
	v_rcp_f32_e32 v14, v14
	v_rcp_f32_e32 v15, v15
	v_rcp_f32_e32 v18, v18
	v_rcp_f32_e32 v19, v19
	v_pk_mul_f32 v[10:11], v[10:11], v[12:13]
	v_pk_mul_f32 v[12:13], v[22:23], v[14:15]
	v_cvt_pk_fp8_f32 v14, v10, v11
	v_cvt_pk_fp8_f32 v15, v12, v13
	v_pk_mul_f32 v[8:9], v[52:53], v[44:45]
	v_pk_mul_f32 v[20:21], v[68:69], v[72:73]
	v_pk_mul_f32 v[8:9], v[8:9], v[16:17]
	v_pk_mul_f32 v[10:11], v[20:21], v[18:19]
	v_cvt_pk_fp8_f32 v14, v8, v9 op_sel:[0,0,1]
	v_cvt_pk_fp8_f32 v15, v10, v11 op_sel:[0,0,1]
	v_add_u32_e32 v7, 0xa0, v6
	v_mad_i64_i32 v[8:9], s[18:19], v7, s57, v[4:5]
	v_lshl_add_u64 v[8:9], v[8:9], 0, v[2:3]
	v_mov_b32_e32 v220, v14
	v_mov_b32_e32 v221, v15
	v_mov_b32_e32 v218, v8
	v_mov_b32_e32 v219, v9
	v_pk_mul_f32 v[10:11], v[38:39], v[34:35]
	v_pk_mul_f32 v[22:23], v[46:47], v[54:55]
	v_pk_mul_f32 v[12:13], v[38:39], s[98:99] op_sel_hi:[1,0]
	v_pk_mul_f32 v[16:17], v[40:41], s[98:99] op_sel_hi:[1,0]
	v_pk_mul_f32 v[14:15], v[46:47], s[98:99] op_sel_hi:[1,0]
	v_pk_mul_f32 v[18:19], v[48:49], s[98:99] op_sel_hi:[1,0]
	v_exp_f32_e32 v12, v12
	v_exp_f32_e32 v13, v13
	v_exp_f32_e32 v16, v16
	v_exp_f32_e32 v17, v17
	v_exp_f32_e32 v14, v14
	v_exp_f32_e32 v15, v15
	v_exp_f32_e32 v18, v18
	v_exp_f32_e32 v19, v19
	v_pk_fma_f32 v[12:13], v[12:13], v[212:213], v[212:213] op_sel:[0,1,1] op_sel_hi:[1,1,1]
	v_pk_fma_f32 v[16:17], v[16:17], v[212:213], v[212:213] op_sel:[0,1,1] op_sel_hi:[1,1,1]
	v_pk_fma_f32 v[14:15], v[14:15], v[212:213], v[212:213] op_sel:[0,1,1] op_sel_hi:[1,1,1]
	v_pk_fma_f32 v[18:19], v[18:19], v[212:213], v[212:213] op_sel:[0,1,1] op_sel_hi:[1,1,1]
	v_rcp_f32_e32 v12, v12
	v_rcp_f32_e32 v13, v13
	v_rcp_f32_e32 v16, v16
	v_rcp_f32_e32 v17, v17
	v_rcp_f32_e32 v14, v14
	v_rcp_f32_e32 v15, v15
	v_rcp_f32_e32 v18, v18
	v_rcp_f32_e32 v19, v19
	v_pk_mul_f32 v[10:11], v[10:11], v[12:13]
	v_pk_mul_f32 v[12:13], v[22:23], v[14:15]
	v_cvt_pk_fp8_f32 v14, v10, v11
	v_cvt_pk_fp8_f32 v15, v12, v13
	v_pk_mul_f32 v[8:9], v[40:41], v[36:37]
	v_pk_mul_f32 v[20:21], v[48:49], v[56:57]
	v_pk_mul_f32 v[8:9], v[8:9], v[16:17]
	v_pk_mul_f32 v[10:11], v[20:21], v[18:19]
	v_cvt_pk_fp8_f32 v14, v8, v9 op_sel:[0,0,1]
	v_cvt_pk_fp8_f32 v15, v10, v11 op_sel:[0,0,1]
	v_add_u32_e32 v6, 0xb0, v6
	v_mad_i64_i32 v[4:5], s[18:19], v6, s57, v[4:5]
	v_lshl_add_u64 v[2:3], v[4:5], 0, v[2:3]
	s_mov_b64 s[88:89], -1
	s_and_b64 vcc, exec, s[4:5]
	s_mov_b64 s[4:5], -1
	v_mov_b32_e32 v222, v14
	v_mov_b32_e32 v223, v15
	v_lshl_add_u64 v[224:225], v[2:3], 0, -8
	v_cmp_ne_u32_e64 s[18:19], 0, v226
	s_nop 1
	v_permlane16_swap_b32_e32 v220, v222
	v_permlane16_swap_b32_e32 v221, v223
	v_cndmask_b32_e64 v224, v218, v224, s[18:19]
	v_cndmask_b32_e64 v225, v219, v225, s[18:19]
	global_store_dwordx4 v[224:225], v[220:223], off sc1
	s_cbranch_vccnz .LBB0_1068
	s_andn2_b64 vcc, exec, s[14:15]
	s_cbranch_vccnz .LBB0_1067
	s_barrier

.LBB0_1125:
	v_lshlrev_b32_e32 v2, 2, v220
	s_nop 15
	s_nop 15
	v_add_u32_e32 v2, 0, v2
	ds_read_b32 v14, v2 offset:160
	v_lshlrev_b32_e32 v16, 8, v221
	v_add_u32_e32 v2, v16, v185
	s_waitcnt lgkmcnt(0)
	v_cmp_lt_i32_e64 s[16:17], v2, v14
	s_nop 1
	v_cndmask_b32_e64 v2, v16, v2, s[16:17]
	v_ashrrev_i32_e32 v3, 31, v2
	v_mad_i64_i32 v[4:5], s[4:5], v220, s31, v[2:3]
	v_lshl_add_u64 v[2:3], v[4:5], 2, s[82:83]
	global_load_dword v24, v[2:3], off
	v_lshl_add_u64 v[2:3], v[4:5], 2, s[90:91]
	global_load_dword v224, v[2:3], off
	v_add_u32_e32 v2, v16, v223
	v_cmp_lt_i32_e32 vcc, v2, v14
	s_nop 1
	v_cndmask_b32_e32 v2, v16, v2, vcc
	v_ashrrev_i32_e32 v3, 31, v2
	v_mad_i64_i32 v[2:3], s[4:5], v220, s31, v[2:3]
	v_lshlrev_b64 v[2:3], 2, v[2:3]
	v_lshl_add_u64 v[6:7], s[82:83], 0, v[2:3]
	v_lshl_add_u64 v[2:3], s[90:91], 0, v[2:3]
	global_load_dword v8, v[6:7], off
	global_load_dword v17, v[2:3], off
	v_add_u32_e32 v2, v16, v216
	v_cmp_lt_i32_e64 s[4:5], v2, v14
	s_nop 1
	v_cndmask_b32_e64 v2, v16, v2, s[4:5]
	v_ashrrev_i32_e32 v3, 31, v2
	v_mad_i64_i32 v[2:3], s[6:7], v220, s31, v[2:3]
	v_lshlrev_b64 v[2:3], 2, v[2:3]
	v_lshl_add_u64 v[6:7], s[82:83], 0, v[2:3]
	v_lshl_add_u64 v[2:3], s[90:91], 0, v[2:3]
	global_load_dword v10, v[6:7], off
	global_load_dword v15, v[2:3], off
	v_add_u32_e32 v2, v16, v212
	v_cmp_lt_i32_e64 s[6:7], v2, v14
	s_nop 1
	v_cndmask_b32_e64 v2, v16, v2, s[6:7]
	v_ashrrev_i32_e32 v3, 31, v2
	v_mad_i64_i32 v[2:3], s[8:9], v220, s31, v[2:3]
	v_lshlrev_b64 v[2:3], 2, v[2:3]
	v_lshl_add_u64 v[6:7], s[82:83], 0, v[2:3]
	v_lshl_add_u64 v[2:3], s[90:91], 0, v[2:3]
	global_load_dword v12, v[6:7], off
	global_load_dword v13, v[2:3], off
	v_add_u32_e32 v2, v16, v250
	v_cmp_lt_i32_e64 s[8:9], v2, v14
	s_nop 1
	v_cndmask_b32_e64 v2, v16, v2, s[8:9]
	v_ashrrev_i32_e32 v3, 31, v2
	v_mad_i64_i32 v[2:3], s[10:11], v220, s31, v[2:3]
	v_lshlrev_b64 v[2:3], 2, v[2:3]
	v_lshl_add_u64 v[6:7], s[82:83], 0, v[2:3]
	v_lshl_add_u64 v[2:3], s[90:91], 0, v[2:3]
	global_load_dword v20, v[6:7], off
	global_load_dword v11, v[2:3], off
	v_add_u32_e32 v2, v16, v251
	v_cmp_lt_i32_e64 s[10:11], v2, v14
	s_nop 1
	v_cndmask_b32_e64 v2, v16, v2, s[10:11]
	v_ashrrev_i32_e32 v3, 31, v2
	v_mad_i64_i32 v[2:3], s[12:13], v220, s31, v[2:3]
	v_lshlrev_b64 v[2:3], 2, v[2:3]
	v_lshl_add_u64 v[6:7], s[82:83], 0, v[2:3]
	v_lshl_add_u64 v[2:3], s[90:91], 0, v[2:3]
	global_load_dword v21, v[6:7], off
	global_load_dword v9, v[2:3], off
	v_add_u32_e32 v2, v16, v252
	v_cmp_lt_i32_e64 s[12:13], v2, v14
	s_nop 1
	v_cndmask_b32_e64 v2, v16, v2, s[12:13]
	v_ashrrev_i32_e32 v3, 31, v2
	v_mad_i64_i32 v[2:3], s[14:15], v220, s31, v[2:3]
	v_lshlrev_b64 v[2:3], 2, v[2:3]
	v_lshl_add_u64 v[6:7], s[82:83], 0, v[2:3]
	v_lshl_add_u64 v[2:3], s[90:91], 0, v[2:3]
	global_load_dword v22, v[6:7], off
	global_load_dword v19, v[2:3], off
	v_add_u32_e32 v2, v16, v253
	v_cmp_lt_i32_e64 s[14:15], v2, v14
	s_nop 1
	v_cndmask_b32_e64 v2, v16, v2, s[14:15]
	v_ashrrev_i32_e32 v3, 31, v2
	v_mad_i64_i32 v[2:3], s[62:63], v220, s31, v[2:3]
	v_lshlrev_b64 v[2:3], 2, v[2:3]
	v_lshl_add_u64 v[6:7], s[82:83], 0, v[2:3]
	v_lshl_add_u64 v[2:3], s[90:91], 0, v[2:3]
	global_load_dword v23, v[6:7], off
	global_load_dword v18, v[2:3], off
	s_waitcnt vmcnt(0)
	v_cndmask_b32_e64 v6, -1, v24, s[16:17]
	v_lshl_or_b32 v2, s22, 8, v254
	v_ashrrev_i32_e32 v3, 31, v2
	v_cmp_lt_i32_e64 s[16:17], -1, v6
	s_and_saveexec_b64 s[22:23], s[16:17]
	s_cbranch_execz .LBB0_1127
	v_mov_b32_e32 v7, v0
	v_mul_f32_e32 v14, 0.5, v224
	v_lshlrev_b64 v[4:5], 10, v[6:7]
	v_lshl_add_u64 v[24:25], s[92:93], 0, v[4:5]
	v_pk_mul_f32 v[26:27], v[158:159], v[14:15] op_sel_hi:[1,0]
	v_pk_mul_f32 v[30:31], v[154:155], v[14:15] op_sel_hi:[1,0]
	v_cvt_pk_fp8_f32 v4, v26, v27
	v_cvt_pk_fp8_f32 v5, v30, v31
	v_pk_mul_f32 v[6:7], v[160:161], v[14:15] op_sel_hi:[1,0]
	v_pk_mul_f32 v[28:29], v[156:157], v[14:15] op_sel_hi:[1,0]
	v_cvt_pk_fp8_f32 v4, v6, v7 op_sel:[0,0,1]
	v_cvt_pk_fp8_f32 v5, v28, v29 op_sel:[0,0,1]
	v_pk_mul_f32 v[28:29], v[150:151], v[14:15] op_sel_hi:[1,0]
	v_pk_mul_f32 v[32:33], v[146:147], v[14:15] op_sel_hi:[1,0]
	v_cvt_pk_fp8_f32 v6, v28, v29
	v_cvt_pk_fp8_f32 v7, v32, v33
	v_pk_mul_f32 v[26:27], v[152:153], v[14:15] op_sel_hi:[1,0]
	v_pk_mul_f32 v[30:31], v[148:149], v[14:15] op_sel_hi:[1,0]
	v_cvt_pk_fp8_f32 v6, v26, v27 op_sel:[0,0,1]
	v_cvt_pk_fp8_f32 v7, v30, v31 op_sel:[0,0,1]
	v_lshl_add_u64 v[24:25], v[24:25], 0, v[2:3]
	v_lshl_add_u64 v[24:25], v[24:25], 0, v[170:171]
	v_permlane16_swap_b32_e32 v4, v6
	v_permlane16_swap_b32_e32 v5, v7
	global_store_dwordx4 v[24:25], v[4:7], off

.LBB0_1135:
	v_mul_f32_e32 v22, 0.5, v17
	v_pk_mul_f32 v[26:27], v[142:143], v[22:23] op_sel_hi:[1,0]
	v_pk_mul_f32 v[30:31], v[138:139], v[22:23] op_sel_hi:[1,0]
	v_cvt_pk_fp8_f32 v20, v26, v27
	v_cvt_pk_fp8_f32 v21, v30, v31
	v_pk_mul_f32 v[24:25], v[144:145], v[22:23] op_sel_hi:[1,0]
	v_pk_mul_f32 v[28:29], v[140:141], v[22:23] op_sel_hi:[1,0]
	v_cvt_pk_fp8_f32 v20, v24, v25 op_sel:[0,0,1]
	v_cvt_pk_fp8_f32 v21, v28, v29 op_sel:[0,0,1]
	v_pk_mul_f32 v[24:25], v[136:137], v[22:23] op_sel_hi:[1,0]
	v_pk_mul_f32 v[26:27], v[134:135], v[22:23] op_sel_hi:[1,0]
	v_pk_mul_f32 v[28:29], v[132:133], v[22:23] op_sel_hi:[1,0]
	v_pk_mul_f32 v[30:31], v[130:131], v[22:23] op_sel_hi:[1,0]
	v_cvt_pk_fp8_f32 v22, v26, v27
	v_cvt_pk_fp8_f32 v23, v30, v31
	v_mov_b32_e32 v17, v0
	v_lshlrev_b64 v[16:17], 10, v[16:17]
	v_cvt_pk_fp8_f32 v22, v24, v25 op_sel:[0,0,1]
	v_cvt_pk_fp8_f32 v23, v28, v29 op_sel:[0,0,1]
	v_lshl_add_u64 v[16:17], s[92:93], 0, v[16:17]
	v_lshl_add_u64 v[16:17], v[16:17], 0, v[2:3]
	v_permlane16_swap_b32_e32 v20, v22
	v_permlane16_swap_b32_e32 v21, v23
	v_lshl_add_u64 v[16:17], v[16:17], 0, v[170:171]
	global_store_dwordx4 v[16:17], v[20:23], off
	s_or_b64 exec, exec, s[4:5]
	v_cmp_lt_i32_e32 vcc, -1, v14
	s_and_saveexec_b64 s[4:5], vcc
	s_cbranch_execz .LBB0_1129
.LBB0_1136:
	v_mul_f32_e32 v16, 0.5, v15
	v_mov_b32_e32 v15, v0
	v_lshlrev_b64 v[14:15], 10, v[14:15]
	v_lshl_add_u64 v[20:21], s[92:93], 0, v[14:15]
	v_pk_mul_f32 v[24:25], v[126:127], v[16:17] op_sel_hi:[1,0]
	v_pk_mul_f32 v[28:29], v[122:123], v[16:17] op_sel_hi:[1,0]
	v_cvt_pk_fp8_f32 v14, v24, v25
	v_cvt_pk_fp8_f32 v15, v28, v29
	v_pk_mul_f32 v[22:23], v[128:129], v[16:17] op_sel_hi:[1,0]
	v_pk_mul_f32 v[26:27], v[124:125], v[16:17] op_sel_hi:[1,0]
	v_cvt_pk_fp8_f32 v14, v22, v23 op_sel:[0,0,1]
	v_cvt_pk_fp8_f32 v15, v26, v27 op_sel:[0,0,1]
	v_pk_mul_f32 v[22:23], v[120:121], v[16:17] op_sel_hi:[1,0]
	v_pk_mul_f32 v[24:25], v[118:119], v[16:17] op_sel_hi:[1,0]
	v_pk_mul_f32 v[26:27], v[116:117], v[16:17] op_sel_hi:[1,0]
	v_pk_mul_f32 v[28:29], v[114:115], v[16:17] op_sel_hi:[1,0]
	v_cvt_pk_fp8_f32 v16, v24, v25
	v_cvt_pk_fp8_f32 v17, v28, v29
	v_lshl_add_u64 v[20:21], v[20:21], 0, v[2:3]
	v_lshl_add_u64 v[20:21], v[20:21], 0, v[170:171]
	v_cvt_pk_fp8_f32 v16, v22, v23 op_sel:[0,0,1]
	v_cvt_pk_fp8_f32 v17, v26, v27 op_sel:[0,0,1]
	s_nop 0
	v_permlane16_swap_b32_e32 v14, v16
	v_permlane16_swap_b32_e32 v15, v17
	global_store_dwordx4 v[20:21], v[14:17], off
	s_or_b64 exec, exec, s[4:5]
	v_cmp_lt_i32_e32 vcc, -1, v12
	s_and_saveexec_b64 s[4:5], vcc
	s_cbranch_execz .LBB0_1130
.LBB0_1137:
	v_mul_f32_e32 v14, 0.5, v13
	v_mov_b32_e32 v13, v0
	v_lshlrev_b64 v[12:13], 10, v[12:13]
	v_lshl_add_u64 v[16:17], s[92:93], 0, v[12:13]
	v_pk_mul_f32 v[22:23], v[110:111], v[14:15] op_sel_hi:[1,0]
	v_pk_mul_f32 v[26:27], v[106:107], v[14:15] op_sel_hi:[1,0]
	v_cvt_pk_fp8_f32 v12, v22, v23
	v_cvt_pk_fp8_f32 v13, v26, v27
	v_pk_mul_f32 v[20:21], v[112:113], v[14:15] op_sel_hi:[1,0]
	v_pk_mul_f32 v[24:25], v[108:109], v[14:15] op_sel_hi:[1,0]
	v_cvt_pk_fp8_f32 v12, v20, v21 op_sel:[0,0,1]
	v_cvt_pk_fp8_f32 v13, v24, v25 op_sel:[0,0,1]
	v_pk_mul_f32 v[20:21], v[104:105], v[14:15] op_sel_hi:[1,0]
	v_pk_mul_f32 v[22:23], v[102:103], v[14:15] op_sel_hi:[1,0]
	v_pk_mul_f32 v[24:25], v[100:101], v[14:15] op_sel_hi:[1,0]
	v_pk_mul_f32 v[26:27], v[98:99], v[14:15] op_sel_hi:[1,0]
	v_cvt_pk_fp8_f32 v14, v22, v23
	v_cvt_pk_fp8_f32 v15, v26, v27
	v_lshl_add_u64 v[16:17], v[16:17], 0, v[2:3]
	v_lshl_add_u64 v[16:17], v[16:17], 0, v[170:171]
	v_cvt_pk_fp8_f32 v14, v20, v21 op_sel:[0,0,1]
	v_cvt_pk_fp8_f32 v15, v24, v25 op_sel:[0,0,1]
	s_nop 0
	v_permlane16_swap_b32_e32 v12, v14
	v_permlane16_swap_b32_e32 v13, v15
	global_store_dwordx4 v[16:17], v[12:15], off
	s_or_b64 exec, exec, s[4:5]
	v_cmp_lt_i32_e32 vcc, -1, v10
	s_and_saveexec_b64 s[4:5], vcc
	s_cbranch_execz .LBB0_1131
.LBB0_1138:
	v_mul_f32_e32 v12, 0.5, v11
	v_mov_b32_e32 v11, v0
	v_lshlrev_b64 v[10:11], 10, v[10:11]
	v_lshl_add_u64 v[14:15], s[92:93], 0, v[10:11]
	v_pk_mul_f32 v[20:21], v[94:95], v[12:13] op_sel_hi:[1,0]
	v_pk_mul_f32 v[24:25], v[90:91], v[12:13] op_sel_hi:[1,0]
	v_cvt_pk_fp8_f32 v10, v20, v21
	v_cvt_pk_fp8_f32 v11, v24, v25
	v_pk_mul_f32 v[16:17], v[96:97], v[12:13] op_sel_hi:[1,0]
	v_pk_mul_f32 v[22:23], v[92:93], v[12:13] op_sel_hi:[1,0]
	v_cvt_pk_fp8_f32 v10, v16, v17 op_sel:[0,0,1]
	v_cvt_pk_fp8_f32 v11, v22, v23 op_sel:[0,0,1]
	v_pk_mul_f32 v[16:17], v[88:89], v[12:13] op_sel_hi:[1,0]
	v_pk_mul_f32 v[20:21], v[86:87], v[12:13] op_sel_hi:[1,0]
	v_pk_mul_f32 v[22:23], v[84:85], v[12:13] op_sel_hi:[1,0]
	v_pk_mul_f32 v[24:25], v[82:83], v[12:13] op_sel_hi:[1,0]
	v_cvt_pk_fp8_f32 v12, v20, v21
	v_cvt_pk_fp8_f32 v13, v24, v25
	v_lshl_add_u64 v[14:15], v[14:15], 0, v[2:3]
	v_lshl_add_u64 v[14:15], v[14:15], 0, v[170:171]
	v_cvt_pk_fp8_f32 v12, v16, v17 op_sel:[0,0,1]
	v_cvt_pk_fp8_f32 v13, v22, v23 op_sel:[0,0,1]
	s_nop 0
	v_permlane16_swap_b32_e32 v10, v12
	v_permlane16_swap_b32_e32 v11, v13
	global_store_dwordx4 v[14:15], v[10:13], off
	s_or_b64 exec, exec, s[4:5]
	v_cmp_lt_i32_e32 vcc, -1, v8
	s_and_saveexec_b64 s[4:5], vcc
	s_cbranch_execz .LBB0_1132
.LBB0_1139:
	v_mul_f32_e32 v10, 0.5, v9
	v_mov_b32_e32 v9, v0
	v_lshlrev_b64 v[8:9], 10, v[8:9]
	v_lshl_add_u64 v[12:13], s[92:93], 0, v[8:9]
	v_pk_mul_f32 v[16:17], v[78:79], v[10:11] op_sel_hi:[1,0]
	v_pk_mul_f32 v[22:23], v[74:75], v[10:11] op_sel_hi:[1,0]
	v_cvt_pk_fp8_f32 v8, v16, v17
	v_cvt_pk_fp8_f32 v9, v22, v23
	v_pk_mul_f32 v[14:15], v[80:81], v[10:11] op_sel_hi:[1,0]
	v_pk_mul_f32 v[20:21], v[76:77], v[10:11] op_sel_hi:[1,0]
	v_cvt_pk_fp8_f32 v8, v14, v15 op_sel:[0,0,1]
	v_cvt_pk_fp8_f32 v9, v20, v21 op_sel:[0,0,1]
	v_pk_mul_f32 v[14:15], v[72:73], v[10:11] op_sel_hi:[1,0]
	v_pk_mul_f32 v[16:17], v[70:71], v[10:11] op_sel_hi:[1,0]
	v_pk_mul_f32 v[20:21], v[60:61], v[10:11] op_sel_hi:[1,0]
	v_pk_mul_f32 v[22:23], v[58:59], v[10:11] op_sel_hi:[1,0]
	v_cvt_pk_fp8_f32 v10, v16, v17
	v_cvt_pk_fp8_f32 v11, v22, v23
	v_lshl_add_u64 v[12:13], v[12:13], 0, v[2:3]
	v_lshl_add_u64 v[12:13], v[12:13], 0, v[170:171]
	v_cvt_pk_fp8_f32 v10, v14, v15 op_sel:[0,0,1]
	v_cvt_pk_fp8_f32 v11, v20, v21 op_sel:[0,0,1]
	s_nop 0
	v_permlane16_swap_b32_e32 v8, v10
	v_permlane16_swap_b32_e32 v9, v11
	global_store_dwordx4 v[12:13], v[8:11], off
	s_or_b64 exec, exec, s[4:5]
	v_cmp_lt_i32_e32 vcc, -1, v6
	s_and_saveexec_b64 s[4:5], vcc
	s_cbranch_execz .LBB0_1133
.LBB0_1140:
	v_mov_b32_e32 v7, v0
	v_mul_f32_e32 v8, 0.5, v19
	v_lshlrev_b64 v[6:7], 10, v[6:7]
	v_lshl_add_u64 v[10:11], s[92:93], 0, v[6:7]
	v_pk_mul_f32 v[14:15], v[54:55], v[8:9] op_sel_hi:[1,0]
	v_pk_mul_f32 v[20:21], v[50:51], v[8:9] op_sel_hi:[1,0]
	v_cvt_pk_fp8_f32 v6, v14, v15
	v_cvt_pk_fp8_f32 v7, v20, v21
	v_pk_mul_f32 v[12:13], v[56:57], v[8:9] op_sel_hi:[1,0]
	v_pk_mul_f32 v[16:17], v[52:53], v[8:9] op_sel_hi:[1,0]
	v_cvt_pk_fp8_f32 v6, v12, v13 op_sel:[0,0,1]
	v_cvt_pk_fp8_f32 v7, v16, v17 op_sel:[0,0,1]
	v_pk_mul_f32 v[12:13], v[68:69], v[8:9] op_sel_hi:[1,0]
	v_pk_mul_f32 v[14:15], v[66:67], v[8:9] op_sel_hi:[1,0]
	v_pk_mul_f32 v[16:17], v[64:65], v[8:9] op_sel_hi:[1,0]
	v_pk_mul_f32 v[20:21], v[62:63], v[8:9] op_sel_hi:[1,0]
	v_cvt_pk_fp8_f32 v8, v14, v15
	v_cvt_pk_fp8_f32 v9, v20, v21
	v_lshl_add_u64 v[10:11], v[10:11], 0, v[2:3]
	v_lshl_add_u64 v[10:11], v[10:11], 0, v[170:171]
	v_cvt_pk_fp8_f32 v8, v12, v13 op_sel:[0,0,1]
	v_cvt_pk_fp8_f32 v9, v16, v17 op_sel:[0,0,1]
	s_nop 0
	v_permlane16_swap_b32_e32 v6, v8
	v_permlane16_swap_b32_e32 v7, v9
	global_store_dwordx4 v[10:11], v[6:9], off
	s_or_b64 exec, exec, s[4:5]
	v_cmp_lt_i32_e32 vcc, -1, v4
	s_and_saveexec_b64 s[4:5], vcc
	s_cbranch_execz .LBB0_1134
.LBB0_1141:
	v_mov_b32_e32 v5, v0
	v_mul_f32_e32 v6, 0.5, v18
	v_lshlrev_b64 v[4:5], 10, v[4:5]
	v_lshl_add_u64 v[8:9], s[92:93], 0, v[4:5]
	v_pk_mul_f32 v[12:13], v[38:39], v[6:7] op_sel_hi:[1,0]
	v_pk_mul_f32 v[16:17], v[34:35], v[6:7] op_sel_hi:[1,0]
	v_cvt_pk_fp8_f32 v4, v12, v13
	v_cvt_pk_fp8_f32 v5, v16, v17
	v_pk_mul_f32 v[10:11], v[40:41], v[6:7] op_sel_hi:[1,0]
	v_pk_mul_f32 v[14:15], v[36:37], v[6:7] op_sel_hi:[1,0]
	v_cvt_pk_fp8_f32 v4, v10, v11 op_sel:[0,0,1]
	v_cvt_pk_fp8_f32 v5, v14, v15 op_sel:[0,0,1]
	v_pk_mul_f32 v[10:11], v[48:49], v[6:7] op_sel_hi:[1,0]
	v_pk_mul_f32 v[12:13], v[46:47], v[6:7] op_sel_hi:[1,0]
	v_pk_mul_f32 v[14:15], v[44:45], v[6:7] op_sel_hi:[1,0]
	v_pk_mul_f32 v[16:17], v[42:43], v[6:7] op_sel_hi:[1,0]
	v_cvt_pk_fp8_f32 v6, v12, v13
	v_cvt_pk_fp8_f32 v7, v16, v17
	v_lshl_add_u64 v[2:3], v[8:9], 0, v[2:3]
	v_lshl_add_u64 v[2:3], v[2:3], 0, v[170:171]
	v_cvt_pk_fp8_f32 v6, v10, v11 op_sel:[0,0,1]
	v_cvt_pk_fp8_f32 v7, v14, v15 op_sel:[0,0,1]
	s_nop 0
	v_permlane16_swap_b32_e32 v4, v6
	v_permlane16_swap_b32_e32 v5, v7
	global_store_dwordx4 v[2:3], v[4:7], off
	s_or_b64 exec, exec, s[4:5]
	s_and_b64 vcc, exec, s[0:1]
	s_mov_b64 s[0:1], -1
	s_cbranch_vccnz .LBB0_1096
